# phase-output stores of P1 P2 P5 P6 P7 P9 P10 made write-through (sc1) to shorten the grid barriers' release write-back
# speedup vs baseline: 1.0012x; 1.0012x over previous
; __device__ __forceinline__ void p1_norm(Frame& F) {
;     ...
;     for (int idx = F.bx * NTHR + F.tid; idx < 5 * NMOD; idx += F.G * NTHR)
;         mod[idx] = ((modp[idx] + modp[5 * NMOD + idx]) + (modp[2 * 5 * NMOD + idx] + modp[3 * 5 * NMOD + idx])) + IN_BMOD[idx % NMOD];
.LBB0_229:
	v_add_co_u32_e32 v8, vcc, 0x3c000, v4
	v_mul_hi_i32 v3, v2, s3
	s_nop 0
	v_addc_co_u32_e32 v9, vcc, 0, v5, vcc
	v_add_co_u32_e32 v10, vcc, 0x78000, v4
	v_lshrrev_b32_e32 v7, 31, v3
	v_ashrrev_i32_e32 v3, 11, v3
	v_addc_co_u32_e32 v11, vcc, 0, v5, vcc
	v_add_u32_e32 v3, v3, v7
	v_add_co_u32_e32 v12, vcc, 0xb4000, v4
	v_mul_i32_i24_e32 v3, 0x3000, v3
	global_load_dword v6, v[4:5], off
	v_addc_co_u32_e32 v13, vcc, 0, v5, vcc
	global_load_dword v8, v[8:9], off
	s_nop 0
	global_load_dword v7, v[10:11], off
	global_load_dword v9, v[12:13], off
	v_sub_u32_e32 v10, v2, v3
	v_ashrrev_i32_e32 v11, 31, v10
	v_lshl_add_u64 v[10:11], v[10:11], 2, s[14:15]
	global_load_dword v3, v[10:11], off
	v_add_co_u32_e32 v10, vcc, 0x70e00000, v4
	v_add_u32_e32 v2, s2, v2
	s_nop 0
	v_addc_co_u32_e32 v11, vcc, -1, v5, vcc
	v_cmp_lt_i32_e32 vcc, s8, v2
	v_lshl_add_u64 v[4:5], v[4:5], 0, s[4:5]
	s_or_b64 s[6:7], vcc, s[6:7]
	s_waitcnt vmcnt(1)
	v_pk_add_f32 v[6:7], v[6:7], v[8:9]
	s_nop 0
	v_add_f32_e32 v6, v6, v7
	s_waitcnt vmcnt(0)
	v_add_f32_e32 v3, v3, v6
	global_store_dword v[10:11], v3, off sc1
	s_andn2_b64 exec, exec, s[6:7]
	s_cbranch_execnz .LBB0_229

; __device__ __forceinline__ void p1_norm(Frame& F) {
;     ...
;         const int row = rb + F.wave;
;         const int bw = row < M_LAT ? row / T : 4;
;         if (row < r1 && bw == b0) {
;             const float* xr = row < M_LAT ? IN_X + (size_t)row * D : IN_CTX + (size_t)(row - M_LAT) * D;
;             f32x4 v[8]; float ss = 0.f;
; #pragma unroll
;             for (int j = 0; j < 8; ++j) { v[j] = *(const f32x4*)(xr + 4 * F.lane + 256 * j); ss += (v[j].x * v[j].x + v[j].y * v[j].y) + (v[j].z * v[j].z + v[j].w * v[j].w); }
;             const float rstd = __builtin_amdgcn_rsqf(wave_sum(ss) * (1.0f / D) + RMS_EPS);
.LBB0_232:
	global_load_dwordx4 v[18:21], v6, s[2:3]
	global_load_dwordx4 v[22:25], v6, s[2:3] offset:1024
	global_load_dwordx4 v[26:29], v6, s[2:3] offset:2048
	global_load_dwordx4 v[30:33], v6, s[2:3] offset:3072
	v_lshl_add_u64 v[2:3], s[2:3], 0, v[6:7]
	v_add_co_u32_e32 v42, vcc, s20, v2
	s_waitcnt vmcnt(3)
	v_mov_b32_e32 v48, v19
	v_addc_co_u32_e32 v43, vcc, 0, v3, vcc
	global_load_dwordx4 v[34:37], v[42:43], off
	global_load_dwordx4 v[38:41], v[42:43], off offset:1024
	global_load_dwordx4 v[2:5], v[42:43], off offset:3072
	s_nop 0
	global_load_dwordx4 v[42:45], v[42:43], off offset:2048
	s_waitcnt vmcnt(6)
	v_mov_b32_e32 v49, v23
	v_mov_b32_e32 v52, v21
	v_mov_b32_e32 v53, v25
	v_mov_b32_e32 v46, v18
	v_mov_b32_e32 v47, v22
	v_mov_b32_e32 v50, v20
	v_mov_b32_e32 v51, v24
	s_waitcnt vmcnt(5)
	v_pk_mul_f32 v[54:55], v[28:29], v[28:29]
	v_pk_mul_f32 v[56:57], v[26:27], v[26:27]
	v_pk_mul_f32 v[48:49], v[48:49], v[48:49]
	v_pk_mul_f32 v[52:53], v[52:53], v[52:53]
	v_pk_mov_b32 v[62:63], v[56:57], v[54:55] op_sel:[1,0]
	v_mov_b32_e32 v57, v55
	v_pk_fma_f32 v[46:47], v[46:47], v[46:47], v[48:49]
	v_pk_fma_f32 v[48:49], v[50:51], v[50:51], v[52:53]
	s_waitcnt vmcnt(4)
	v_mul_f32_e32 v58, v31, v31
	v_mul_f32_e32 v60, v33, v33
	v_pk_add_f32 v[50:51], v[62:63], v[56:57]
	v_pk_add_f32 v[46:47], v[46:47], v[48:49]
	v_pk_fma_f32 v[54:55], v[30:31], v[30:31], v[58:59] op_sel_hi:[1,1,0]
	v_pk_fma_f32 v[58:59], v[32:33], v[32:33], v[60:61] op_sel_hi:[1,1,0]
	v_pk_add_f32 v[48:49], v[50:51], v[50:51] op_sel:[0,1] op_sel_hi:[1,0]
	v_pk_add_f32 v[46:47], v[46:47], v[46:47] op_sel:[0,1] op_sel_hi:[1,0]
	s_waitcnt vmcnt(3)
	v_mul_f32_e32 v63, v34, v34
	v_mul_f32_e32 v64, v35, v35
	v_mul_f32_e32 v55, v36, v36
	v_mul_f32_e32 v59, v37, v37
	s_waitcnt vmcnt(2)
	v_pk_mul_f32 v[52:53], v[40:41], v[40:41]
	v_pk_mul_f32 v[56:57], v[38:39], v[38:39]
	v_mov_b32_e32 v49, v64
	v_mov_b32_e32 v47, v63
	v_pk_mov_b32 v[50:51], v[56:57], v[52:53] op_sel:[1,0]
	v_mov_b32_e32 v57, v53
	v_pk_add_f32 v[54:55], v[54:55], v[58:59]
	v_pk_add_f32 v[46:47], v[46:47], v[48:49]
	s_waitcnt vmcnt(0)
	v_mul_f32_e32 v60, v43, v43
	v_mul_f32_e32 v62, v45, v45
	v_pk_add_f32 v[50:51], v[50:51], v[56:57]
	v_pk_add_f32 v[46:47], v[46:47], v[54:55]
	v_mul_f32_e32 v65, v2, v2
	v_mul_f32_e32 v66, v3, v3
	v_mul_f32_e32 v67, v4, v4
	v_mul_f32_e32 v68, v5, v5
	v_pk_fma_f32 v[52:53], v[42:43], v[42:43], v[60:61] op_sel_hi:[1,1,0]
	v_pk_fma_f32 v[60:61], v[44:45], v[44:45], v[62:63] op_sel_hi:[1,1,0]
	v_pk_add_f32 v[50:51], v[50:51], v[50:51] op_sel:[0,1] op_sel_hi:[1,0]
	v_pk_add_f32 v[46:47], v[46:47], v[46:47] op_sel:[0,1] op_sel_hi:[1,0]
	v_mov_b32_e32 v53, v67
	v_mov_b32_e32 v61, v68
	v_mov_b32_e32 v51, v66
	v_mov_b32_e32 v47, v65
	v_pk_add_f32 v[52:53], v[52:53], v[60:61]
	v_pk_add_f32 v[46:47], v[46:47], v[50:51]
	s_nop 0
	v_pk_add_f32 v[46:47], v[46:47], v[52:53]
	s_nop 0
	v_add_f32_e32 v46, v46, v47
	s_nop 1
	v_add_f32_dpp v46, v46, v46 quad_perm:[1,0,3,2] row_mask:0xf bank_mask:0xf bound_ctrl:1
	s_nop 1
	v_add_f32_dpp v46, v46, v46 quad_perm:[2,3,0,1] row_mask:0xf bank_mask:0xf bound_ctrl:1
	s_nop 1
	v_add_f32_dpp v46, v46, v46 row_ror:4 row_mask:0xf bank_mask:0xf bound_ctrl:1
	s_nop 1
	v_add_f32_dpp v46, v46, v46 row_ror:8 row_mask:0xf bank_mask:0xf bound_ctrl:1
	s_nop 0
	v_readlane_b32 s0, v46, 16
	v_readlane_b32 s6, v46, 48
	v_readlane_b32 s2, v46, 0
	v_readlane_b32 s3, v46, 32
	v_mov_b32_e32 v46, s0
	v_mov_b32_e32 v47, s6
	v_pk_add_f32 v[46:47], s[2:3], v[46:47]
	s_lshl_b64 s[2:3], s[8:9], 12
	v_add_f32_e32 v46, v46, v47
	v_fmamk_f32 v46, v46, 0x3a000000, v17
	v_rsq_f32_e32 v54, v46
	ds_read_b128 v[46:49], v14
	ds_read_b128 v[50:53], v14 offset:8192
	s_mov_b32 s0, s21
	v_pk_mul_f32 v[18:19], v[18:19], v[54:55] op_sel_hi:[1,0]
	v_pk_mul_f32 v[20:21], v[20:21], v[54:55] op_sel_hi:[1,0]
	s_waitcnt lgkmcnt(0)
; #define LAS __attribute__((address_space(3)))
; __device__ __forceinline__ unsigned cvt_pk_bf16(float lo, float hi) { unsigned r; asm volatile("v_cvt_pk_bf16_f32 %0, %1, %2" : "=v"(r) : "v"(lo), "v"(hi)); return r; }
; __device__ __forceinline__ void p1_norm(Frame& F) {
;     ...
; #pragma unroll
;             for (int j = 0; j < 8; ++j) { const int c = 4 * F.lane + 256 * j;
;                 const f32x4 o = (v[j] * rstd) * *(const LAS f32x4*)(gs + c) + *(const LAS f32x4*)(sh + c);
;                 u32x2 w; w.x = pg8::cvt_pk_bf16(o.x, o.y); w.y = pg8::cvt_pk_bf16(o.z, o.w);
;                 *(u32x2*)(H + (size_t)row * D + c) = w; }
	v_pk_fma_f32 v[18:19], v[46:47], v[18:19], v[50:51]
	v_pk_fma_f32 v[20:21], v[48:49], v[20:21], v[52:53]
	v_cvt_pk_bf16_f32 v50, v18, v19
	v_pk_mul_f32 v[22:23], v[22:23], v[54:55] op_sel_hi:[1,0]
	v_cvt_pk_bf16_f32 v51, v20, v21
	ds_read_b128 v[18:21], v14 offset:1024
	ds_read_b128 v[46:49], v14 offset:9216
	v_pk_mul_f32 v[24:25], v[24:25], v[54:55] op_sel_hi:[1,0]
	v_lshl_add_u64 v[52:53], v[8:9], 0, s[2:3]
	global_store_dwordx2 v[52:53], v[50:51], off sc1
	v_pk_mul_f32 v[26:27], v[26:27], v[54:55] op_sel_hi:[1,0]
	s_waitcnt lgkmcnt(0)
	v_pk_fma_f32 v[20:21], v[20:21], v[24:25], v[48:49]
	v_pk_fma_f32 v[18:19], v[18:19], v[22:23], v[46:47]
	v_pk_mul_f32 v[28:29], v[28:29], v[54:55] op_sel_hi:[1,0]
	v_cvt_pk_bf16_f32 v46, v18, v19
	v_cvt_pk_bf16_f32 v47, v20, v21
	ds_read_b128 v[18:21], v14 offset:2048
	ds_read_b128 v[22:25], v14 offset:10240
	global_store_dwordx2 v[52:53], v[46:47], off offset:512 sc1
	v_pk_mul_f32 v[2:3], v[2:3], v[54:55] op_sel_hi:[1,0]
	v_pk_mul_f32 v[4:5], v[4:5], v[54:55] op_sel_hi:[1,0]
	s_waitcnt lgkmcnt(0)
	v_pk_fma_f32 v[20:21], v[28:29], v[20:21], v[24:25]
	v_pk_fma_f32 v[18:19], v[26:27], v[18:19], v[22:23]
	v_pk_mul_f32 v[28:29], v[30:31], v[54:55] op_sel_hi:[1,0]
	v_cvt_pk_bf16_f32 v26, v18, v19
	v_cvt_pk_bf16_f32 v27, v20, v21
	ds_read_b128 v[18:21], v14 offset:3072
	ds_read_b128 v[22:25], v14 offset:11264
	v_pk_mul_f32 v[30:31], v[32:33], v[54:55] op_sel_hi:[1,0]
	global_store_dwordx2 v[52:53], v[26:27], off offset:1024 sc1
	s_waitcnt lgkmcnt(0)
	v_pk_fma_f32 v[20:21], v[30:31], v[20:21], v[24:25]
	v_pk_fma_f32 v[18:19], v[28:29], v[18:19], v[22:23]
	v_pk_mul_f32 v[28:29], v[34:35], v[54:55] op_sel_hi:[1,0]
	v_cvt_pk_bf16_f32 v26, v18, v19
	v_cvt_pk_bf16_f32 v27, v20, v21
	ds_read_b128 v[18:21], v14 offset:4096
	ds_read_b128 v[22:25], v14 offset:12288
	v_pk_mul_f32 v[30:31], v[36:37], v[54:55] op_sel_hi:[1,0]
	global_store_dwordx2 v[52:53], v[26:27], off offset:1536 sc1
	s_waitcnt lgkmcnt(0)
	v_pk_fma_f32 v[20:21], v[30:31], v[20:21], v[24:25]
	v_pk_fma_f32 v[18:19], v[28:29], v[18:19], v[22:23]
	v_pk_mul_f32 v[28:29], v[38:39], v[54:55] op_sel_hi:[1,0]
	v_cvt_pk_bf16_f32 v26, v18, v19
	v_cvt_pk_bf16_f32 v27, v20, v21
	ds_read_b128 v[18:21], v14 offset:5120
	ds_read_b128 v[22:25], v14 offset:13312
	v_pk_mul_f32 v[30:31], v[40:41], v[54:55] op_sel_hi:[1,0]
	global_store_dwordx2 v[52:53], v[26:27], off offset:2048 sc1
	s_waitcnt lgkmcnt(0)
	v_pk_fma_f32 v[20:21], v[30:31], v[20:21], v[24:25]
	v_pk_fma_f32 v[18:19], v[28:29], v[18:19], v[22:23]
	v_pk_mul_f32 v[28:29], v[44:45], v[54:55] op_sel_hi:[1,0]
	v_cvt_pk_bf16_f32 v26, v18, v19
	v_cvt_pk_bf16_f32 v27, v20, v21
	ds_read_b128 v[18:21], v14 offset:6144
	ds_read_b128 v[22:25], v14 offset:14336
	global_store_dwordx2 v[52:53], v[26:27], off offset:2560 sc1
	v_pk_mul_f32 v[26:27], v[42:43], v[54:55] op_sel_hi:[1,0]
	s_waitcnt lgkmcnt(0)
	v_pk_fma_f32 v[20:21], v[28:29], v[20:21], v[24:25]
	v_pk_fma_f32 v[18:19], v[26:27], v[18:19], v[22:23]
	s_nop 0
	v_cvt_pk_bf16_f32 v26, v18, v19
	v_cvt_pk_bf16_f32 v27, v20, v21
	ds_read_b128 v[18:21], v14 offset:7168
	ds_read_b128 v[22:25], v14 offset:15360
	global_store_dwordx2 v[52:53], v[26:27], off offset:3072 sc1
	s_waitcnt lgkmcnt(0)
	v_pk_fma_f32 v[2:3], v[2:3], v[18:19], v[22:23]
	v_pk_fma_f32 v[4:5], v[4:5], v[20:21], v[24:25]
	v_cvt_pk_bf16_f32 v2, v2, v3
	s_nop 0
	v_cvt_pk_bf16_f32 v3, v4, v5
	global_store_dwordx2 v[52:53], v[2:3], off offset:3584 sc1

; __device__ __forceinline__ void p1_norm(Frame& F) {
;     ...
;                 if (row < r1 && bw == bl) {
;                     const float* xr = row < M_LAT ? IN_X + (size_t)row * D : IN_CTX + (size_t)(row - M_LAT) * D;
;                     f32x4 v[8]; float ss = 0.f;
; #pragma unroll
;                     for (int j = 0; j < 8; ++j) { v[j] = *(const f32x4*)(xr + 4 * F.lane + 256 * j); ss += (v[j].x * v[j].x + v[j].y * v[j].y) + (v[j].z * v[j].z + v[j].w * v[j].w); }
;                     const float rstd = __builtin_amdgcn_rsqf(wave_sum(ss) * (1.0f / D) + RMS_EPS);
.LBB0_244:
	global_load_dwordx4 v[18:21], v6, s[2:3]
	global_load_dwordx4 v[22:25], v6, s[2:3] offset:1024
	global_load_dwordx4 v[26:29], v6, s[2:3] offset:2048
	global_load_dwordx4 v[30:33], v6, s[2:3] offset:3072
	v_lshl_add_u64 v[2:3], s[2:3], 0, v[6:7]
	v_add_co_u32_e32 v42, vcc, s20, v2
	s_waitcnt vmcnt(3)
	v_mov_b32_e32 v48, v19
	v_addc_co_u32_e32 v43, vcc, 0, v3, vcc
	global_load_dwordx4 v[34:37], v[42:43], off
	global_load_dwordx4 v[38:41], v[42:43], off offset:1024
	global_load_dwordx4 v[2:5], v[42:43], off offset:3072
	s_nop 0
	global_load_dwordx4 v[42:45], v[42:43], off offset:2048
	s_waitcnt vmcnt(6)
	v_mov_b32_e32 v49, v23
	v_mov_b32_e32 v52, v21
	v_mov_b32_e32 v53, v25
	v_mov_b32_e32 v46, v18
	v_mov_b32_e32 v47, v22
	v_mov_b32_e32 v50, v20
	v_mov_b32_e32 v51, v24
	s_waitcnt vmcnt(5)
	v_pk_mul_f32 v[54:55], v[28:29], v[28:29]
	v_pk_mul_f32 v[56:57], v[26:27], v[26:27]
	v_pk_mul_f32 v[48:49], v[48:49], v[48:49]
	v_pk_mul_f32 v[52:53], v[52:53], v[52:53]
	v_pk_mov_b32 v[62:63], v[56:57], v[54:55] op_sel:[1,0]
	v_mov_b32_e32 v57, v55
	v_pk_fma_f32 v[46:47], v[46:47], v[46:47], v[48:49]
	v_pk_fma_f32 v[48:49], v[50:51], v[50:51], v[52:53]
	s_waitcnt vmcnt(4)
	v_mul_f32_e32 v58, v31, v31
	v_mul_f32_e32 v60, v33, v33
	v_pk_add_f32 v[50:51], v[62:63], v[56:57]
	v_pk_add_f32 v[46:47], v[46:47], v[48:49]
	v_pk_fma_f32 v[54:55], v[30:31], v[30:31], v[58:59] op_sel_hi:[1,1,0]
	v_pk_fma_f32 v[58:59], v[32:33], v[32:33], v[60:61] op_sel_hi:[1,1,0]
	v_pk_add_f32 v[48:49], v[50:51], v[50:51] op_sel:[0,1] op_sel_hi:[1,0]
	v_pk_add_f32 v[46:47], v[46:47], v[46:47] op_sel:[0,1] op_sel_hi:[1,0]
	s_waitcnt vmcnt(3)
	v_mul_f32_e32 v63, v34, v34
	v_mul_f32_e32 v64, v35, v35
	v_mul_f32_e32 v55, v36, v36
	v_mul_f32_e32 v59, v37, v37
	s_waitcnt vmcnt(2)
	v_pk_mul_f32 v[52:53], v[40:41], v[40:41]
	v_pk_mul_f32 v[56:57], v[38:39], v[38:39]
	v_mov_b32_e32 v49, v64
	v_mov_b32_e32 v47, v63
	v_pk_mov_b32 v[50:51], v[56:57], v[52:53] op_sel:[1,0]
	v_mov_b32_e32 v57, v53
	v_pk_add_f32 v[54:55], v[54:55], v[58:59]
	v_pk_add_f32 v[46:47], v[46:47], v[48:49]
	s_waitcnt vmcnt(0)
	v_mul_f32_e32 v60, v43, v43
	v_mul_f32_e32 v62, v45, v45
	v_pk_add_f32 v[50:51], v[50:51], v[56:57]
	v_pk_add_f32 v[46:47], v[46:47], v[54:55]
	v_mul_f32_e32 v65, v2, v2
	v_mul_f32_e32 v66, v3, v3
	v_mul_f32_e32 v67, v4, v4
	v_mul_f32_e32 v68, v5, v5
	v_pk_fma_f32 v[52:53], v[42:43], v[42:43], v[60:61] op_sel_hi:[1,1,0]
	v_pk_fma_f32 v[60:61], v[44:45], v[44:45], v[62:63] op_sel_hi:[1,1,0]
	v_pk_add_f32 v[50:51], v[50:51], v[50:51] op_sel:[0,1] op_sel_hi:[1,0]
	v_pk_add_f32 v[46:47], v[46:47], v[46:47] op_sel:[0,1] op_sel_hi:[1,0]
	v_mov_b32_e32 v53, v67
	v_mov_b32_e32 v61, v68
	v_mov_b32_e32 v51, v66
	v_mov_b32_e32 v47, v65
	v_pk_add_f32 v[52:53], v[52:53], v[60:61]
	v_pk_add_f32 v[46:47], v[46:47], v[50:51]
	s_nop 0
	v_pk_add_f32 v[46:47], v[46:47], v[52:53]
	s_nop 0
	v_add_f32_e32 v46, v46, v47
	s_nop 1
	v_add_f32_dpp v46, v46, v46 quad_perm:[1,0,3,2] row_mask:0xf bank_mask:0xf bound_ctrl:1
	s_nop 1
	v_add_f32_dpp v46, v46, v46 quad_perm:[2,3,0,1] row_mask:0xf bank_mask:0xf bound_ctrl:1
	s_nop 1
	v_add_f32_dpp v46, v46, v46 row_ror:4 row_mask:0xf bank_mask:0xf bound_ctrl:1
	s_nop 1
	v_add_f32_dpp v46, v46, v46 row_ror:8 row_mask:0xf bank_mask:0xf bound_ctrl:1
	s_nop 0
	v_readlane_b32 s0, v46, 16
	v_readlane_b32 s14, v46, 48
	v_readlane_b32 s2, v46, 0
	v_readlane_b32 s3, v46, 32
	v_mov_b32_e32 v46, s0
	v_mov_b32_e32 v47, s14
	v_pk_add_f32 v[46:47], s[2:3], v[46:47]
	s_lshl_b64 s[2:3], s[12:13], 12
	v_add_f32_e32 v46, v46, v47
	v_fmamk_f32 v46, v46, 0x3a000000, v17
	v_rsq_f32_e32 v54, v46
	ds_read_b128 v[46:49], v14
	ds_read_b128 v[50:53], v14 offset:8192
	v_pk_mul_f32 v[18:19], v[18:19], v[54:55] op_sel_hi:[1,0]
	v_pk_mul_f32 v[20:21], v[20:21], v[54:55] op_sel_hi:[1,0]
	s_waitcnt lgkmcnt(0)
; #define LAS __attribute__((address_space(3)))
; __device__ __forceinline__ unsigned cvt_pk_bf16(float lo, float hi) { unsigned r; asm volatile("v_cvt_pk_bf16_f32 %0, %1, %2" : "=v"(r) : "v"(lo), "v"(hi)); return r; }
; __device__ __forceinline__ void p1_norm(Frame& F) {
;     ...
; #pragma unroll
;                     for (int j = 0; j < 8; ++j) { const int c = 4 * F.lane + 256 * j;
;                         const f32x4 o = (v[j] * rstd) * *(const LAS f32x4*)(gs + c) + *(const LAS f32x4*)(sh + c);
;                         u32x2 w; w.x = pg8::cvt_pk_bf16(o.x, o.y); w.y = pg8::cvt_pk_bf16(o.z, o.w);
;                         *(u32x2*)(H + (size_t)row * D + c) = w; }
	v_pk_fma_f32 v[18:19], v[46:47], v[18:19], v[50:51]
	v_pk_fma_f32 v[20:21], v[48:49], v[20:21], v[52:53]
	v_cvt_pk_bf16_f32 v50, v18, v19
	v_pk_mul_f32 v[22:23], v[22:23], v[54:55] op_sel_hi:[1,0]
	v_cvt_pk_bf16_f32 v51, v20, v21
	ds_read_b128 v[18:21], v14 offset:1024
	ds_read_b128 v[46:49], v14 offset:9216
	v_pk_mul_f32 v[24:25], v[24:25], v[54:55] op_sel_hi:[1,0]
	v_lshl_add_u64 v[52:53], v[8:9], 0, s[2:3]
	global_store_dwordx2 v[52:53], v[50:51], off sc1
	v_pk_mul_f32 v[26:27], v[26:27], v[54:55] op_sel_hi:[1,0]
	s_waitcnt lgkmcnt(0)
	v_pk_fma_f32 v[20:21], v[20:21], v[24:25], v[48:49]
	v_pk_fma_f32 v[18:19], v[18:19], v[22:23], v[46:47]
	v_pk_mul_f32 v[28:29], v[28:29], v[54:55] op_sel_hi:[1,0]
	v_cvt_pk_bf16_f32 v46, v18, v19
	v_cvt_pk_bf16_f32 v47, v20, v21
	ds_read_b128 v[18:21], v14 offset:2048
	ds_read_b128 v[22:25], v14 offset:10240
	global_store_dwordx2 v[52:53], v[46:47], off offset:512 sc1
	v_pk_mul_f32 v[2:3], v[2:3], v[54:55] op_sel_hi:[1,0]
	v_pk_mul_f32 v[4:5], v[4:5], v[54:55] op_sel_hi:[1,0]
	s_waitcnt lgkmcnt(0)
	v_pk_fma_f32 v[20:21], v[28:29], v[20:21], v[24:25]
	v_pk_fma_f32 v[18:19], v[26:27], v[18:19], v[22:23]
	v_pk_mul_f32 v[28:29], v[30:31], v[54:55] op_sel_hi:[1,0]
	v_cvt_pk_bf16_f32 v26, v18, v19
	v_cvt_pk_bf16_f32 v27, v20, v21
	ds_read_b128 v[18:21], v14 offset:3072
	ds_read_b128 v[22:25], v14 offset:11264
	v_pk_mul_f32 v[30:31], v[32:33], v[54:55] op_sel_hi:[1,0]
	global_store_dwordx2 v[52:53], v[26:27], off offset:1024 sc1
	s_waitcnt lgkmcnt(0)
	v_pk_fma_f32 v[20:21], v[30:31], v[20:21], v[24:25]
	v_pk_fma_f32 v[18:19], v[28:29], v[18:19], v[22:23]
	v_pk_mul_f32 v[28:29], v[34:35], v[54:55] op_sel_hi:[1,0]
	v_cvt_pk_bf16_f32 v26, v18, v19
	v_cvt_pk_bf16_f32 v27, v20, v21
	ds_read_b128 v[18:21], v14 offset:4096
	ds_read_b128 v[22:25], v14 offset:12288
	v_pk_mul_f32 v[30:31], v[36:37], v[54:55] op_sel_hi:[1,0]
	global_store_dwordx2 v[52:53], v[26:27], off offset:1536 sc1
	s_waitcnt lgkmcnt(0)
	v_pk_fma_f32 v[20:21], v[30:31], v[20:21], v[24:25]
	v_pk_fma_f32 v[18:19], v[28:29], v[18:19], v[22:23]
	v_pk_mul_f32 v[28:29], v[38:39], v[54:55] op_sel_hi:[1,0]
	v_cvt_pk_bf16_f32 v26, v18, v19
	v_cvt_pk_bf16_f32 v27, v20, v21
	ds_read_b128 v[18:21], v14 offset:5120
	ds_read_b128 v[22:25], v14 offset:13312
	v_pk_mul_f32 v[30:31], v[40:41], v[54:55] op_sel_hi:[1,0]
	global_store_dwordx2 v[52:53], v[26:27], off offset:2048 sc1
	s_waitcnt lgkmcnt(0)
	v_pk_fma_f32 v[20:21], v[30:31], v[20:21], v[24:25]
	v_pk_fma_f32 v[18:19], v[28:29], v[18:19], v[22:23]
	v_pk_mul_f32 v[28:29], v[44:45], v[54:55] op_sel_hi:[1,0]
	v_cvt_pk_bf16_f32 v26, v18, v19
	v_cvt_pk_bf16_f32 v27, v20, v21
	ds_read_b128 v[18:21], v14 offset:6144
	ds_read_b128 v[22:25], v14 offset:14336
	global_store_dwordx2 v[52:53], v[26:27], off offset:2560 sc1
	v_pk_mul_f32 v[26:27], v[42:43], v[54:55] op_sel_hi:[1,0]
	s_waitcnt lgkmcnt(0)
	v_pk_fma_f32 v[20:21], v[28:29], v[20:21], v[24:25]
	v_pk_fma_f32 v[18:19], v[26:27], v[18:19], v[22:23]
	s_nop 0
	v_cvt_pk_bf16_f32 v26, v18, v19
	v_cvt_pk_bf16_f32 v27, v20, v21
	ds_read_b128 v[18:21], v14 offset:7168
	ds_read_b128 v[22:25], v14 offset:15360
	global_store_dwordx2 v[52:53], v[26:27], off offset:3072 sc1
	s_waitcnt lgkmcnt(0)
	v_pk_fma_f32 v[2:3], v[2:3], v[18:19], v[22:23]
	v_pk_fma_f32 v[4:5], v[4:5], v[20:21], v[24:25]
	v_cvt_pk_bf16_f32 v2, v2, v3
	s_nop 0
	v_cvt_pk_bf16_f32 v3, v4, v5
	global_store_dwordx2 v[52:53], v[2:3], off offset:3584 sc1

; #define LAS __attribute__((address_space(3)))
; __device__ __forceinline__ unsigned cvt_pk_bf16(float lo, float hi) { unsigned r; asm volatile("v_cvt_pk_bf16_f32 %0, %1, %2" : "=v"(r) : "v"(lo), "v"(hi)); return r; }
;     __device__ __forceinline__ void operator()(const f32x4 (&acc)[2][2][4][2], const Unit& u, int wr, int wc, int fr, int fq) const {
;     ...
;         LAS unsigned char* wp0 = stg + (16 * wr + fr) * STG_PITCH + 64 * wc + 16 * fq;
;         LAS unsigned char* wp1 = stg2 + (16 * wr + fr) * 512 + (((4 * wc + fq) ^ (fr & 7)) * 16);
;         const int rr = tid >> 4, cc = tid & 15; const LAS unsigned char* rp0 = stg + rr * STG_PITCH + cc * 16;
;         const LAS unsigned char* rp1 = stg2 + rr * 512 + ((cc ^ (rr & 7)) * 16);
;         bf16_t* gp = O + (size_t)(u.pm * BM + 64 * (rr >> 4) + (rr & 15)) * ldc + pnl * BM + cc * 8;
; #pragma unroll
;         for (int ai = 0; ai < 2; ++ai)
; #pragma unroll
;             for (int mp = 0; mp < 2; ++mp) {
; #pragma unroll
;                 for (int s = 0; s < 2; ++s)
; #pragma unroll
;                     for (int bj = 0; bj < 2; ++bj) { const int m = 2 * mp + s; const f32x4 v0 = acc[ai][bj][m][0] * scale + bv[bj][0], v1 = acc[ai][bj][m][1] * scale + bv[bj][1];
;                         u32x4 w; w.x = cvt_pk_bf16(v0[0], v0[1]); w.y = cvt_pk_bf16(v0[2], v0[3]); w.z = cvt_pk_bf16(v1[0], v1[1]); w.w = cvt_pk_bf16(v1[2], v1[3]);
;                         *(LAS u32x4*)((s ? wp1 : wp0) + 256 * bj) = w; }
;                 asm volatile("s_waitcnt lgkmcnt(0)" ::: "memory"); __builtin_amdgcn_s_barrier(); asm volatile("" ::: "memory");
;                 bf16_t* g2 = gp + (size_t)(ai * HALF + mp * 32) * ldc;
;                 *(u32x4*)(g2) = *(const LAS u32x4*)(rp0); *(u32x4*)(g2 + HALF) = *(const LAS u32x4*)(rp0 + 256);
;                 *(u32x4*)(g2 + (size_t)16 * ldc) = *(const LAS u32x4*)(rp1); *(u32x4*)(g2 + (size_t)16 * ldc + HALF) = *(const LAS u32x4*)(rp1 + 256);
;                 asm volatile("s_waitcnt lgkmcnt(0)" ::: "memory"); __builtin_amdgcn_s_barrier(); asm volatile("" ::: "memory");
.LBB0_329:
	s_ashr_i32 s2, s19, 31
	s_lshr_b32 s2, s2, 12
	s_add_i32 s2, s19, s2
	s_and_b32 s2, s2, 0xf00000
	v_lshl_or_b32 v146, s18, 8, v150
	v_mov_b64_e32 v[144:145], s[4:5]
	s_movk_i32 s3, 0x3480
	s_sub_i32 s2, s19, s2
	v_mad_i64_i32 v[144:145], s[18:19], v146, s3, v[144:145]
	v_pk_add_f32 v[128:129], v[128:129], 0 op_sel_hi:[1,0]
	v_pk_add_f32 v[126:127], v[126:127], 0 op_sel_hi:[1,0]
	v_pk_add_f32 v[146:147], v[124:125], 0 op_sel_hi:[1,0]
	v_pk_add_f32 v[124:125], v[122:123], 0 op_sel_hi:[1,0]
	v_cvt_pk_bf16_f32 v122, v126, v127
	v_cvt_pk_bf16_f32 v123, v128, v129
	v_pk_add_f32 v[120:121], v[120:121], 0 op_sel_hi:[1,0]
	v_cvt_pk_bf16_f32 v124, v124, v125
	v_cvt_pk_bf16_f32 v125, v146, v147
	ds_write_b128 v151, v[122:125]
	v_pk_add_f32 v[122:123], v[112:113], 0 op_sel_hi:[1,0]
	v_pk_add_f32 v[112:113], v[110:111], 0 op_sel_hi:[1,0]
	v_pk_add_f32 v[118:119], v[118:119], 0 op_sel_hi:[1,0]
	v_pk_add_f32 v[104:105], v[104:105], 0 op_sel_hi:[1,0]
	v_cvt_pk_bf16_f32 v110, v118, v119
	v_cvt_pk_bf16_f32 v111, v120, v121
	v_cvt_pk_bf16_f32 v112, v112, v113
	v_cvt_pk_bf16_f32 v113, v122, v123
	ds_write_b128 v151, v[110:113] offset:256
	v_pk_add_f32 v[110:111], v[116:117], 0 op_sel_hi:[1,0]
	v_pk_add_f32 v[112:113], v[114:115], 0 op_sel_hi:[1,0]
	v_pk_add_f32 v[114:115], v[108:109], 0 op_sel_hi:[1,0]
	v_pk_add_f32 v[108:109], v[106:107], 0 op_sel_hi:[1,0]
	v_cvt_pk_bf16_f32 v106, v112, v113
	v_cvt_pk_bf16_f32 v107, v110, v111
	v_pk_add_f32 v[102:103], v[102:103], 0 op_sel_hi:[1,0]
	v_cvt_pk_bf16_f32 v108, v108, v109
	v_cvt_pk_bf16_f32 v109, v114, v115
	ds_write_b128 v152, v[106:109] offset:49152
	v_pk_add_f32 v[106:107], v[100:101], 0 op_sel_hi:[1,0]
	v_pk_add_f32 v[100:101], v[98:99], 0 op_sel_hi:[1,0]
	v_cvt_pk_bf16_f32 v98, v102, v103
	v_cvt_pk_bf16_f32 v99, v104, v105
	s_lshl_b32 s2, s2, 8
	v_cvt_pk_bf16_f32 v100, v100, v101
	v_cvt_pk_bf16_f32 v101, v106, v107
	ds_write_b128 v152, v[98:101] offset:49408
	s_waitcnt lgkmcnt(0)
	s_barrier
	ds_read_b128 v[100:103], v153
	ds_read_b128 v[104:107], v153 offset:256
	s_ashr_i32 s3, s2, 31
	v_lshl_add_u64 v[98:99], s[2:3], 1, v[144:145]
	v_lshl_add_u64 v[98:99], v[98:99], 0, v[138:139]
	s_waitcnt lgkmcnt(0)
	global_store_dwordx4 v[98:99], v[100:103], off sc1
	global_store_dwordx4 v[98:99], v[104:107], off offset:256 sc1
	ds_read_b128 v[100:103], v154 offset:49152
	ds_read_b128 v[104:107], v154 offset:49408
	s_mov_b32 s2, 0x34000
	v_add_co_u32_e32 v108, vcc, s2, v98
	v_pk_add_f32 v[96:97], v[96:97], 0 op_sel_hi:[1,0]
	s_nop 0
	v_addc_co_u32_e32 v109, vcc, 0, v99, vcc
	s_waitcnt lgkmcnt(0)
	global_store_dwordx4 v[108:109], v[100:103], off offset:2048 sc1
	global_store_dwordx4 v[108:109], v[104:107], off offset:2304 sc1
	s_waitcnt lgkmcnt(0)
	s_barrier
	v_pk_add_f32 v[94:95], v[94:95], 0 op_sel_hi:[1,0]
	v_pk_add_f32 v[100:101], v[92:93], 0 op_sel_hi:[1,0]
	v_pk_add_f32 v[92:93], v[90:91], 0 op_sel_hi:[1,0]
	v_cvt_pk_bf16_f32 v90, v94, v95
	v_cvt_pk_bf16_f32 v91, v96, v97
	v_pk_add_f32 v[88:89], v[88:89], 0 op_sel_hi:[1,0]
	v_cvt_pk_bf16_f32 v92, v92, v93
	v_cvt_pk_bf16_f32 v93, v100, v101
	ds_write_b128 v151, v[90:93]
	v_pk_add_f32 v[90:91], v[80:81], 0 op_sel_hi:[1,0]
	v_pk_add_f32 v[80:81], v[78:79], 0 op_sel_hi:[1,0]
	v_pk_add_f32 v[86:87], v[86:87], 0 op_sel_hi:[1,0]
	v_pk_add_f32 v[72:73], v[72:73], 0 op_sel_hi:[1,0]
	v_cvt_pk_bf16_f32 v78, v86, v87
	v_cvt_pk_bf16_f32 v79, v88, v89
	v_cvt_pk_bf16_f32 v80, v80, v81
	v_cvt_pk_bf16_f32 v81, v90, v91
	ds_write_b128 v151, v[78:81] offset:256
	v_pk_add_f32 v[78:79], v[84:85], 0 op_sel_hi:[1,0]
	v_pk_add_f32 v[80:81], v[82:83], 0 op_sel_hi:[1,0]
	v_pk_add_f32 v[82:83], v[76:77], 0 op_sel_hi:[1,0]
	v_pk_add_f32 v[76:77], v[74:75], 0 op_sel_hi:[1,0]
	v_cvt_pk_bf16_f32 v74, v80, v81
	v_cvt_pk_bf16_f32 v75, v78, v79
	v_pk_add_f32 v[70:71], v[70:71], 0 op_sel_hi:[1,0]
	v_cvt_pk_bf16_f32 v76, v76, v77
	v_cvt_pk_bf16_f32 v77, v82, v83
	ds_write_b128 v152, v[74:77] offset:49152
	v_pk_add_f32 v[74:75], v[68:69], 0 op_sel_hi:[1,0]
	v_pk_add_f32 v[68:69], v[66:67], 0 op_sel_hi:[1,0]
	v_cvt_pk_bf16_f32 v66, v70, v71
	v_cvt_pk_bf16_f32 v67, v72, v73
	s_mov_b32 s2, 0x69000
	v_cvt_pk_bf16_f32 v68, v68, v69
	v_cvt_pk_bf16_f32 v69, v74, v75
	ds_write_b128 v152, v[66:69] offset:49408
	s_waitcnt lgkmcnt(0)
	s_barrier
	ds_read_b128 v[66:69], v153
	ds_read_b128 v[70:73], v153 offset:256
	v_add_co_u32_e32 v74, vcc, s2, v98
	s_mov_b32 s2, 0x9d000
	s_nop 0
	v_addc_co_u32_e32 v75, vcc, 0, v99, vcc
	s_waitcnt lgkmcnt(0)
	global_store_dwordx4 v[74:75], v[66:69], off sc1
	global_store_dwordx4 v[74:75], v[70:73], off offset:256 sc1
	ds_read_b128 v[66:69], v154 offset:49152
	ds_read_b128 v[70:73], v154 offset:49408
	v_add_co_u32_e32 v74, vcc, s2, v98
	v_pk_add_f32 v[64:65], v[64:65], 0 op_sel_hi:[1,0]
	s_nop 0
	v_addc_co_u32_e32 v75, vcc, 0, v99, vcc
	s_waitcnt lgkmcnt(0)
	global_store_dwordx4 v[74:75], v[66:69], off offset:2048 sc1
	global_store_dwordx4 v[74:75], v[70:73], off offset:2304 sc1
	s_waitcnt lgkmcnt(0)
	s_barrier
; #define LAS __attribute__((address_space(3)))
; __device__ __forceinline__ unsigned cvt_pk_bf16(float lo, float hi) { unsigned r; asm volatile("v_cvt_pk_bf16_f32 %0, %1, %2" : "=v"(r) : "v"(lo), "v"(hi)); return r; }
;     __device__ __forceinline__ void operator()(const f32x4 (&acc)[2][2][4][2], const Unit& u, int wr, int wc, int fr, int fq) const {
;     ...
; #pragma unroll
;         for (int ai = 0; ai < 2; ++ai)
; #pragma unroll
;             for (int mp = 0; mp < 2; ++mp) {
; #pragma unroll
;                 for (int s = 0; s < 2; ++s)
; #pragma unroll
;                     for (int bj = 0; bj < 2; ++bj) { const int m = 2 * mp + s; const f32x4 v0 = acc[ai][bj][m][0] * scale + bv[bj][0], v1 = acc[ai][bj][m][1] * scale + bv[bj][1];
;                         u32x4 w; w.x = cvt_pk_bf16(v0[0], v0[1]); w.y = cvt_pk_bf16(v0[2], v0[3]); w.z = cvt_pk_bf16(v1[0], v1[1]); w.w = cvt_pk_bf16(v1[2], v1[3]);
;                         *(LAS u32x4*)((s ? wp1 : wp0) + 256 * bj) = w; }
;                 asm volatile("s_waitcnt lgkmcnt(0)" ::: "memory"); __builtin_amdgcn_s_barrier(); asm volatile("" ::: "memory");
;                 bf16_t* g2 = gp + (size_t)(ai * HALF + mp * 32) * ldc;
;                 *(u32x4*)(g2) = *(const LAS u32x4*)(rp0); *(u32x4*)(g2 + HALF) = *(const LAS u32x4*)(rp0 + 256);
;                 *(u32x4*)(g2 + (size_t)16 * ldc) = *(const LAS u32x4*)(rp1); *(u32x4*)(g2 + (size_t)16 * ldc + HALF) = *(const LAS u32x4*)(rp1 + 256);
;                 asm volatile("s_waitcnt lgkmcnt(0)" ::: "memory"); __builtin_amdgcn_s_barrier(); asm volatile("" ::: "memory");
;             }
	v_pk_add_f32 v[62:63], v[62:63], 0 op_sel_hi:[1,0]
	v_pk_add_f32 v[66:67], v[60:61], 0 op_sel_hi:[1,0]
	v_pk_add_f32 v[60:61], v[58:59], 0 op_sel_hi:[1,0]
	v_cvt_pk_bf16_f32 v58, v62, v63
	v_cvt_pk_bf16_f32 v59, v64, v65
	v_pk_add_f32 v[56:57], v[56:57], 0 op_sel_hi:[1,0]
	v_cvt_pk_bf16_f32 v60, v60, v61
	v_cvt_pk_bf16_f32 v61, v66, v67
	ds_write_b128 v151, v[58:61]
	v_pk_add_f32 v[58:59], v[48:49], 0 op_sel_hi:[1,0]
	v_pk_add_f32 v[48:49], v[46:47], 0 op_sel_hi:[1,0]
	v_pk_add_f32 v[54:55], v[54:55], 0 op_sel_hi:[1,0]
	v_pk_add_f32 v[40:41], v[40:41], 0 op_sel_hi:[1,0]
	v_cvt_pk_bf16_f32 v46, v54, v55
	v_cvt_pk_bf16_f32 v47, v56, v57
	v_cvt_pk_bf16_f32 v48, v48, v49
	v_cvt_pk_bf16_f32 v49, v58, v59
	ds_write_b128 v151, v[46:49] offset:256
	v_pk_add_f32 v[46:47], v[52:53], 0 op_sel_hi:[1,0]
	v_pk_add_f32 v[48:49], v[50:51], 0 op_sel_hi:[1,0]
	v_pk_add_f32 v[50:51], v[44:45], 0 op_sel_hi:[1,0]
	v_pk_add_f32 v[44:45], v[42:43], 0 op_sel_hi:[1,0]
	v_cvt_pk_bf16_f32 v42, v48, v49
	v_cvt_pk_bf16_f32 v43, v46, v47
	v_pk_add_f32 v[38:39], v[38:39], 0 op_sel_hi:[1,0]
	v_cvt_pk_bf16_f32 v44, v44, v45
	v_cvt_pk_bf16_f32 v45, v50, v51
	ds_write_b128 v152, v[42:45] offset:49152
	v_pk_add_f32 v[42:43], v[36:37], 0 op_sel_hi:[1,0]
	v_pk_add_f32 v[36:37], v[34:35], 0 op_sel_hi:[1,0]
	v_cvt_pk_bf16_f32 v34, v38, v39
	v_cvt_pk_bf16_f32 v35, v40, v41
	s_mov_b32 s2, 0x1a4000
	v_cvt_pk_bf16_f32 v36, v36, v37
	v_cvt_pk_bf16_f32 v37, v42, v43
	ds_write_b128 v152, v[34:37] offset:49408
	s_waitcnt lgkmcnt(0)
	s_barrier
	ds_read_b128 v[34:37], v153
	ds_read_b128 v[38:41], v153 offset:256
	v_add_co_u32_e32 v42, vcc, s2, v98
	s_mov_b32 s2, 0x1d8000
	s_nop 0
	v_addc_co_u32_e32 v43, vcc, 0, v99, vcc
	s_waitcnt lgkmcnt(0)
	global_store_dwordx4 v[42:43], v[34:37], off sc1
	global_store_dwordx4 v[42:43], v[38:41], off offset:256 sc1
	ds_read_b128 v[34:37], v154 offset:49152
	ds_read_b128 v[38:41], v154 offset:49408
	v_add_co_u32_e32 v42, vcc, s2, v98
	v_pk_add_f32 v[32:33], v[32:33], 0 op_sel_hi:[1,0]
	s_nop 0
	v_addc_co_u32_e32 v43, vcc, 0, v99, vcc
	s_waitcnt lgkmcnt(0)
	global_store_dwordx4 v[42:43], v[34:37], off offset:2048 sc1
	global_store_dwordx4 v[42:43], v[38:41], off offset:2304 sc1
	s_waitcnt lgkmcnt(0)
	s_barrier
	v_pk_add_f32 v[30:31], v[30:31], 0 op_sel_hi:[1,0]
	v_pk_add_f32 v[34:35], v[28:29], 0 op_sel_hi:[1,0]
	v_pk_add_f32 v[28:29], v[26:27], 0 op_sel_hi:[1,0]
	v_cvt_pk_bf16_f32 v26, v30, v31
	v_cvt_pk_bf16_f32 v27, v32, v33
	v_pk_add_f32 v[24:25], v[24:25], 0 op_sel_hi:[1,0]
	v_cvt_pk_bf16_f32 v28, v28, v29
	v_cvt_pk_bf16_f32 v29, v34, v35
	ds_write_b128 v151, v[26:29]
	v_pk_add_f32 v[26:27], v[16:17], 0 op_sel_hi:[1,0]
	v_pk_add_f32 v[16:17], v[14:15], 0 op_sel_hi:[1,0]
	v_pk_add_f32 v[22:23], v[22:23], 0 op_sel_hi:[1,0]
	v_pk_add_f32 v[8:9], v[8:9], 0 op_sel_hi:[1,0]
	v_cvt_pk_bf16_f32 v14, v22, v23
	v_cvt_pk_bf16_f32 v15, v24, v25
	v_cvt_pk_bf16_f32 v16, v16, v17
	v_cvt_pk_bf16_f32 v17, v26, v27
	ds_write_b128 v151, v[14:17] offset:256
	v_pk_add_f32 v[14:15], v[20:21], 0 op_sel_hi:[1,0]
	v_pk_add_f32 v[16:17], v[18:19], 0 op_sel_hi:[1,0]
	v_pk_add_f32 v[18:19], v[12:13], 0 op_sel_hi:[1,0]
	v_pk_add_f32 v[12:13], v[10:11], 0 op_sel_hi:[1,0]
	v_cvt_pk_bf16_f32 v10, v16, v17
	v_cvt_pk_bf16_f32 v11, v14, v15
	v_pk_add_f32 v[6:7], v[6:7], 0 op_sel_hi:[1,0]
	v_cvt_pk_bf16_f32 v12, v12, v13
	v_cvt_pk_bf16_f32 v13, v18, v19
	ds_write_b128 v152, v[10:13] offset:49152
	v_pk_add_f32 v[10:11], v[4:5], 0 op_sel_hi:[1,0]
	v_pk_add_f32 v[4:5], v[2:3], 0 op_sel_hi:[1,0]
	v_cvt_pk_bf16_f32 v2, v6, v7
	v_cvt_pk_bf16_f32 v3, v8, v9
	s_mov_b32 s2, 0x20d000
	v_cvt_pk_bf16_f32 v4, v4, v5
	v_cvt_pk_bf16_f32 v5, v10, v11
	ds_write_b128 v152, v[2:5] offset:49408
	s_waitcnt lgkmcnt(0)
	s_barrier
	ds_read_b128 v[2:5], v153
	ds_read_b128 v[6:9], v153 offset:256
	v_add_co_u32_e32 v10, vcc, s2, v98
	s_cmp_eq_u32 s72, s71
	s_nop 0
	v_addc_co_u32_e32 v11, vcc, 0, v99, vcc
	s_waitcnt lgkmcnt(0)
	global_store_dwordx4 v[10:11], v[2:5], off sc1
	global_store_dwordx4 v[10:11], v[6:9], off offset:256 sc1
	ds_read_b128 v[2:5], v154 offset:49152
	ds_read_b128 v[6:9], v154 offset:49408
	v_add_co_u32_e32 v10, vcc, 0x241000, v98
	s_mov_b64 s[2:3], -1
	s_nop 0
	v_addc_co_u32_e32 v11, vcc, 0, v99, vcc
	s_waitcnt lgkmcnt(0)
	global_store_dwordx4 v[10:11], v[2:5], off offset:2048 sc1
	global_store_dwordx4 v[10:11], v[6:9], off offset:2304 sc1
	s_waitcnt lgkmcnt(0)
	s_barrier
	s_cbranch_scc1 .LBB0_322
	s_andn2_b64 vcc, exec, s[0:1]
	s_cbranch_vccnz .LBB0_321
	s_barrier
	s_branch .LBB0_321

; __device__ __forceinline__ unsigned cvt_pk_bf16(float lo, float hi) { unsigned r; asm volatile("v_cvt_pk_bf16_f32 %0, %1, %2" : "=v"(r) : "v"(lo), "v"(hi)); return r; }
; __device__ __forceinline__ float row16_sum(float x) { x = dpp_add<0xB1>(x); x = dpp_add<0x4E>(x); x = dpp_add<0x124>(x); x = dpp_add<0x128>(x); return x; }
; __device__ __forceinline__ void p5_readout(Frame& F) {
;     ...
;     for (int tg = F.bx; tg < M_LAT / 4; tg += F.G) {
;         const int tok = 4 * tg + t4;
; #pragma unroll
;         for (int hh = 0; hh < 2; ++hh) {
;             const int c = (F.wave + 8 * hh) * 64 + 4 * q; const size_t o = (size_t)tok * DR + c;
;             const f32x4 v = ld_bf4(SBb + (size_t)SB_V * (SB_STRIDE / 2) + o), g = ld_bf4(G + o);
;             const f32x2 bon = *(const f32x2*)(WSP(float, WS_XG) + ((size_t)tok * NH + (F.wave + 8 * hh)) * 2);
;             f32x4 osum = (f32x4){0.f, 0.f, 0.f, 0.f};
; #pragma unroll
;             for (int d = 0; d < 2; ++d) {
;                 const f32x4 y = ld_bf4(Y + (size_t)d * M_LAT * DR + o);
;                 const float mu = row16_sum((y.x + y.y) + (y.z + y.w)) * (1.0f / 64.0f); const f32x4 dy = y - mu;
;                 const float var = row16_sum((dy.x * dy.x + dy.y * dy.y) + (dy.z * dy.z + dy.w * dy.w)) * (1.0f / 64.0f);
;     ...
;             const int col = tok & 63; const bf16_t* pr = P + (size_t)tok * P_PAD + cc;
;             f32x4 gb0, gb1, gc0, gc1, u0, u1, pg0, pg1, pu0, pu1, ng0, ng1, nu0, nu1; const f32x4 z = (f32x4){0.f, 0.f, 0.f, 0.f};
;             ld_bf8(pr, gb0, gb1); ld_bf8(pr + DC, gc0, gc1); ld_bf8(pr + 2 * DC, u0, u1);
;             if (col > 0) { ld_bf8(pr - P_PAD + DC, pg0, pg1); ld_bf8(pr - P_PAD + 2 * DC, pu0, pu1); } else { pg0 = z; pg1 = z; pu0 = z; pu1 = z; }
;             if (col < 63) { ld_bf8(pr + P_PAD + DC, ng0, ng1); ld_bf8(pr + P_PAD + 2 * DC, nu0, nu1); } else { ng0 = z; ng1 = z; nu0 = z; nu1 = z; }
;             const f32x4 o0 = gb0 * ((pg0 * pu0) * cw[0][0] + (gc0 * u0) * cw[1][0] + (ng0 * nu0) * cw[2][0]);
;             const f32x4 o1 = gb1 * ((pg1 * pu1) * cw[0][1] + (gc1 * u1) * cw[1][1] + (ng1 * nu1) * cw[2][1]);
;             u32x4 w; w.x = pg8::cvt_pk_bf16(o0.x, o0.y); w.y = pg8::cvt_pk_bf16(o0.z, o0.w); w.z = pg8::cvt_pk_bf16(o1.x, o1.y); w.w = pg8::cvt_pk_bf16(o1.z, o1.w);
;             *(u32x4*)(MI + (size_t)tok * D + cc) = w;
.LBB0_648:
	s_or_b64 exec, exec, s[2:3]
	s_waitcnt vmcnt(1)
	v_lshlrev_b32_e32 v98, 16, v46
	v_and_b32_e32 v99, 0xffff0000, v46
	v_lshlrev_b32_e32 v46, 16, v47
	v_and_b32_e32 v47, 0xffff0000, v47
	s_waitcnt vmcnt(0)
	v_lshlrev_b32_e32 v102, 16, v42
	v_and_b32_e32 v103, 0xffff0000, v42
	v_lshlrev_b32_e32 v42, 16, v43
	v_and_b32_e32 v43, 0xffff0000, v43
	v_pk_mul_f32 v[82:83], v[82:83], v[84:85]
	v_pk_mul_f32 v[78:79], v[78:79], v[80:81]
	v_pk_mul_f32 v[80:81], v[24:25], v[82:83]
	v_pk_mul_f32 v[78:79], v[22:23], v[78:79]
	v_pk_mul_f32 v[82:83], v[98:99], v[102:103]
	v_pk_mul_f32 v[42:43], v[46:47], v[42:43]
	v_pk_fma_f32 v[46:47], v[26:27], v[82:83], v[78:79]
	v_pk_fma_f32 v[42:43], v[28:29], v[42:43], v[80:81]
	v_lshlrev_b32_e32 v74, 16, v50
	v_and_b32_e32 v75, 0xffff0000, v50
	v_lshlrev_b32_e32 v50, 16, v51
	v_and_b32_e32 v51, 0xffff0000, v51
	v_pk_fma_f32 v[46:47], v[30:31], v[92:93], v[46:47]
	v_pk_fma_f32 v[42:43], v[32:33], v[90:91], v[42:43]
	v_lshlrev_b32_e32 v100, 16, v48
	v_and_b32_e32 v101, 0xffff0000, v48
	v_lshlrev_b32_e32 v48, 16, v49
	v_and_b32_e32 v49, 0xffff0000, v49
	v_lshlrev_b32_e32 v104, 16, v44
	v_and_b32_e32 v105, 0xffff0000, v44
	v_lshlrev_b32_e32 v44, 16, v45
	v_and_b32_e32 v45, 0xffff0000, v45
	v_pk_mul_f32 v[50:51], v[42:43], v[50:51]
	v_pk_mul_f32 v[42:43], v[46:47], v[74:75]
	v_pk_mul_f32 v[46:47], v[76:77], v[72:73]
	v_pk_mul_f32 v[68:69], v[70:71], v[68:69]
	v_pk_mul_f32 v[46:47], v[20:21], v[46:47]
	v_pk_mul_f32 v[68:69], v[18:19], v[68:69]
	v_pk_mul_f32 v[70:71], v[100:101], v[104:105]
	v_pk_mul_f32 v[44:45], v[48:49], v[44:45]
	v_lshlrev_b32_e32 v96, 16, v52
	v_pk_fma_f32 v[44:45], v[36:37], v[44:45], v[46:47]
	v_pk_fma_f32 v[46:47], v[34:35], v[70:71], v[68:69]
	v_and_b32_e32 v97, 0xffff0000, v52
	v_lshlrev_b32_e32 v52, 16, v53
	v_and_b32_e32 v53, 0xffff0000, v53
	v_pk_fma_f32 v[46:47], v[38:39], v[88:89], v[46:47]
	v_pk_fma_f32 v[44:45], v[40:41], v[86:87], v[44:45]
	s_add_i32 s20, s20, s79
	v_pk_mul_f32 v[48:49], v[44:45], v[52:53]
	v_pk_mul_f32 v[44:45], v[46:47], v[96:97]
	v_lshl_add_u64 v[46:47], v[60:61], 0, v[66:67]
	s_cmpk_lt_i32 s20, 0x1000
	v_add_u32_e32 v64, s16, v64
	v_cvt_pk_bf16_f32 v42, v42, v43
	v_cvt_pk_bf16_f32 v43, v50, v51
	v_cvt_pk_bf16_f32 v44, v44, v45
	v_cvt_pk_bf16_f32 v45, v48, v49
	global_store_dwordx4 v[46:47], v[42:45], off sc1
	s_cbranch_scc0 .LBB0_653
.LBB0_649:
	v_ashrrev_i32_e32 v65, 31, v64
	v_lshlrev_b64 v[44:45], 10, v[64:65]
	v_lshl_add_u64 v[42:43], v[44:45], 0, v[54:55]
	v_lshlrev_b64 v[42:43], 1, v[42:43]
	v_lshl_add_u64 v[46:47], s[10:11], 0, v[42:43]
	v_lshl_add_u64 v[48:49], s[6:7], 0, v[42:43]
	v_lshl_add_u64 v[42:43], s[0:1], 0, v[42:43]
	global_load_dwordx2 v[46:47], v[46:47], off
	v_lshlrev_b64 v[66:67], 12, v[64:65]
	global_load_dwordx2 v[50:51], v[42:43], off
	v_add_co_u32_e32 v42, vcc, s17, v42
	global_load_dwordx2 v[48:49], v[48:49], off
	s_nop 0
	v_addc_co_u32_e32 v43, vcc, 0, v43, vcc
	global_load_dwordx2 v[52:53], v[42:43], off
	v_lshlrev_b64 v[42:43], 7, v[64:65]
	v_lshl_add_u64 v[68:69], s[12:13], 0, v[42:43]
	v_lshl_add_u64 v[42:43], v[68:69], 0, s[8:9]
	global_load_dwordx2 v[70:71], v[42:43], off
	v_lshl_add_u64 v[42:43], s[4:5], 0, v[66:67]
	v_lshl_add_u64 v[44:45], v[44:45], 0, v[62:63]
	v_lshl_add_u64 v[72:73], v[54:55], 1, v[42:43]
	v_lshlrev_b64 v[44:45], 1, v[44:45]
	v_lshl_add_u64 v[74:75], s[10:11], 0, v[44:45]
	v_lshl_add_u64 v[42:43], v[42:43], 0, v[56:57]
	s_waitcnt vmcnt(0)
	v_lshlrev_b32_e32 v76, 16, v46
	v_and_b32_e32 v77, 0xffff0000, v46
	v_lshlrev_b32_e32 v81, 16, v51
	v_lshlrev_b32_e32 v80, 16, v50
	v_and_b32_e32 v51, 0xffff0000, v51
	v_and_b32_e32 v50, 0xffff0000, v50
	v_pk_add_f32 v[82:83], v[80:81], v[50:51]
	v_lshlrev_b32_e32 v46, 16, v47
	v_lshlrev_b32_e32 v85, 16, v53
	v_lshlrev_b32_e32 v84, 16, v52
	v_and_b32_e32 v53, 0xffff0000, v53
	v_and_b32_e32 v52, 0xffff0000, v52
	v_add_f32_e32 v65, v82, v83
	v_pk_add_f32 v[82:83], v[84:85], v[52:53]
	v_and_b32_e32 v47, 0xffff0000, v47
	v_add_f32_dpp v65, v65, v65 quad_perm:[1,0,3,2] row_mask:0xf bank_mask:0xf bound_ctrl:1
	v_add_f32_e32 v82, v82, v83
	v_lshlrev_b32_e32 v78, 16, v48
	v_add_f32_dpp v65, v65, v65 quad_perm:[2,3,0,1] row_mask:0xf bank_mask:0xf bound_ctrl:1
	v_add_f32_dpp v82, v82, v82 quad_perm:[1,0,3,2] row_mask:0xf bank_mask:0xf bound_ctrl:1
	v_and_b32_e32 v79, 0xffff0000, v48
	v_add_f32_dpp v65, v65, v65 row_ror:4 row_mask:0xf bank_mask:0xf bound_ctrl:1
	v_add_f32_dpp v82, v82, v82 quad_perm:[2,3,0,1] row_mask:0xf bank_mask:0xf bound_ctrl:1
	v_lshlrev_b32_e32 v48, 16, v49
	v_add_f32_dpp v65, v65, v65 row_ror:8 row_mask:0xf bank_mask:0xf bound_ctrl:1
	v_add_f32_dpp v82, v82, v82 row_ror:4 row_mask:0xf bank_mask:0xf bound_ctrl:1
	v_fmac_f32_e32 v50, 0xbc800000, v65
	v_fmac_f32_e32 v80, 0xbc800000, v65
	v_fmac_f32_e32 v51, 0xbc800000, v65
	v_fmac_f32_e32 v81, 0xbc800000, v65
	v_add_f32_dpp v65, v82, v82 row_ror:8 row_mask:0xf bank_mask:0xf bound_ctrl:1
	v_mov_b32_e32 v82, v81
	v_mov_b32_e32 v83, v51
	v_mov_b32_e32 v81, v50
	v_fmac_f32_e32 v52, 0xbc800000, v65
	v_fmac_f32_e32 v53, 0xbc800000, v65
	v_fmac_f32_e32 v85, 0xbc800000, v65
	v_fmac_f32_e32 v84, 0xbc800000, v65
	v_pk_mul_f32 v[50:51], v[82:83], v[82:83]
	v_pk_mul_f32 v[86:87], v[80:81], v[80:81]
	v_mov_b32_e32 v88, v85
	v_mov_b32_e32 v89, v53
	v_mov_b32_e32 v85, v52
	v_pk_mov_b32 v[52:53], v[86:87], v[50:51] op_sel:[1,0]
	v_mov_b32_e32 v87, v51
	v_pk_mul_f32 v[50:51], v[88:89], v[88:89]
	v_pk_mul_f32 v[90:91], v[84:85], v[84:85]
	v_pk_add_f32 v[52:53], v[52:53], v[86:87]
	v_pk_mov_b32 v[86:87], v[90:91], v[50:51] op_sel:[1,0]
	v_mov_b32_e32 v91, v51
	v_add_f32_e32 v52, v52, v53
	v_pk_add_f32 v[50:51], v[86:87], v[90:91]
; __device__ __forceinline__ f32x4 ld_bf4(const bf16_t* p) { const u32x2 w = *(const u32x2*)p; return (f32x4){__builtin_bit_cast(float, w.x << 16), __builtin_bit_cast(float, w.x & 0xffff0000u), __builtin_bit_cast(float, w.y << 16), __builtin_bit_cast(float, w.y & 0xffff0000u)}; }
; __device__ __forceinline__ void st_bf4(bf16_t* p, f32x4 v) { u32x2 w; w.x = pg8::cvt_pk_bf16(v.x, v.y); w.y = pg8::cvt_pk_bf16(v.z, v.w); *(u32x2*)p = w; }
; __device__ __forceinline__ float row16_sum(float x) { x = dpp_add<0xB1>(x); x = dpp_add<0x4E>(x); x = dpp_add<0x124>(x); x = dpp_add<0x128>(x); return x; }
; __device__ __forceinline__ void p5_readout(Frame& F) {
;     ...
;         for (int hh = 0; hh < 2; ++hh) {
;             const int c = (F.wave + 8 * hh) * 64 + 4 * q; const size_t o = (size_t)tok * DR + c;
;             const f32x4 v = ld_bf4(SBb + (size_t)SB_V * (SB_STRIDE / 2) + o), g = ld_bf4(G + o);
;             const f32x2 bon = *(const f32x2*)(WSP(float, WS_XG) + ((size_t)tok * NH + (F.wave + 8 * hh)) * 2);
;             f32x4 osum = (f32x4){0.f, 0.f, 0.f, 0.f};
; #pragma unroll
;             for (int d = 0; d < 2; ++d) {
;                 const f32x4 y = ld_bf4(Y + (size_t)d * M_LAT * DR + o);
;                 const float mu = row16_sum((y.x + y.y) + (y.z + y.w)) * (1.0f / 64.0f); const f32x4 dy = y - mu;
;                 const float var = row16_sum((dy.x * dy.x + dy.y * dy.y) + (dy.z * dy.z + dy.w * dy.w)) * (1.0f / 64.0f);
;                 const float bonus = d ? bon.y : bon.x;
;                 osum += dy * __builtin_amdgcn_rsqf(var + LNX_EPS) * lw[hh] + lb[hh] + bonus * v;
;             }
;             st_bf4(MI + (size_t)tok * D + DC + c, osum * g);
	v_and_b32_e32 v49, 0xffff0000, v49
	v_add_f32_dpp v52, v52, v52 quad_perm:[1,0,3,2] row_mask:0xf bank_mask:0xf bound_ctrl:1
	v_add_f32_e32 v50, v50, v51
	s_nop 0
	v_add_f32_dpp v51, v52, v52 quad_perm:[2,3,0,1] row_mask:0xf bank_mask:0xf bound_ctrl:1
	v_add_f32_dpp v50, v50, v50 quad_perm:[1,0,3,2] row_mask:0xf bank_mask:0xf bound_ctrl:1
	s_nop 0
	v_add_f32_dpp v51, v51, v51 row_ror:4 row_mask:0xf bank_mask:0xf bound_ctrl:1
	v_add_f32_dpp v50, v50, v50 quad_perm:[2,3,0,1] row_mask:0xf bank_mask:0xf bound_ctrl:1
	s_nop 0
	v_add_f32_dpp v51, v51, v51 row_ror:8 row_mask:0xf bank_mask:0xf bound_ctrl:1
	v_add_f32_dpp v52, v50, v50 row_ror:4 row_mask:0xf bank_mask:0xf bound_ctrl:1
	v_fmamk_f32 v50, v51, 0x3c800000, v94
	v_rsq_f32_e32 v50, v50
	v_add_f32_dpp v51, v52, v52 row_ror:8 row_mask:0xf bank_mask:0xf bound_ctrl:1
	v_fmamk_f32 v51, v51, 0x3c800000, v94
	v_rsq_f32_e32 v52, v51
	v_pk_mul_f32 v[80:81], v[80:81], v[50:51] op_sel_hi:[1,0]
	v_pk_mul_f32 v[50:51], v[82:83], v[50:51] op_sel_hi:[1,0]
	v_pk_fma_f32 v[80:81], v[2:3], v[80:81], v[10:11]
	v_pk_fma_f32 v[50:51], v[4:5], v[50:51], v[12:13]
	v_pk_mul_f32 v[82:83], v[88:89], v[52:53] op_sel_hi:[1,0]
	v_pk_mul_f32 v[52:53], v[84:85], v[52:53] op_sel_hi:[1,0]
	v_pk_fma_f32 v[80:81], v[70:71], v[76:77], v[80:81] op_sel_hi:[0,1,1]
	v_pk_fma_f32 v[50:51], v[70:71], v[46:47], v[50:51] op_sel_hi:[0,1,1]
	v_pk_fma_f32 v[52:53], v[2:3], v[52:53], v[10:11]
	v_pk_fma_f32 v[82:83], v[4:5], v[82:83], v[12:13]
	v_pk_add_f32 v[50:51], v[50:51], 0 op_sel_hi:[1,0]
	v_pk_add_f32 v[80:81], v[80:81], 0 op_sel_hi:[1,0]
	v_pk_fma_f32 v[46:47], v[70:71], v[46:47], v[82:83] op_sel:[1,0,0]
	v_pk_fma_f32 v[52:53], v[70:71], v[76:77], v[52:53] op_sel:[1,0,0]
	v_pk_add_f32 v[46:47], v[50:51], v[46:47]
	v_pk_add_f32 v[52:53], v[80:81], v[52:53]
	v_pk_mul_f32 v[46:47], v[46:47], v[48:49]
	v_pk_mul_f32 v[48:49], v[52:53], v[78:79]
	v_lshl_add_u64 v[52:53], v[68:69], 0, s[14:15]
	v_cvt_pk_bf16_f32 v48, v48, v49
	v_cvt_pk_bf16_f32 v49, v46, v47
	global_store_dwordx2 v[72:73], v[48:49], off offset:2048 sc1
	v_lshl_add_u64 v[48:49], s[6:7], 0, v[44:45]
	v_lshl_add_u64 v[44:45], s[0:1], 0, v[44:45]
	global_load_dwordx2 v[46:47], v[74:75], off
	global_load_dwordx2 v[50:51], v[44:45], off
	v_add_co_u32_e32 v44, vcc, s17, v44
	global_load_dwordx2 v[48:49], v[48:49], off
	s_nop 0
	v_addc_co_u32_e32 v45, vcc, 0, v45, vcc
	global_load_dwordx2 v[44:45], v[44:45], off
	v_mad_i64_i32 v[74:75], s[2:3], v64, s18, v[58:59]
	global_load_dwordx2 v[52:53], v[52:53], off
	v_add_co_u32_e32 v68, vcc, 0x1000, v74
	s_waitcnt vmcnt(4)
	v_lshlrev_b32_e32 v70, 16, v46
	s_waitcnt vmcnt(3)
	v_lshlrev_b32_e32 v77, 16, v51
	v_lshlrev_b32_e32 v76, 16, v50
	v_and_b32_e32 v51, 0xffff0000, v51
	v_and_b32_e32 v50, 0xffff0000, v50
	v_pk_add_f32 v[80:81], v[76:77], v[50:51]
	v_and_b32_e32 v71, 0xffff0000, v46
	s_waitcnt vmcnt(1)
; __device__ __forceinline__ f32x4 ld_bf4(const bf16_t* p) { const u32x2 w = *(const u32x2*)p; return (f32x4){__builtin_bit_cast(float, w.x << 16), __builtin_bit_cast(float, w.x & 0xffff0000u), __builtin_bit_cast(float, w.y << 16), __builtin_bit_cast(float, w.y & 0xffff0000u)}; }
; __device__ __forceinline__ void st_bf4(bf16_t* p, f32x4 v) { u32x2 w; w.x = pg8::cvt_pk_bf16(v.x, v.y); w.y = pg8::cvt_pk_bf16(v.z, v.w); *(u32x2*)p = w; }
; __device__ __forceinline__ float row16_sum(float x) { x = dpp_add<0xB1>(x); x = dpp_add<0x4E>(x); x = dpp_add<0x124>(x); x = dpp_add<0x128>(x); return x; }
; __device__ __forceinline__ void p5_readout(Frame& F) {
;     ...
;         for (int hh = 0; hh < 2; ++hh) {
;             const int c = (F.wave + 8 * hh) * 64 + 4 * q; const size_t o = (size_t)tok * DR + c;
;             const f32x4 v = ld_bf4(SBb + (size_t)SB_V * (SB_STRIDE / 2) + o), g = ld_bf4(G + o);
;             const f32x2 bon = *(const f32x2*)(WSP(float, WS_XG) + ((size_t)tok * NH + (F.wave + 8 * hh)) * 2);
;             f32x4 osum = (f32x4){0.f, 0.f, 0.f, 0.f};
; #pragma unroll
;             for (int d = 0; d < 2; ++d) {
;                 const f32x4 y = ld_bf4(Y + (size_t)d * M_LAT * DR + o);
;                 const float mu = row16_sum((y.x + y.y) + (y.z + y.w)) * (1.0f / 64.0f); const f32x4 dy = y - mu;
;                 const float var = row16_sum((dy.x * dy.x + dy.y * dy.y) + (dy.z * dy.z + dy.w * dy.w)) * (1.0f / 64.0f);
;                 const float bonus = d ? bon.y : bon.x;
;                 osum += dy * __builtin_amdgcn_rsqf(var + LNX_EPS) * lw[hh] + lb[hh] + bonus * v;
;             }
;             st_bf4(MI + (size_t)tok * D + DC + c, osum * g);
;         }
;         {
;             const int col = tok & 63; const bf16_t* pr = P + (size_t)tok * P_PAD + cc;
;             f32x4 gb0, gb1, gc0, gc1, u0, u1, pg0, pg1, pu0, pu1, ng0, ng1, nu0, nu1; const f32x4 z = (f32x4){0.f, 0.f, 0.f, 0.f};
;             ld_bf8(pr, gb0, gb1); ld_bf8(pr + DC, gc0, gc1); ld_bf8(pr + 2 * DC, u0, u1);
;             if (col > 0) { ld_bf8(pr - P_PAD + DC, pg0, pg1); ld_bf8(pr - P_PAD + 2 * DC, pu0, pu1); } else { pg0 = z; pg1 = z; pu0 = z; pu1 = z; }
;             if (col < 63) { ld_bf8(pr + P_PAD + DC, ng0, ng1); ld_bf8(pr + P_PAD + 2 * DC, nu0, nu1); } else { ng0 = z; ng1 = z; nu0 = z; nu1 = z; }
	v_lshlrev_b32_e32 v79, 16, v45
	v_lshlrev_b32_e32 v78, 16, v44
	v_and_b32_e32 v45, 0xffff0000, v45
	v_and_b32_e32 v44, 0xffff0000, v44
	v_pk_add_f32 v[82:83], v[78:79], v[44:45]
	v_add_f32_e32 v65, v80, v81
	v_add_f32_e32 v80, v82, v83
	v_lshlrev_b32_e32 v46, 16, v47
	v_add_f32_dpp v65, v65, v65 quad_perm:[1,0,3,2] row_mask:0xf bank_mask:0xf bound_ctrl:1
	v_add_f32_dpp v80, v80, v80 quad_perm:[1,0,3,2] row_mask:0xf bank_mask:0xf bound_ctrl:1
	v_and_b32_e32 v47, 0xffff0000, v47
	v_add_f32_dpp v65, v65, v65 quad_perm:[2,3,0,1] row_mask:0xf bank_mask:0xf bound_ctrl:1
	v_add_f32_dpp v80, v80, v80 quad_perm:[2,3,0,1] row_mask:0xf bank_mask:0xf bound_ctrl:1
	v_lshlrev_b32_e32 v72, 16, v48
	v_add_f32_dpp v65, v65, v65 row_ror:4 row_mask:0xf bank_mask:0xf bound_ctrl:1
	v_add_f32_dpp v80, v80, v80 row_ror:4 row_mask:0xf bank_mask:0xf bound_ctrl:1
	v_and_b32_e32 v73, 0xffff0000, v48
	v_add_f32_dpp v65, v65, v65 row_ror:8 row_mask:0xf bank_mask:0xf bound_ctrl:1
	v_add_f32_dpp v80, v80, v80 row_ror:8 row_mask:0xf bank_mask:0xf bound_ctrl:1
	v_fmac_f32_e32 v50, 0xbc800000, v65
	v_fmac_f32_e32 v51, 0xbc800000, v65
	v_fmac_f32_e32 v77, 0xbc800000, v65
	v_fmac_f32_e32 v76, 0xbc800000, v65
	v_fmac_f32_e32 v44, 0xbc800000, v80
	v_fmac_f32_e32 v78, 0xbc800000, v80
	v_fmac_f32_e32 v45, 0xbc800000, v80
	v_fmac_f32_e32 v79, 0xbc800000, v80
	v_mov_b32_e32 v80, v77
	v_mov_b32_e32 v81, v51
	v_mov_b32_e32 v77, v50
	v_mov_b32_e32 v50, v79
	v_mov_b32_e32 v51, v45
	v_mov_b32_e32 v79, v44
	v_pk_mul_f32 v[44:45], v[80:81], v[80:81]
	v_pk_mul_f32 v[82:83], v[76:77], v[76:77]
	v_pk_mul_f32 v[84:85], v[50:51], v[50:51]
	v_pk_mul_f32 v[86:87], v[78:79], v[78:79]
	v_pk_mov_b32 v[88:89], v[82:83], v[44:45] op_sel:[1,0]
	v_mov_b32_e32 v83, v45
	v_pk_mov_b32 v[44:45], v[86:87], v[84:85] op_sel:[1,0]
	v_mov_b32_e32 v87, v85
	v_pk_add_f32 v[82:83], v[88:89], v[82:83]
	v_pk_add_f32 v[44:45], v[44:45], v[86:87]
	v_add_f32_e32 v65, v82, v83
	v_add_f32_e32 v44, v44, v45
	v_lshlrev_b32_e32 v48, 16, v49
	v_add_f32_dpp v45, v65, v65 quad_perm:[1,0,3,2] row_mask:0xf bank_mask:0xf bound_ctrl:1
	v_add_f32_dpp v44, v44, v44 quad_perm:[1,0,3,2] row_mask:0xf bank_mask:0xf bound_ctrl:1
	v_and_b32_e32 v49, 0xffff0000, v49
	v_add_f32_dpp v45, v45, v45 quad_perm:[2,3,0,1] row_mask:0xf bank_mask:0xf bound_ctrl:1
	v_add_f32_dpp v44, v44, v44 quad_perm:[2,3,0,1] row_mask:0xf bank_mask:0xf bound_ctrl:1
	v_addc_co_u32_e32 v69, vcc, 0, v75, vcc
	v_add_f32_dpp v45, v45, v45 row_ror:4 row_mask:0xf bank_mask:0xf bound_ctrl:1
	v_add_f32_dpp v44, v44, v44 row_ror:4 row_mask:0xf bank_mask:0xf bound_ctrl:1
	v_mov_b32_e32 v84, 0
	v_add_f32_dpp v45, v45, v45 row_ror:8 row_mask:0xf bank_mask:0xf bound_ctrl:1
	v_add_f32_dpp v65, v44, v44 row_ror:8 row_mask:0xf bank_mask:0xf bound_ctrl:1
	v_fmamk_f32 v44, v45, 0x3c800000, v94
	v_rsq_f32_e32 v44, v44
	v_fmamk_f32 v45, v65, 0x3c800000, v94
	v_rsq_f32_e32 v82, v45
	v_and_b32_e32 v65, 63, v64
	v_pk_mul_f32 v[76:77], v[76:77], v[44:45] op_sel_hi:[1,0]
	v_pk_mul_f32 v[44:45], v[80:81], v[44:45] op_sel_hi:[1,0]
	v_pk_mul_f32 v[50:51], v[50:51], v[82:83] op_sel_hi:[1,0]
	v_pk_mul_f32 v[78:79], v[78:79], v[82:83] op_sel_hi:[1,0]
	v_pk_fma_f32 v[76:77], v[6:7], v[76:77], v[14:15]
	v_pk_fma_f32 v[44:45], v[8:9], v[44:45], v[16:17]
	v_pk_fma_f32 v[78:79], v[6:7], v[78:79], v[14:15]
	v_pk_fma_f32 v[50:51], v[8:9], v[50:51], v[16:17]
	s_waitcnt vmcnt(0)
	v_pk_fma_f32 v[76:77], v[52:53], v[70:71], v[76:77] op_sel_hi:[0,1,1]
	v_pk_fma_f32 v[44:45], v[52:53], v[46:47], v[44:45] op_sel_hi:[0,1,1]
	v_pk_fma_f32 v[46:47], v[52:53], v[46:47], v[50:51] op_sel:[1,0,0]
	v_pk_fma_f32 v[50:51], v[52:53], v[70:71], v[78:79] op_sel:[1,0,0]
	v_pk_add_f32 v[52:53], v[76:77], 0 op_sel_hi:[1,0]
	v_pk_add_f32 v[44:45], v[44:45], 0 op_sel_hi:[1,0]
	v_pk_add_f32 v[50:51], v[52:53], v[50:51]
	v_pk_add_f32 v[44:45], v[44:45], v[46:47]
	v_pk_mul_f32 v[46:47], v[50:51], v[72:73]
	v_pk_mul_f32 v[44:45], v[44:45], v[48:49]
	v_cvt_pk_bf16_f32 v46, v46, v47
	v_cmp_ne_u32_e32 vcc, 0, v65
	v_cvt_pk_bf16_f32 v47, v44, v45
	global_store_dwordx2 v[42:43], v[46:47], off offset:2048 sc1
	global_load_dwordx4 v[50:53], v[74:75], off
	s_nop 0
	global_load_dwordx4 v[46:49], v[74:75], off offset:2048
	global_load_dwordx4 v[42:45], v[68:69], off
	v_mov_b32_e32 v78, 0
	v_mov_b32_e32 v79, 0
	v_mov_b32_e32 v82, 0
	v_mov_b32_e32 v83, 0
	v_mov_b32_e32 v70, 0
	v_mov_b32_e32 v71, 0
	v_mov_b32_e32 v76, 0
	v_mov_b32_e32 v77, 0
	v_mov_b32_e32 v68, 0
	v_mov_b32_e32 v69, 0
	v_mov_b32_e32 v72, 0
	v_mov_b32_e32 v73, 0
	v_mov_b32_e32 v80, 0
	v_mov_b32_e32 v81, 0
	v_mov_b32_e32 v85, 0
	s_and_saveexec_b64 s[2:3], vcc
	s_cbranch_execz .LBB0_651
	v_add_co_u32_e32 v72, vcc, 0xffffe000, v74
	s_nop 1
	v_addc_co_u32_e32 v73, vcc, -1, v75, vcc
	global_load_dwordx4 v[68:71], v[72:73], off offset:-3200
	global_load_dwordx4 v[86:89], v[72:73], off offset:-1152
	s_waitcnt vmcnt(1)
	v_lshlrev_b32_e32 v80, 16, v68
	v_and_b32_e32 v81, 0xffff0000, v68
	v_lshlrev_b32_e32 v84, 16, v69
	v_and_b32_e32 v85, 0xffff0000, v69
	v_lshlrev_b32_e32 v68, 16, v70
	v_and_b32_e32 v69, 0xffff0000, v70
	v_lshlrev_b32_e32 v72, 16, v71
	v_and_b32_e32 v73, 0xffff0000, v71
	s_waitcnt vmcnt(0)
	v_lshlrev_b32_e32 v78, 16, v86
	v_and_b32_e32 v79, 0xffff0000, v86
	v_lshlrev_b32_e32 v82, 16, v87
	v_and_b32_e32 v83, 0xffff0000, v87
	v_lshlrev_b32_e32 v70, 16, v88
	v_and_b32_e32 v71, 0xffff0000, v88
	v_lshlrev_b32_e32 v76, 16, v89
	v_and_b32_e32 v77, 0xffff0000, v89

; #define LAS __attribute__((address_space(3)))
; __device__ __forceinline__ unsigned cvt_pk_bf16(float lo, float hi) { unsigned r; asm volatile("v_cvt_pk_bf16_f32 %0, %1, %2" : "=v"(r) : "v"(lo), "v"(hi)); return r; }
;     __device__ __forceinline__ void operator()(const f32x4 (&acc)[2][2][4][2], const Unit& u, int wr, int wc, int fr, int fq) const {
;     ...
;         LAS unsigned char* wp0 = stg + (16 * wr + fr) * STG_PITCH + 64 * wc + 16 * fq;
;         LAS unsigned char* wp1 = stg2 + (16 * wr + fr) * 512 + (((4 * wc + fq) ^ (fr & 7)) * 16);
;         const int rr = tid >> 4, cc = tid & 15; const LAS unsigned char* rp0 = stg + rr * STG_PITCH + cc * 16;
;         const LAS unsigned char* rp1 = stg2 + rr * 512 + ((cc ^ (rr & 7)) * 16);
;         bf16_t* gp = O + (size_t)(u.pm * BM + 64 * (rr >> 4) + (rr & 15)) * ldc + pnl * BM + cc * 8;
; #pragma unroll
;         for (int ai = 0; ai < 2; ++ai)
; #pragma unroll
;             for (int mp = 0; mp < 2; ++mp) {
; #pragma unroll
;                 for (int s = 0; s < 2; ++s)
; #pragma unroll
;                     for (int bj = 0; bj < 2; ++bj) { const int m = 2 * mp + s; const f32x4 v0 = acc[ai][bj][m][0] * scale + bv[bj][0], v1 = acc[ai][bj][m][1] * scale + bv[bj][1];
;                         u32x4 w; w.x = cvt_pk_bf16(v0[0], v0[1]); w.y = cvt_pk_bf16(v0[2], v0[3]); w.z = cvt_pk_bf16(v1[0], v1[1]); w.w = cvt_pk_bf16(v1[2], v1[3]);
;                         *(LAS u32x4*)((s ? wp1 : wp0) + 256 * bj) = w; }
;                 asm volatile("s_waitcnt lgkmcnt(0)" ::: "memory"); __builtin_amdgcn_s_barrier(); asm volatile("" ::: "memory");
;                 bf16_t* g2 = gp + (size_t)(ai * HALF + mp * 32) * ldc;
;                 *(u32x4*)(g2) = *(const LAS u32x4*)(rp0); *(u32x4*)(g2 + HALF) = *(const LAS u32x4*)(rp0 + 256);
;                 *(u32x4*)(g2 + (size_t)16 * ldc) = *(const LAS u32x4*)(rp1); *(u32x4*)(g2 + (size_t)16 * ldc + HALF) = *(const LAS u32x4*)(rp1 + 256);
;                 asm volatile("s_waitcnt lgkmcnt(0)" ::: "memory"); __builtin_amdgcn_s_barrier(); asm volatile("" ::: "memory");
.LBB0_724:
	v_pk_add_f32 v[128:129], v[128:129], 0 op_sel_hi:[1,0]
	v_pk_add_f32 v[126:127], v[126:127], 0 op_sel_hi:[1,0]
	v_pk_add_f32 v[146:147], v[124:125], 0 op_sel_hi:[1,0]
	v_pk_add_f32 v[124:125], v[122:123], 0 op_sel_hi:[1,0]
	v_cvt_pk_bf16_f32 v122, v126, v127
	v_cvt_pk_bf16_f32 v123, v128, v129
	v_pk_add_f32 v[120:121], v[120:121], 0 op_sel_hi:[1,0]
	v_cvt_pk_bf16_f32 v124, v124, v125
	v_cvt_pk_bf16_f32 v125, v146, v147
	ds_write_b128 v151, v[122:125]
	v_pk_add_f32 v[122:123], v[112:113], 0 op_sel_hi:[1,0]
	v_pk_add_f32 v[112:113], v[110:111], 0 op_sel_hi:[1,0]
	v_pk_add_f32 v[118:119], v[118:119], 0 op_sel_hi:[1,0]
	s_ashr_i32 s2, s19, 31
	v_cvt_pk_bf16_f32 v110, v118, v119
	v_cvt_pk_bf16_f32 v111, v120, v121
	v_cvt_pk_bf16_f32 v112, v112, v113
	v_cvt_pk_bf16_f32 v113, v122, v123
	ds_write_b128 v151, v[110:113] offset:256
	v_pk_add_f32 v[110:111], v[116:117], 0 op_sel_hi:[1,0]
	v_pk_add_f32 v[112:113], v[114:115], 0 op_sel_hi:[1,0]
	v_pk_add_f32 v[114:115], v[108:109], 0 op_sel_hi:[1,0]
	v_pk_add_f32 v[108:109], v[106:107], 0 op_sel_hi:[1,0]
	v_cvt_pk_bf16_f32 v106, v112, v113
	v_cvt_pk_bf16_f32 v107, v110, v111
	s_lshr_b32 s2, s2, 12
	v_cvt_pk_bf16_f32 v108, v108, v109
	v_cvt_pk_bf16_f32 v109, v114, v115
	ds_write_b128 v152, v[106:109] offset:49152
	v_pk_add_f32 v[106:107], v[100:101], 0 op_sel_hi:[1,0]
	v_pk_add_f32 v[100:101], v[98:99], 0 op_sel_hi:[1,0]
	s_add_i32 s2, s19, s2
	v_pk_add_f32 v[104:105], v[104:105], 0 op_sel_hi:[1,0]
	v_pk_add_f32 v[102:103], v[102:103], 0 op_sel_hi:[1,0]
	s_and_b32 s2, s2, 0xf00000
	v_cvt_pk_bf16_f32 v98, v102, v103
	v_cvt_pk_bf16_f32 v99, v104, v105
	v_cvt_pk_bf16_f32 v100, v100, v101
	v_cvt_pk_bf16_f32 v101, v106, v107
	ds_write_b128 v152, v[98:101] offset:49408
	v_lshl_or_b32 v144, s18, 8, v150
	s_waitcnt lgkmcnt(0)
	s_barrier
	s_sub_i32 s2, s19, s2
	v_ashrrev_i32_e32 v145, 31, v144
	ds_read_b128 v[100:103], v153
	ds_read_b128 v[104:107], v153 offset:256
	s_lshl_b32 s2, s2, 8
	v_lshlrev_b64 v[144:145], 12, v[144:145]
	v_lshl_add_u64 v[144:145], s[4:5], 0, v[144:145]
	s_ashr_i32 s3, s2, 31
	v_lshl_add_u64 v[98:99], s[2:3], 1, v[144:145]
	v_lshl_add_u64 v[98:99], v[98:99], 0, v[138:139]
	s_waitcnt lgkmcnt(0)
	global_store_dwordx4 v[98:99], v[100:103], off sc1
	global_store_dwordx4 v[98:99], v[104:107], off offset:256 sc1
	ds_read_b128 v[100:103], v154 offset:49152
	ds_read_b128 v[104:107], v154 offset:49408
	v_add_co_u32_e32 v108, vcc, s53, v98
	v_pk_add_f32 v[96:97], v[96:97], 0 op_sel_hi:[1,0]
	s_nop 0
	v_addc_co_u32_e32 v109, vcc, 0, v99, vcc
	s_waitcnt lgkmcnt(0)
	global_store_dwordx4 v[108:109], v[100:103], off sc1
	global_store_dwordx4 v[108:109], v[104:107], off offset:256 sc1
	s_waitcnt lgkmcnt(0)
	s_barrier
	v_pk_add_f32 v[94:95], v[94:95], 0 op_sel_hi:[1,0]
	v_pk_add_f32 v[100:101], v[92:93], 0 op_sel_hi:[1,0]
	v_pk_add_f32 v[92:93], v[90:91], 0 op_sel_hi:[1,0]
	v_cvt_pk_bf16_f32 v90, v94, v95
	v_cvt_pk_bf16_f32 v91, v96, v97
	v_pk_add_f32 v[88:89], v[88:89], 0 op_sel_hi:[1,0]
	v_cvt_pk_bf16_f32 v92, v92, v93
	v_cvt_pk_bf16_f32 v93, v100, v101
	ds_write_b128 v151, v[90:93]
	v_pk_add_f32 v[90:91], v[80:81], 0 op_sel_hi:[1,0]
	v_pk_add_f32 v[80:81], v[78:79], 0 op_sel_hi:[1,0]
	v_pk_add_f32 v[86:87], v[86:87], 0 op_sel_hi:[1,0]
	v_pk_add_f32 v[72:73], v[72:73], 0 op_sel_hi:[1,0]
	v_cvt_pk_bf16_f32 v78, v86, v87
	v_cvt_pk_bf16_f32 v79, v88, v89
	v_cvt_pk_bf16_f32 v80, v80, v81
	v_cvt_pk_bf16_f32 v81, v90, v91
	ds_write_b128 v151, v[78:81] offset:256
	v_pk_add_f32 v[78:79], v[84:85], 0 op_sel_hi:[1,0]
	v_pk_add_f32 v[80:81], v[82:83], 0 op_sel_hi:[1,0]
	v_pk_add_f32 v[82:83], v[76:77], 0 op_sel_hi:[1,0]
	v_pk_add_f32 v[76:77], v[74:75], 0 op_sel_hi:[1,0]
	v_cvt_pk_bf16_f32 v74, v80, v81
	v_cvt_pk_bf16_f32 v75, v78, v79
	v_pk_add_f32 v[70:71], v[70:71], 0 op_sel_hi:[1,0]
	v_cvt_pk_bf16_f32 v76, v76, v77
	v_cvt_pk_bf16_f32 v77, v82, v83
	ds_write_b128 v152, v[74:77] offset:49152
	v_pk_add_f32 v[74:75], v[68:69], 0 op_sel_hi:[1,0]
	v_pk_add_f32 v[68:69], v[66:67], 0 op_sel_hi:[1,0]
	v_cvt_pk_bf16_f32 v66, v70, v71
	v_cvt_pk_bf16_f32 v67, v72, v73
	v_pk_add_f32 v[64:65], v[64:65], 0 op_sel_hi:[1,0]
	v_cvt_pk_bf16_f32 v68, v68, v69
	v_cvt_pk_bf16_f32 v69, v74, v75
	ds_write_b128 v152, v[66:69] offset:49408
	s_waitcnt lgkmcnt(0)
	s_barrier
	ds_read_b128 v[66:69], v153
	ds_read_b128 v[70:73], v153 offset:256
	v_add_co_u32_e32 v74, vcc, s54, v98
	v_pk_add_f32 v[62:63], v[62:63], 0 op_sel_hi:[1,0]
	s_nop 0
	v_addc_co_u32_e32 v75, vcc, 0, v99, vcc
	s_waitcnt lgkmcnt(0)
	global_store_dwordx4 v[74:75], v[66:69], off sc1
	global_store_dwordx4 v[74:75], v[70:73], off offset:256 sc1
	ds_read_b128 v[66:69], v154 offset:49152
	ds_read_b128 v[70:73], v154 offset:49408
	v_add_co_u32_e32 v74, vcc, s52, v98
	v_pk_add_f32 v[56:57], v[56:57], 0 op_sel_hi:[1,0]
	s_nop 0
	v_addc_co_u32_e32 v75, vcc, 0, v99, vcc
	s_waitcnt lgkmcnt(0)
	global_store_dwordx4 v[74:75], v[66:69], off sc1
	global_store_dwordx4 v[74:75], v[70:73], off offset:256 sc1
	s_waitcnt lgkmcnt(0)
	s_barrier
; #define LAS __attribute__((address_space(3)))
; __device__ __forceinline__ unsigned cvt_pk_bf16(float lo, float hi) { unsigned r; asm volatile("v_cvt_pk_bf16_f32 %0, %1, %2" : "=v"(r) : "v"(lo), "v"(hi)); return r; }
;     __device__ __forceinline__ void operator()(const f32x4 (&acc)[2][2][4][2], const Unit& u, int wr, int wc, int fr, int fq) const {
;     ...
; #pragma unroll
;         for (int ai = 0; ai < 2; ++ai)
; #pragma unroll
;             for (int mp = 0; mp < 2; ++mp) {
; #pragma unroll
;                 for (int s = 0; s < 2; ++s)
; #pragma unroll
;                     for (int bj = 0; bj < 2; ++bj) { const int m = 2 * mp + s; const f32x4 v0 = acc[ai][bj][m][0] * scale + bv[bj][0], v1 = acc[ai][bj][m][1] * scale + bv[bj][1];
;                         u32x4 w; w.x = cvt_pk_bf16(v0[0], v0[1]); w.y = cvt_pk_bf16(v0[2], v0[3]); w.z = cvt_pk_bf16(v1[0], v1[1]); w.w = cvt_pk_bf16(v1[2], v1[3]);
;                         *(LAS u32x4*)((s ? wp1 : wp0) + 256 * bj) = w; }
;                 asm volatile("s_waitcnt lgkmcnt(0)" ::: "memory"); __builtin_amdgcn_s_barrier(); asm volatile("" ::: "memory");
;                 bf16_t* g2 = gp + (size_t)(ai * HALF + mp * 32) * ldc;
;                 *(u32x4*)(g2) = *(const LAS u32x4*)(rp0); *(u32x4*)(g2 + HALF) = *(const LAS u32x4*)(rp0 + 256);
;                 *(u32x4*)(g2 + (size_t)16 * ldc) = *(const LAS u32x4*)(rp1); *(u32x4*)(g2 + (size_t)16 * ldc + HALF) = *(const LAS u32x4*)(rp1 + 256);
;                 asm volatile("s_waitcnt lgkmcnt(0)" ::: "memory"); __builtin_amdgcn_s_barrier(); asm volatile("" ::: "memory");
;             }
	v_pk_add_f32 v[66:67], v[60:61], 0 op_sel_hi:[1,0]
	v_pk_add_f32 v[60:61], v[58:59], 0 op_sel_hi:[1,0]
	v_cvt_pk_bf16_f32 v58, v62, v63
	v_cvt_pk_bf16_f32 v59, v64, v65
	v_pk_add_f32 v[54:55], v[54:55], 0 op_sel_hi:[1,0]
	v_cvt_pk_bf16_f32 v60, v60, v61
	v_cvt_pk_bf16_f32 v61, v66, v67
	ds_write_b128 v151, v[58:61]
	v_pk_add_f32 v[58:59], v[48:49], 0 op_sel_hi:[1,0]
	v_pk_add_f32 v[48:49], v[46:47], 0 op_sel_hi:[1,0]
	v_cvt_pk_bf16_f32 v46, v54, v55
	v_cvt_pk_bf16_f32 v47, v56, v57
	v_pk_add_f32 v[40:41], v[40:41], 0 op_sel_hi:[1,0]
	v_cvt_pk_bf16_f32 v48, v48, v49
	v_cvt_pk_bf16_f32 v49, v58, v59
	ds_write_b128 v151, v[46:49] offset:256
	v_pk_add_f32 v[46:47], v[52:53], 0 op_sel_hi:[1,0]
	v_pk_add_f32 v[48:49], v[50:51], 0 op_sel_hi:[1,0]
	v_pk_add_f32 v[50:51], v[44:45], 0 op_sel_hi:[1,0]
	v_pk_add_f32 v[44:45], v[42:43], 0 op_sel_hi:[1,0]
	v_cvt_pk_bf16_f32 v42, v48, v49
	v_cvt_pk_bf16_f32 v43, v46, v47
	v_pk_add_f32 v[38:39], v[38:39], 0 op_sel_hi:[1,0]
	v_cvt_pk_bf16_f32 v44, v44, v45
	v_cvt_pk_bf16_f32 v45, v50, v51
	ds_write_b128 v152, v[42:45] offset:49152
	v_pk_add_f32 v[42:43], v[36:37], 0 op_sel_hi:[1,0]
	v_pk_add_f32 v[36:37], v[34:35], 0 op_sel_hi:[1,0]
	v_cvt_pk_bf16_f32 v34, v38, v39
	v_cvt_pk_bf16_f32 v35, v40, v41
	v_pk_add_f32 v[32:33], v[32:33], 0 op_sel_hi:[1,0]
	v_cvt_pk_bf16_f32 v36, v36, v37
	v_cvt_pk_bf16_f32 v37, v42, v43
	ds_write_b128 v152, v[34:37] offset:49408
	s_waitcnt lgkmcnt(0)
	s_barrier
	ds_read_b128 v[34:37], v153
	ds_read_b128 v[38:41], v153 offset:256
	v_add_co_u32_e32 v42, vcc, s55, v98
	v_pk_add_f32 v[30:31], v[30:31], 0 op_sel_hi:[1,0]
	s_nop 0
	v_addc_co_u32_e32 v43, vcc, 0, v99, vcc
	s_waitcnt lgkmcnt(0)
	global_store_dwordx4 v[42:43], v[34:37], off sc1
	global_store_dwordx4 v[42:43], v[38:41], off offset:256 sc1
	ds_read_b128 v[34:37], v154 offset:49152
	ds_read_b128 v[38:41], v154 offset:49408
	v_add_co_u32_e32 v42, vcc, s56, v98
	v_pk_add_f32 v[24:25], v[24:25], 0 op_sel_hi:[1,0]
	s_nop 0
	v_addc_co_u32_e32 v43, vcc, 0, v99, vcc
	s_waitcnt lgkmcnt(0)
	global_store_dwordx4 v[42:43], v[34:37], off sc1
	global_store_dwordx4 v[42:43], v[38:41], off offset:256 sc1
	s_waitcnt lgkmcnt(0)
	s_barrier
	v_pk_add_f32 v[34:35], v[28:29], 0 op_sel_hi:[1,0]
	v_pk_add_f32 v[28:29], v[26:27], 0 op_sel_hi:[1,0]
	v_cvt_pk_bf16_f32 v26, v30, v31
	v_cvt_pk_bf16_f32 v27, v32, v33
	v_pk_add_f32 v[22:23], v[22:23], 0 op_sel_hi:[1,0]
	v_cvt_pk_bf16_f32 v28, v28, v29
	v_cvt_pk_bf16_f32 v29, v34, v35
	ds_write_b128 v151, v[26:29]
	v_pk_add_f32 v[26:27], v[16:17], 0 op_sel_hi:[1,0]
	v_pk_add_f32 v[16:17], v[14:15], 0 op_sel_hi:[1,0]
	v_cvt_pk_bf16_f32 v14, v22, v23
	v_cvt_pk_bf16_f32 v15, v24, v25
	v_pk_add_f32 v[8:9], v[8:9], 0 op_sel_hi:[1,0]
	v_cvt_pk_bf16_f32 v16, v16, v17
	v_cvt_pk_bf16_f32 v17, v26, v27
	ds_write_b128 v151, v[14:17] offset:256
	v_pk_add_f32 v[14:15], v[20:21], 0 op_sel_hi:[1,0]
	v_pk_add_f32 v[16:17], v[18:19], 0 op_sel_hi:[1,0]
	v_pk_add_f32 v[18:19], v[12:13], 0 op_sel_hi:[1,0]
	v_pk_add_f32 v[12:13], v[10:11], 0 op_sel_hi:[1,0]
	v_cvt_pk_bf16_f32 v10, v16, v17
	v_cvt_pk_bf16_f32 v11, v14, v15
	v_pk_add_f32 v[6:7], v[6:7], 0 op_sel_hi:[1,0]
	v_cvt_pk_bf16_f32 v12, v12, v13
	v_cvt_pk_bf16_f32 v13, v18, v19
	ds_write_b128 v152, v[10:13] offset:49152
	v_pk_add_f32 v[10:11], v[4:5], 0 op_sel_hi:[1,0]
	v_pk_add_f32 v[4:5], v[2:3], 0 op_sel_hi:[1,0]
	v_cvt_pk_bf16_f32 v2, v6, v7
	v_cvt_pk_bf16_f32 v3, v8, v9
	s_cmp_eq_u32 s51, s50
	v_cvt_pk_bf16_f32 v4, v4, v5
	v_cvt_pk_bf16_f32 v5, v10, v11
	ds_write_b128 v152, v[2:5] offset:49408
	s_waitcnt lgkmcnt(0)
	s_barrier
	ds_read_b128 v[2:5], v153
	ds_read_b128 v[6:9], v153 offset:256
	v_add_co_u32_e32 v10, vcc, s57, v98
	s_mov_b64 s[2:3], -1
	s_nop 0
	v_addc_co_u32_e32 v11, vcc, 0, v99, vcc
	s_waitcnt lgkmcnt(0)
	global_store_dwordx4 v[10:11], v[2:5], off sc1
	global_store_dwordx4 v[10:11], v[6:9], off offset:256 sc1
	ds_read_b128 v[2:5], v154 offset:49152
	ds_read_b128 v[6:9], v154 offset:49408
	v_add_co_u32_e32 v10, vcc, 0xb0000, v98
	s_nop 1
	v_addc_co_u32_e32 v11, vcc, 0, v99, vcc
	s_waitcnt lgkmcnt(0)
	global_store_dwordx4 v[10:11], v[2:5], off sc1
	global_store_dwordx4 v[10:11], v[6:9], off offset:256 sc1
	s_waitcnt lgkmcnt(0)
	s_barrier
	s_cbranch_scc1 .LBB0_717
	s_andn2_b64 vcc, exec, s[0:1]
	s_cbranch_vccnz .LBB0_716
	s_barrier
	s_branch .LBB0_716

; #define LAS __attribute__((address_space(3)))
; __device__ __forceinline__ f32x4 ld_bf4(const bf16_t* p) { const u32x2 w = *(const u32x2*)p; return (f32x4){__builtin_bit_cast(float, w.x << 16), __builtin_bit_cast(float, w.x & 0xffff0000u), __builtin_bit_cast(float, w.y << 16), __builtin_bit_cast(float, w.y & 0xffff0000u)}; }
; __device__ __forceinline__ void st_bf4(bf16_t* p, f32x4 v) { u32x2 w; w.x = pg8::cvt_pk_bf16(v.x, v.y); w.y = pg8::cvt_pk_bf16(v.z, v.w); *(u32x2*)p = w; }
; template <bool FAST>
; __device__ __forceinline__ void p7_route_t(Frame& F, const bool do_route) {
;     ...
;         const int row_ = FAST ? (F.bx * NIT + it) * 8 + F.wave : gw + it * NGW;
;         const bool valid = row_ < M_LAT; const int row = valid ? row_ : M_LAT - 1;
;         const float* mr = mod + (row / T) * NMOD;
;         f32x4 v[8], xv[8]; float ss = 0.f;
; #pragma unroll
;         for (int j = 0; j < 8; ++j) { v[j] = ld_bf4(MIX + (size_t)row * D + 4 * F.lane + 256 * j); xv[j] = *(const f32x4*)(IN_X + (size_t)row * D + 4 * F.lane + 256 * j); }
; #pragma unroll
;         for (int j = 0; j < 8; ++j) ss += (v[j].x * v[j].x + v[j].y * v[j].y) + (v[j].z * v[j].z + v[j].w * v[j].w);
;         float rstd = __builtin_amdgcn_rsqf(wave_sum(ss) * (1.0f / D) + RMS_EPS);
;         ss = 0.f;
; #pragma unroll
;         for (int j = 0; j < 8; ++j) { const int c = 4 * F.lane + 256 * j;
;             const f32x4 gg = FAST ? *(const LAS f32x4*)(pvec + c) : *(const f32x4*)(IN_NORMG + D + c) * *(const f32x4*)(mr + 2 * D + c);
;             v[j] = xv[j] + gg * (v[j] * rstd);
;             if (valid) st_bf4(X1 + (size_t)row * D + c, v[j]);
;             ss += (v[j].x * v[j].x + v[j].y * v[j].y) + (v[j].z * v[j].z + v[j].w * v[j].w); }
.LBB0_790:
	s_add_i32 s0, s93, s33
	s_lshl_b32 s0, s0, 3
	v_readlane_b32 s1, v254, 35
	s_add_i32 s90, s0, s1
	s_cmpk_gt_i32 s90, 0x3fff
	s_cselect_b64 s[0:1], -1, 0
	s_cmpk_lt_i32 s90, 0x4000
	s_cselect_b64 s[18:19], -1, 0
	s_min_i32 s16, s90, 0x3fff
	s_ashr_i32 s17, s16, 31
	s_lshl_b64 s[2:3], s[16:17], 12
	v_lshl_add_u64 v[2:3], v[36:37], 0, s[2:3]
	global_load_dwordx2 v[30:31], v[2:3], off offset:1536
	global_load_dwordx2 v[44:45], v[2:3], off offset:3584
	global_load_dwordx2 v[50:51], v[2:3], off
	global_load_dwordx2 v[52:53], v[2:3], off offset:512
	global_load_dwordx2 v[54:55], v[2:3], off offset:1024
	global_load_dwordx2 v[56:57], v[2:3], off offset:2048
	global_load_dwordx2 v[58:59], v[2:3], off offset:2560
	global_load_dwordx2 v[110:111], v[2:3], off offset:3072
	s_lshl_b64 s[2:3], s[16:17], 13
	v_lshl_add_u64 v[2:3], v[38:39], 0, s[2:3]
	global_load_dwordx4 v[46:49], v[2:3], off
	global_load_dwordx4 v[26:29], v[2:3], off offset:1024
	global_load_dwordx4 v[22:25], v[2:3], off offset:2048
	global_load_dwordx4 v[18:21], v[2:3], off offset:3072
	v_add_co_u32_e32 v2, vcc, s92, v2
	s_ashr_i32 s91, s90, 31
	s_nop 0
	v_addc_co_u32_e32 v3, vcc, 0, v3, vcc
	global_load_dwordx4 v[14:17], v[2:3], off
	global_load_dwordx4 v[10:13], v[2:3], off offset:1024
	global_load_dwordx4 v[6:9], v[2:3], off offset:2048
	s_nop 0
	global_load_dwordx4 v[2:5], v[2:3], off offset:3072
	s_waitcnt vmcnt(15)
	v_lshlrev_b32_e32 v63, 16, v30
	v_and_b32_e32 v61, 0xffff0000, v30
	s_waitcnt vmcnt(13)
	v_and_b32_e32 v115, 0xffff0000, v50
	v_and_b32_e32 v117, 0xffff0000, v51
	v_lshlrev_b32_e32 v64, 16, v31
	v_and_b32_e32 v65, 0xffff0000, v31
	v_lshlrev_b32_e32 v33, 16, v44
	v_and_b32_e32 v31, 0xffff0000, v44
	v_lshlrev_b32_e32 v114, 16, v50
	v_lshlrev_b32_e32 v116, 16, v51
	s_waitcnt vmcnt(12)
	v_and_b32_e32 v77, 0xffff0000, v53
	v_and_b32_e32 v76, 0xffff0000, v52
	s_waitcnt vmcnt(11)
	v_and_b32_e32 v73, 0xffff0000, v55
	v_mul_f32_e32 v30, v117, v117
	v_mul_f32_e32 v32, v115, v115
	v_lshlrev_b32_e32 v75, 16, v53
	v_lshlrev_b32_e32 v74, 16, v52
	v_lshlrev_b32_e32 v70, 16, v54
	v_and_b32_e32 v71, 0xffff0000, v54
	v_lshlrev_b32_e32 v72, 16, v55
	v_pk_mul_f32 v[54:55], v[76:77], v[76:77]
	v_mul_f32_e32 v62, v73, v73
	v_pk_fma_f32 v[120:121], v[116:117], v[116:117], v[30:31] op_sel_hi:[1,1,0]
	v_pk_fma_f32 v[122:123], v[114:115], v[114:115], v[32:33] op_sel_hi:[1,1,0]
	s_waitcnt vmcnt(8)
	v_lshlrev_b32_e32 v50, 16, v110
	v_and_b32_e32 v51, 0xffff0000, v110
	v_lshlrev_b32_e32 v52, 16, v111
	v_and_b32_e32 v53, 0xffff0000, v111
	v_mov_b32_e32 v111, v63
	v_mul_f32_e32 v60, v71, v71
	v_pk_fma_f32 v[54:55], v[74:75], v[74:75], v[54:55]
	v_pk_fma_f32 v[126:127], v[72:73], v[72:73], v[62:63] op_sel_hi:[1,1,0]
	v_mov_b32_e32 v62, v122
	v_mov_b32_e32 v110, v120
	v_mul_f32_e32 v128, v61, v61
	v_mul_f32_e32 v129, v64, v64
	v_mul_f32_e32 v130, v65, v65
	v_pk_fma_f32 v[124:125], v[70:71], v[70:71], v[60:61] op_sel_hi:[1,1,0]
	v_pk_add_f32 v[120:121], v[122:123], v[120:121]
	v_pk_add_f32 v[54:55], v[54:55], v[54:55] op_sel:[0,1] op_sel_hi:[1,0]
	v_pk_mul_f32 v[110:111], v[62:63], v[110:111]
	v_and_b32_e32 v69, 0xffff0000, v57
	v_and_b32_e32 v68, 0xffff0000, v56
	v_mov_b32_e32 v125, v129
	v_mov_b32_e32 v127, v130
	v_mov_b32_e32 v55, v128
	v_mov_b32_e32 v121, v111
	v_lshlrev_b32_e32 v67, 16, v57
	v_lshlrev_b32_e32 v66, 16, v56
	v_pk_mul_f32 v[112:113], v[68:69], v[68:69]
	v_pk_add_f32 v[122:123], v[124:125], v[126:127]
	v_pk_add_f32 v[54:55], v[120:121], v[54:55]
	v_pk_fma_f32 v[112:113], v[66:67], v[66:67], v[112:113]
	v_pk_add_f32 v[54:55], v[54:55], v[122:123]
	v_lshlrev_b32_e32 v57, 16, v59
	v_lshlrev_b32_e32 v56, 16, v58
	v_and_b32_e32 v59, 0xffff0000, v59
	v_and_b32_e32 v58, 0xffff0000, v58
	v_pk_add_f32 v[112:113], v[112:113], v[112:113] op_sel:[0,1] op_sel_hi:[1,0]
	v_pk_add_f32 v[54:55], v[54:55], v[54:55] op_sel:[0,1] op_sel_hi:[1,0]
	v_pk_mul_f32 v[118:119], v[58:59], v[58:59]
	v_mov_b32_e32 v32, v54
	v_mov_b32_e32 v110, v112
	v_mov_b32_e32 v111, v33
	v_pk_fma_f32 v[118:119], v[56:57], v[56:57], v[118:119]
	v_pk_add_f32 v[54:55], v[54:55], v[112:113]
	v_pk_mul_f32 v[110:111], v[32:33], v[110:111]
	v_mul_f32_e32 v131, v31, v31
	v_mov_b32_e32 v55, v111
	v_pk_add_f32 v[110:111], v[118:119], v[118:119] op_sel:[0,1] op_sel_hi:[1,0]
	v_mul_f32_e32 v30, v51, v51
	v_mov_b32_e32 v111, v131
	v_lshlrev_b32_e32 v44, 16, v45
	v_and_b32_e32 v45, 0xffff0000, v45
	v_pk_add_f32 v[54:55], v[54:55], v[110:111]
	v_pk_fma_f32 v[110:111], v[50:51], v[50:51], v[30:31] op_sel_hi:[1,1,0]
	v_mul_f32_e32 v30, v53, v53
	v_mul_f32_e32 v60, v44, v44
	v_mul_f32_e32 v62, v45, v45
	v_pk_fma_f32 v[112:113], v[52:53], v[52:53], v[30:31] op_sel_hi:[1,1,0]
	v_mov_b32_e32 v111, v60
	v_mov_b32_e32 v113, v62
	v_pk_add_f32 v[110:111], v[110:111], v[112:113]
	v_lshlrev_b32_e32 v62, 1, v34
	v_pk_add_f32 v[54:55], v[54:55], v[110:111]
	ds_read_b128 v[110:113], v78
	v_add_f32_e32 v30, v54, v55
	s_nop 1
	v_add_f32_dpp v30, v30, v30 quad_perm:[1,0,3,2] row_mask:0xf bank_mask:0xf bound_ctrl:1
	s_nop 1
	v_add_f32_dpp v30, v30, v30 quad_perm:[2,3,0,1] row_mask:0xf bank_mask:0xf bound_ctrl:1
	s_nop 1
	v_add_f32_dpp v30, v30, v30 row_ror:4 row_mask:0xf bank_mask:0xf bound_ctrl:1
	s_nop 1
	v_add_f32_dpp v30, v30, v30 row_ror:8 row_mask:0xf bank_mask:0xf bound_ctrl:1
	s_nop 0
	v_readlane_b32 s20, v30, 16
	v_readlane_b32 s21, v30, 48
	v_readlane_b32 s2, v30, 0
	v_readlane_b32 s3, v30, 32
	v_mov_b32_e32 v54, s20
	v_mov_b32_e32 v55, s21
	v_pk_add_f32 v[54:55], s[2:3], v[54:55]
	s_lshl_b64 s[2:3], s[90:91], 12
	v_add_f32_e32 v30, v54, v55
	v_fmamk_f32 v30, v30, 0x3a000000, v106
	v_rsq_f32_e32 v54, v30
	s_add_u32 s20, s84, s2
	s_addc_u32 s21, s26, s3
	s_and_b64 vcc, exec, s[18:19]
	v_pk_mul_f32 v[116:117], v[54:55], v[116:117] op_sel_hi:[0,1]
	v_pk_mul_f32 v[114:115], v[54:55], v[114:115] op_sel_hi:[0,1]
	s_waitcnt vmcnt(7) lgkmcnt(0)
	v_pk_fma_f32 v[46:47], v[110:111], v[114:115], v[46:47]
	v_pk_fma_f32 v[48:49], v[112:113], v[116:117], v[48:49]
	s_cbranch_vccz .LBB0_792
	v_cvt_pk_bf16_f32 v110, v46, v47
	v_cvt_pk_bf16_f32 v111, v48, v49
	global_store_dwordx2 v62, v[110:111], s[20:21] sc1
; #define LAS __attribute__((address_space(3)))
; __device__ __forceinline__ void st_bf4(bf16_t* p, f32x4 v) { u32x2 w; w.x = pg8::cvt_pk_bf16(v.x, v.y); w.y = pg8::cvt_pk_bf16(v.z, v.w); *(u32x2*)p = w; }
; template <bool FAST>
; __device__ __forceinline__ void p7_route_t(Frame& F, const bool do_route) {
;     ...
;         for (int j = 0; j < 8; ++j) { const int c = 4 * F.lane + 256 * j;
;             const f32x4 gg = FAST ? *(const LAS f32x4*)(pvec + c) : *(const f32x4*)(IN_NORMG + D + c) * *(const f32x4*)(mr + 2 * D + c);
;             v[j] = xv[j] + gg * (v[j] * rstd);
;             if (valid) st_bf4(X1 + (size_t)row * D + c, v[j]);
;             ss += (v[j].x * v[j].x + v[j].y * v[j].y) + (v[j].z * v[j].z + v[j].w * v[j].w); }
.LBB0_792:
	ds_read_b128 v[110:113], v79
	v_mov_b32_e32 v55, v54
	v_mov_b32_e32 v114, v75
	v_mov_b32_e32 v115, v77
	v_mov_b32_e32 v116, v54
	v_mov_b32_e32 v117, v54
	v_mov_b32_e32 v75, v76
	v_pk_mul_f32 v[114:115], v[116:117], v[114:115]
	v_pk_mul_f32 v[74:75], v[54:55], v[74:75]
	s_lshl_b64 s[16:17], s[16:17], 11
	s_waitcnt vmcnt(6) lgkmcnt(0)
	v_pk_fma_f32 v[28:29], v[114:115], v[112:113], v[28:29]
	v_pk_fma_f32 v[26:27], v[74:75], v[110:111], v[26:27]
	s_and_b64 vcc, exec, s[18:19]
	s_cbranch_vccz .LBB0_794
	v_cvt_pk_bf16_f32 v74, v26, v27
	v_cvt_pk_bf16_f32 v75, v28, v29
	global_store_dwordx2 v62, v[74:75], s[20:21] offset:512 sc1
.LBB0_794:
	ds_read_b128 v[74:77], v80
	v_mov_b32_e32 v110, v54
	v_mov_b32_e32 v111, v54
	v_pk_mul_f32 v[70:71], v[54:55], v[70:71]
	v_pk_mul_f32 v[72:73], v[110:111], v[72:73]
	s_waitcnt vmcnt(5) lgkmcnt(0)
	v_pk_fma_f32 v[22:23], v[70:71], v[74:75], v[22:23]
	v_pk_fma_f32 v[24:25], v[72:73], v[76:77], v[24:25]
	s_and_b64 vcc, exec, s[18:19]
	s_cbranch_vccz .LBB0_796
	v_cvt_pk_bf16_f32 v70, v22, v23
	v_cvt_pk_bf16_f32 v71, v24, v25
	global_store_dwordx2 v62, v[70:71], s[20:21] offset:1024 sc1
.LBB0_796:
	ds_read_b128 v[70:73], v81
	v_mov_b32_e32 v74, v54
	v_mov_b32_e32 v75, v54
	v_mov_b32_e32 v60, v63
	v_pk_mul_f32 v[64:65], v[74:75], v[64:65]
	v_pk_mul_f32 v[60:61], v[54:55], v[60:61]
	s_waitcnt vmcnt(4) lgkmcnt(0)
	v_pk_fma_f32 v[20:21], v[64:65], v[72:73], v[20:21]
	v_pk_fma_f32 v[18:19], v[60:61], v[70:71], v[18:19]
	s_and_b64 vcc, exec, s[18:19]
	s_cbranch_vccz .LBB0_798
	v_cvt_pk_bf16_f32 v60, v18, v19
	v_cvt_pk_bf16_f32 v61, v20, v21
	global_store_dwordx2 v62, v[60:61], s[20:21] offset:1536 sc1
.LBB0_798:
	ds_read_b128 v[70:73], v82
	v_mov_b32_e32 v60, v67
	v_mov_b32_e32 v61, v69
	v_mov_b32_e32 v64, v54
	v_mov_b32_e32 v65, v54
	v_mov_b32_e32 v67, v68
	v_pk_mul_f32 v[60:61], v[64:65], v[60:61]
	v_pk_mul_f32 v[64:65], v[54:55], v[66:67]
	s_waitcnt vmcnt(3) lgkmcnt(0)
	v_pk_fma_f32 v[16:17], v[60:61], v[72:73], v[16:17]
	v_pk_fma_f32 v[14:15], v[64:65], v[70:71], v[14:15]
	s_and_b64 vcc, exec, s[18:19]
	s_cbranch_vccz .LBB0_800
	v_cvt_pk_bf16_f32 v60, v14, v15
	v_cvt_pk_bf16_f32 v61, v16, v17
	global_store_dwordx2 v62, v[60:61], s[20:21] offset:2048 sc1
.LBB0_800:
	ds_read_b128 v[64:67], v83
	v_mov_b32_e32 v60, v57
	v_mov_b32_e32 v61, v59
	v_mov_b32_e32 v68, v54
	v_mov_b32_e32 v69, v54
	v_mov_b32_e32 v57, v58
	v_pk_mul_f32 v[60:61], v[68:69], v[60:61]
	v_pk_mul_f32 v[56:57], v[54:55], v[56:57]
	s_waitcnt vmcnt(2) lgkmcnt(0)
	v_pk_fma_f32 v[12:13], v[60:61], v[66:67], v[12:13]
	v_pk_fma_f32 v[10:11], v[56:57], v[64:65], v[10:11]
	s_and_b64 vcc, exec, s[18:19]
	s_cbranch_vccz .LBB0_802
	v_cvt_pk_bf16_f32 v56, v10, v11
	v_cvt_pk_bf16_f32 v57, v12, v13
	global_store_dwordx2 v62, v[56:57], s[20:21] offset:2560 sc1
.LBB0_802:
	ds_read_b128 v[56:59], v84
	v_mov_b32_e32 v60, v54
	v_mov_b32_e32 v61, v54
	v_pk_mul_f32 v[50:51], v[54:55], v[50:51]
	v_pk_mul_f32 v[52:53], v[60:61], v[52:53]
	s_waitcnt vmcnt(1) lgkmcnt(0)
	v_pk_fma_f32 v[6:7], v[50:51], v[56:57], v[6:7]
	v_pk_fma_f32 v[8:9], v[52:53], v[58:59], v[8:9]
	s_and_b64 vcc, exec, s[18:19]
	s_cbranch_vccz .LBB0_804
	v_cvt_pk_bf16_f32 v50, v6, v7
	v_cvt_pk_bf16_f32 v51, v8, v9
	global_store_dwordx2 v62, v[50:51], s[20:21] offset:3072 sc1
.LBB0_804:
	ds_read_b128 v[50:53], v85
	v_mov_b32_e32 v56, v54
	v_mov_b32_e32 v57, v54
	v_mov_b32_e32 v30, v33
	v_pk_mul_f32 v[44:45], v[56:57], v[44:45]
	v_pk_mul_f32 v[32:33], v[54:55], v[30:31]
	s_waitcnt vmcnt(0) lgkmcnt(0)
	v_pk_fma_f32 v[30:31], v[44:45], v[52:53], v[4:5]
	v_pk_fma_f32 v[32:33], v[32:33], v[50:51], v[2:3]
	s_mov_b64 s[2:3], -1
	s_and_b64 vcc, exec, s[18:19]
	s_cbranch_vccz .LBB0_806
	v_cvt_pk_bf16_f32 v2, v32, v33
	v_cvt_pk_bf16_f32 v3, v30, v31
	global_store_dwordx2 v62, v[2:3], s[20:21] offset:3584 sc1
	s_mov_b64 s[2:3], 0
	v_mov_b32_e32 v3, v32
	v_mov_b32_e32 v2, v30
	v_mov_b32_e32 v5, v33
	v_mov_b32_e32 v4, v31

; #define LAS __attribute__((address_space(3)))
; __device__ __forceinline__ unsigned pk4_fp8(float a, float b, float c, float d) { int w = 0; w = __builtin_amdgcn_cvt_pk_fp8_f32(a, b, w, false); w = __builtin_amdgcn_cvt_pk_fp8_f32(c, d, w, true); return (unsigned)w; }
; template <bool FAST>
; __device__ __forceinline__ void p7_route_t(Frame& F, const bool do_route) {
;     ...
;             ss += (v[j].x * v[j].x + v[j].y * v[j].y) + (v[j].z * v[j].z + v[j].w * v[j].w); }
;         rstd = __builtin_amdgcn_rsqf(wave_sum(ss) * (1.0f / D) + RMS_EPS);
; #pragma unroll
;         for (int j = 0; j < 8; ++j) { const int c = 4 * F.lane + 256 * j;
;             const f32x4 gs = FAST ? *(const LAS f32x4*)(pvec + D + c) : *(const f32x4*)(IN_NORMG + 2 * D + c) * (*(const f32x4*)(mr + 4 * D + c) + 1.0f);
;             const f32x4 sh = FAST ? *(const LAS f32x4*)(pvec + 2 * D + c) : *(const f32x4*)(mr + 3 * D + c);
;             const f32x4 hv = (v[j] * rstd) * gs + sh;
;             if (valid) *(unsigned*)(H2 + (size_t)row * D + c) = pg8::pk4_fp8(hv.x, hv.y, hv.z, hv.w);
;             *(LAS f32x4*)(hbuf + F.wave * D + c) = hv; }
.LBB0_808:
	v_mul_f32_e32 v44, v46, v46
	v_mul_f32_e32 v45, v48, v48
	v_fmac_f32_e32 v44, v47, v47
	v_fmac_f32_e32 v45, v49, v49
	v_add_f32_e32 v44, v45, v44
	v_mul_f32_e32 v45, v26, v26
	v_mul_f32_e32 v50, v28, v28
	v_fmac_f32_e32 v45, v27, v27
	v_fmac_f32_e32 v50, v29, v29
	v_add_f32_e32 v45, v50, v45
	v_add_f32_e32 v44, v44, v45
	v_mul_f32_e32 v45, v22, v22
	v_mul_f32_e32 v50, v24, v24
	v_fmac_f32_e32 v45, v23, v23
	v_fmac_f32_e32 v50, v25, v25
	v_add_f32_e32 v45, v50, v45
	v_add_f32_e32 v44, v44, v45
	v_mul_f32_e32 v45, v18, v18
	v_mul_f32_e32 v50, v20, v20
	v_fmac_f32_e32 v45, v19, v19
	v_fmac_f32_e32 v50, v21, v21
	v_add_f32_e32 v45, v50, v45
	v_add_f32_e32 v44, v44, v45
	v_mul_f32_e32 v45, v14, v14
	v_mul_f32_e32 v50, v16, v16
	v_fmac_f32_e32 v45, v15, v15
	v_fmac_f32_e32 v50, v17, v17
	v_add_f32_e32 v45, v50, v45
	v_add_f32_e32 v44, v44, v45
	v_mul_f32_e32 v45, v10, v10
	v_mul_f32_e32 v50, v12, v12
	v_fmac_f32_e32 v45, v11, v11
	v_fmac_f32_e32 v50, v13, v13
	v_add_f32_e32 v45, v50, v45
	v_add_f32_e32 v44, v44, v45
	v_mul_f32_e32 v45, v6, v6
	v_mul_f32_e32 v50, v8, v8
	v_fmac_f32_e32 v45, v7, v7
	v_fmac_f32_e32 v50, v9, v9
	v_pk_mul_f32 v[2:3], v[2:3], v[2:3]
	v_add_f32_e32 v45, v50, v45
	v_pk_fma_f32 v[2:3], v[4:5], v[4:5], v[2:3]
	v_add_f32_e32 v44, v44, v45
	v_add_f32_e32 v2, v2, v3
	v_add_f32_e32 v2, v44, v2
	s_nop 1
	v_add_f32_dpp v2, v2, v2 quad_perm:[1,0,3,2] row_mask:0xf bank_mask:0xf bound_ctrl:1
	s_nop 1
	v_add_f32_dpp v2, v2, v2 quad_perm:[2,3,0,1] row_mask:0xf bank_mask:0xf bound_ctrl:1
	s_nop 1
	v_add_f32_dpp v2, v2, v2 row_ror:4 row_mask:0xf bank_mask:0xf bound_ctrl:1
	s_nop 1
	v_add_f32_dpp v2, v2, v2 row_ror:8 row_mask:0xf bank_mask:0xf bound_ctrl:1
	s_nop 0
	v_readlane_b32 s20, v2, 16
	v_readlane_b32 s21, v2, 48
	v_readlane_b32 s2, v2, 0
	v_readlane_b32 s3, v2, 32
	v_mov_b32_e32 v2, s20
	v_mov_b32_e32 v3, s21
	v_pk_add_f32 v[2:3], s[2:3], v[2:3]
	s_add_u32 s2, s88, s16
	v_add_f32_e32 v2, v2, v3
	v_fmamk_f32 v2, v2, 0x3a000000, v106
	v_rsq_f32_e32 v44, v2
	ds_read_b128 v[2:5], v86
	ds_read_b128 v[50:53], v87
	s_addc_u32 s3, s89, s17
	s_andn2_b64 vcc, exec, s[18:19]
	v_pk_mul_f32 v[46:47], v[46:47], v[44:45] op_sel_hi:[1,0]
	v_pk_mul_f32 v[48:49], v[48:49], v[44:45] op_sel_hi:[1,0]
	v_cndmask_b32_e64 v45, 0, 1, s[18:19]
	s_waitcnt lgkmcnt(0)
	v_pk_fma_f32 v[4:5], v[4:5], v[48:49], v[52:53]
	v_pk_fma_f32 v[2:3], v[2:3], v[46:47], v[50:51]
	v_cmp_ne_u32_e64 s[16:17], 1, v45
	v_lshl_add_u64 v[46:47], s[2:3], 0, v[34:35]
	s_cbranch_vccnz .LBB0_810
	v_mov_b32_e32 v45, 0
	v_cvt_pk_fp8_f32 v45, v2, v3
	v_cvt_pk_fp8_f32 v45, v4, v5 op_sel:[0,0,1]
	global_store_dword v[46:47], v45, off sc1
.LBB0_810:
	ds_write_b128 v88, v[2:5] offset:1024
	ds_read_b128 v[2:5], v89
	ds_read_b128 v[50:53], v90
	v_mov_b32_e32 v45, v44
	v_mov_b32_e32 v48, v44
	v_mov_b32_e32 v49, v44
	v_pk_mul_f32 v[28:29], v[28:29], v[48:49]
	v_pk_mul_f32 v[26:27], v[26:27], v[44:45]
	s_waitcnt lgkmcnt(0)
	v_pk_fma_f32 v[4:5], v[28:29], v[4:5], v[52:53]
	s_and_b64 vcc, exec, s[16:17]
	v_pk_fma_f32 v[2:3], v[26:27], v[2:3], v[50:51]
	s_cbranch_vccnz .LBB0_812
	v_mov_b32_e32 v26, 0
	v_cvt_pk_fp8_f32 v26, v2, v3
	v_cvt_pk_fp8_f32 v26, v4, v5 op_sel:[0,0,1]
	global_store_dword v[46:47], v26, off offset:256 sc1
.LBB0_812:
	ds_read_b128 v[26:29], v91
	ds_read_b128 v[50:53], v92
	ds_write_b128 v88, v[2:5] offset:2048
	v_pk_mul_f32 v[2:3], v[24:25], v[48:49]
	v_pk_mul_f32 v[22:23], v[22:23], v[44:45]
	s_and_b64 vcc, exec, s[16:17]
	s_waitcnt lgkmcnt(1)
	v_pk_fma_f32 v[4:5], v[2:3], v[28:29], v[52:53]
	v_pk_fma_f32 v[2:3], v[22:23], v[26:27], v[50:51]
	s_cbranch_vccnz .LBB0_814
	v_mov_b32_e32 v22, 0
	v_cvt_pk_fp8_f32 v22, v2, v3
	v_cvt_pk_fp8_f32 v22, v4, v5 op_sel:[0,0,1]
	global_store_dword v[46:47], v22, off offset:512 sc1
.LBB0_814:
	ds_write_b128 v88, v[2:5] offset:3072
	ds_read_b128 v[2:5], v93
	ds_read_b128 v[24:27], v94
	v_mov_b32_e32 v22, v44
	v_mov_b32_e32 v23, v44
	v_pk_mul_f32 v[20:21], v[20:21], v[22:23]
	v_pk_mul_f32 v[18:19], v[18:19], v[44:45]
	s_waitcnt lgkmcnt(0)
	v_pk_fma_f32 v[4:5], v[20:21], v[4:5], v[26:27]
	s_and_b64 vcc, exec, s[16:17]
	v_pk_fma_f32 v[2:3], v[18:19], v[2:3], v[24:25]
	s_cbranch_vccnz .LBB0_816
	v_mov_b32_e32 v18, 0
	v_cvt_pk_fp8_f32 v18, v2, v3
	v_cvt_pk_fp8_f32 v18, v4, v5 op_sel:[0,0,1]
	global_store_dword v[46:47], v18, off offset:768 sc1
.LBB0_816:
	ds_read_b128 v[18:21], v95
	ds_read_b128 v[24:27], v96
	ds_write_b128 v88, v[2:5] offset:4096
	v_pk_mul_f32 v[2:3], v[16:17], v[22:23]
	v_pk_mul_f32 v[14:15], v[14:15], v[44:45]
	s_and_b64 vcc, exec, s[16:17]
	s_waitcnt lgkmcnt(1)
	v_pk_fma_f32 v[4:5], v[2:3], v[20:21], v[26:27]
	v_pk_fma_f32 v[2:3], v[14:15], v[18:19], v[24:25]
	s_cbranch_vccnz .LBB0_818
	v_mov_b32_e32 v14, 0
	v_cvt_pk_fp8_f32 v14, v2, v3
	v_cvt_pk_fp8_f32 v14, v4, v5 op_sel:[0,0,1]
	global_store_dword v[46:47], v14, off offset:1024 sc1
.LBB0_818:
	ds_write_b128 v88, v[2:5] offset:5120
	ds_read_b128 v[2:5], v97
	ds_read_b128 v[16:19], v98
	v_mov_b32_e32 v14, v44
	v_mov_b32_e32 v15, v44
	v_pk_mul_f32 v[12:13], v[12:13], v[14:15]
	v_pk_mul_f32 v[10:11], v[10:11], v[44:45]
	s_waitcnt lgkmcnt(0)
	v_pk_fma_f32 v[4:5], v[12:13], v[4:5], v[18:19]
	s_and_b64 vcc, exec, s[16:17]
	v_pk_fma_f32 v[2:3], v[10:11], v[2:3], v[16:17]
	s_cbranch_vccnz .LBB0_820
	v_mov_b32_e32 v10, 0
	v_cvt_pk_fp8_f32 v10, v2, v3
	v_cvt_pk_fp8_f32 v10, v4, v5 op_sel:[0,0,1]
	global_store_dword v[46:47], v10, off offset:1280 sc1
.LBB0_820:
	ds_read_b128 v[10:13], v99
	ds_read_b128 v[16:19], v100
	ds_write_b128 v88, v[2:5] offset:6144
	v_pk_mul_f32 v[2:3], v[8:9], v[14:15]
	v_pk_mul_f32 v[6:7], v[6:7], v[44:45]
	s_and_b64 vcc, exec, s[16:17]
	s_waitcnt lgkmcnt(1)
	v_pk_fma_f32 v[4:5], v[2:3], v[12:13], v[18:19]
	v_pk_fma_f32 v[2:3], v[6:7], v[10:11], v[16:17]
	s_cbranch_vccnz .LBB0_822
	v_mov_b32_e32 v6, 0
	v_cvt_pk_fp8_f32 v6, v2, v3
	v_cvt_pk_fp8_f32 v6, v4, v5 op_sel:[0,0,1]
	global_store_dword v[46:47], v6, off offset:1536 sc1
.LBB0_822:
	ds_write_b128 v88, v[2:5] offset:7168
	ds_read_b128 v[2:5], v101
	ds_read_b128 v[6:9], v102
	v_mov_b32_e32 v10, v44
	v_mov_b32_e32 v11, v44
	v_pk_mul_f32 v[10:11], v[30:31], v[10:11]
	v_pk_mul_f32 v[12:13], v[32:33], v[44:45]
	s_waitcnt lgkmcnt(0)
	v_pk_fma_f32 v[4:5], v[10:11], v[4:5], v[8:9]
	s_and_b64 vcc, exec, s[16:17]
	v_pk_fma_f32 v[2:3], v[12:13], v[2:3], v[6:7]
	s_cbranch_vccnz .LBB0_824
	v_mov_b32_e32 v6, 0
	v_cvt_pk_fp8_f32 v6, v2, v3
	v_cvt_pk_fp8_f32 v6, v4, v5 op_sel:[0,0,1]
	global_store_dword v[46:47], v6, off offset:1792 sc1

; #define LAS __attribute__((address_space(3)))
; template <bool FAST>
; __device__ __forceinline__ void p7_route_t(Frame& F, const bool do_route) {
;     ...
;         __syncthreads();
;         float lg[NE];
; #pragma unroll
;         for (int e4 = 0; e4 < NE / 4; ++e4) { const f32x4 t = *(const LAS f32x4*)(lgb + F.wave * 32 + 4 * e4); lg[4 * e4] = t.x; lg[4 * e4 + 1] = t.y; lg[4 * e4 + 2] = t.z; lg[4 * e4 + 3] = t.w; }
;         unsigned taken = 0u; int es[TOPK]; float vs[TOPK];
; #pragma unroll
;         for (int k = 0; k < TOPK; ++k) { float best = -3.0e38f; int bi = 0;
; #pragma unroll
;             for (int e = 0; e < NE; ++e) { const bool ok = !((taken >> e) & 1u) && lg[e] > best; best = ok ? lg[e] : best; bi = ok ? e : bi; }
;             taken |= 1u << bi; es[k] = bi; vs[k] = best; }
.LBB0_832:
	s_or_b64 exec, exec, s[2:3]
	s_nor_b64 s[0:1], s[0:1], s[4:5]
	s_waitcnt lgkmcnt(0)
	s_barrier
	s_and_saveexec_b64 s[28:29], s[0:1]
	s_cbranch_execz .LBB0_789
	v_readlane_b32 s0, v254, 42
	s_nop 1
	v_mov_b32_e32 v18, s0
	ds_read_b128 v[2:5], v18 offset:112
	ds_read_b128 v[6:9], v18 offset:96
	ds_read_b128 v[30:33], v18
	ds_read_b128 v[10:13], v18 offset:80
	ds_read_b128 v[14:17], v18 offset:64
	ds_read_b128 v[26:29], v18 offset:16
	ds_read_b128 v[22:25], v18 offset:32
	ds_read_b128 v[18:21], v18 offset:48
	s_waitcnt lgkmcnt(5)
	v_max_f32_e32 v44, v30, v30
	s_mov_b32 s0, 0xff61b1e6
	v_max_f32_e32 v44, 0xff61b1e6, v44
	v_cmp_lt_f32_e32 vcc, s0, v30
	v_cmp_gt_f32_e64 s[0:1], v31, v44
	s_nop 1
	v_cndmask_b32_e64 v44, v44, v31, s[0:1]
	v_cmp_gt_f32_e64 s[16:17], v32, v44
	v_cndmask_b32_e64 v46, 0, 1, s[0:1]
	s_and_b64 s[0:1], s[16:17], exec
	v_cndmask_b32_e64 v44, v44, v32, s[16:17]
	v_cmp_gt_f32_e64 s[18:19], v33, v44
	v_readfirstlane_b32 s0, v46
	s_cselect_b32 s2, 2, s0
	v_cndmask_b32_e64 v44, v44, v33, s[18:19]
	s_waitcnt lgkmcnt(2)
	v_cmp_gt_f32_e64 s[20:21], v26, v44
	s_and_b64 s[0:1], s[18:19], exec
	s_cselect_b32 s2, 3, s2
	v_cndmask_b32_e64 v44, v44, v26, s[20:21]
	v_cmp_gt_f32_e64 s[22:23], v27, v44
	s_and_b64 s[0:1], s[20:21], exec
	s_cselect_b32 s2, 4, s2
	v_cndmask_b32_e64 v44, v44, v27, s[22:23]
	v_cmp_gt_f32_e64 s[24:25], v28, v44
	s_and_b64 s[0:1], s[22:23], exec
	s_cselect_b32 s2, 5, s2
	v_cndmask_b32_e64 v44, v44, v28, s[24:25]
	v_cmp_gt_f32_e64 s[30:31], v29, v44
	s_and_b64 s[0:1], s[24:25], exec
	s_cselect_b32 s2, 6, s2
	v_cndmask_b32_e64 v44, v44, v29, s[30:31]
	s_waitcnt lgkmcnt(1)
	v_cmp_gt_f32_e64 s[34:35], v22, v44
	s_and_b64 s[0:1], s[30:31], exec
	s_cselect_b32 s2, 7, s2
	v_cndmask_b32_e64 v44, v44, v22, s[34:35]
	v_cmp_gt_f32_e64 s[36:37], v23, v44
	s_and_b64 s[0:1], s[34:35], exec
	s_cselect_b32 s2, 8, s2
	v_cndmask_b32_e64 v44, v44, v23, s[36:37]
	v_cmp_gt_f32_e64 s[38:39], v24, v44
	s_and_b64 s[0:1], s[36:37], exec
	s_cselect_b32 s2, 9, s2
	v_cndmask_b32_e64 v44, v44, v24, s[38:39]
	v_cmp_gt_f32_e64 s[40:41], v25, v44
	s_and_b64 s[0:1], s[38:39], exec
	s_cselect_b32 s2, 10, s2
	v_cndmask_b32_e64 v44, v44, v25, s[40:41]
	s_waitcnt lgkmcnt(0)
	v_cmp_gt_f32_e64 s[42:43], v18, v44
	s_and_b64 s[0:1], s[40:41], exec
	s_cselect_b32 s2, 11, s2
	v_cndmask_b32_e64 v44, v44, v18, s[42:43]
	v_cmp_gt_f32_e64 s[44:45], v19, v44
	s_and_b64 s[0:1], s[42:43], exec
	s_cselect_b32 s2, 12, s2
	v_cndmask_b32_e64 v44, v44, v19, s[44:45]
	v_cmp_gt_f32_e64 s[46:47], v20, v44
	s_and_b64 s[0:1], s[44:45], exec
	s_cselect_b32 s2, 13, s2
	v_cndmask_b32_e64 v44, v44, v20, s[46:47]
	v_cmp_gt_f32_e64 s[48:49], v21, v44
	s_and_b64 s[0:1], s[46:47], exec
	s_cselect_b32 s2, 14, s2
	v_cndmask_b32_e64 v44, v44, v21, s[48:49]
	v_cmp_gt_f32_e64 s[50:51], v14, v44
	s_and_b64 s[0:1], s[48:49], exec
	s_cselect_b32 s2, 15, s2
	v_cndmask_b32_e64 v44, v44, v14, s[50:51]
	v_cmp_gt_f32_e64 s[52:53], v15, v44
	s_and_b64 s[0:1], s[50:51], exec
	s_cselect_b32 s2, 16, s2
	v_cndmask_b32_e64 v44, v44, v15, s[52:53]
	v_cmp_gt_f32_e64 s[54:55], v16, v44
	s_and_b64 s[0:1], s[52:53], exec
	s_cselect_b32 s2, 17, s2
	v_cndmask_b32_e64 v44, v44, v16, s[54:55]
	v_cmp_gt_f32_e64 s[56:57], v17, v44
	s_and_b64 s[0:1], s[54:55], exec
	s_cselect_b32 s2, 18, s2
	v_cndmask_b32_e64 v44, v44, v17, s[56:57]
	v_cmp_gt_f32_e64 s[58:59], v10, v44
	s_and_b64 s[0:1], s[56:57], exec
	s_cselect_b32 s2, 19, s2
	v_cndmask_b32_e64 v44, v44, v10, s[58:59]
	v_cmp_gt_f32_e64 s[60:61], v11, v44
	s_and_b64 s[0:1], s[58:59], exec
	s_cselect_b32 s2, 20, s2
	v_cndmask_b32_e64 v44, v44, v11, s[60:61]
	v_cmp_gt_f32_e64 s[62:63], v12, v44
	s_and_b64 s[0:1], s[60:61], exec
	s_cselect_b32 s2, 21, s2
	v_cndmask_b32_e64 v44, v44, v12, s[62:63]
	v_cmp_gt_f32_e64 s[64:65], v13, v44
	s_and_b64 s[0:1], s[62:63], exec
	s_cselect_b32 s2, 22, s2
	v_cndmask_b32_e64 v44, v44, v13, s[64:65]
	v_cmp_gt_f32_e64 s[66:67], v6, v44
	s_and_b64 s[0:1], s[64:65], exec
	s_cselect_b32 s2, 23, s2
	v_cndmask_b32_e64 v44, v44, v6, s[66:67]
	v_cmp_gt_f32_e64 s[68:69], v7, v44
	s_and_b64 s[0:1], s[66:67], exec
	s_cselect_b32 s2, 24, s2
	v_cndmask_b32_e64 v44, v44, v7, s[68:69]
	v_cmp_gt_f32_e64 s[70:71], v8, v44
	s_and_b64 s[0:1], s[68:69], exec
	s_cselect_b32 s2, 25, s2
	v_cndmask_b32_e64 v44, v44, v8, s[70:71]
	v_cmp_gt_f32_e64 s[72:73], v9, v44
	s_and_b64 s[0:1], s[70:71], exec
	s_cselect_b32 s2, 26, s2
	v_cndmask_b32_e64 v44, v44, v9, s[72:73]
	v_cmp_gt_f32_e64 s[74:75], v2, v44
	s_and_b64 s[0:1], s[72:73], exec
	s_cselect_b32 s2, 27, s2
	v_cndmask_b32_e64 v44, v44, v2, s[74:75]
	v_cmp_gt_f32_e64 s[76:77], v3, v44
	s_and_b64 s[0:1], s[74:75], exec
	s_cselect_b32 s2, 28, s2
	v_cndmask_b32_e64 v44, v44, v3, s[76:77]
	v_cmp_gt_f32_e64 s[78:79], v4, v44
	s_and_b64 s[0:1], s[76:77], exec
	s_cselect_b32 s2, 29, s2
	v_cndmask_b32_e64 v44, v44, v4, s[78:79]
	v_cmp_gt_f32_e64 s[80:81], v5, v44
	s_and_b64 s[0:1], s[78:79], exec
	s_cselect_b32 s2, 30, s2
	s_and_b64 s[0:1], s[80:81], exec
	s_cselect_b32 s91, 31, s2
	s_cmp_lg_u32 s91, 31
	s_cselect_b64 s[2:3], -1, 0
	s_lshl_b32 s95, 1, s91
	s_bitcmp0_b32 s95, 30
	v_cndmask_b32_e64 v45, v44, v5, s[80:81]
	s_cselect_b64 s[80:81], -1, 0
	s_bitcmp0_b32 s95, 29
	s_cselect_b64 s[78:79], -1, 0
	s_bitcmp0_b32 s95, 28
	s_cselect_b64 s[76:77], -1, 0
	s_bitcmp0_b32 s95, 27
	s_cselect_b64 s[74:75], -1, 0
	s_bitcmp0_b32 s95, 26
	s_cselect_b64 s[72:73], -1, 0
	s_bitcmp0_b32 s95, 25
	s_cselect_b64 s[70:71], -1, 0
	s_bitcmp0_b32 s95, 24
	s_cselect_b64 s[68:69], -1, 0
	s_bitcmp0_b32 s95, 23
	s_cselect_b64 s[66:67], -1, 0
	s_bitcmp0_b32 s95, 22
	s_cselect_b64 s[64:65], -1, 0
	s_bitcmp0_b32 s95, 21
; template <bool FAST>
; __device__ __forceinline__ void p7_route_t(Frame& F, const bool do_route) {
;     ...
;         unsigned taken = 0u; int es[TOPK]; float vs[TOPK];
; #pragma unroll
;         for (int k = 0; k < TOPK; ++k) { float best = -3.0e38f; int bi = 0;
; #pragma unroll
;             for (int e = 0; e < NE; ++e) { const bool ok = !((taken >> e) & 1u) && lg[e] > best; best = ok ? lg[e] : best; bi = ok ? e : bi; }
;             taken |= 1u << bi; es[k] = bi; vs[k] = best; }
;         float ps[TOPK], psum = 0.f;
; #pragma unroll
;         for (int k = 0; k < TOPK; ++k) { ps[k] = __expf(vs[k] - vs[0]); psum += ps[k]; }
	s_cselect_b64 s[62:63], -1, 0
	s_bitcmp0_b32 s95, 20
	s_cselect_b64 s[60:61], -1, 0
	s_bitcmp0_b32 s95, 19
	s_cselect_b64 s[58:59], -1, 0
	s_bitcmp0_b32 s95, 18
	s_cselect_b64 s[56:57], -1, 0
	s_bitcmp0_b32 s95, 17
	s_cselect_b64 s[54:55], -1, 0
	s_bitcmp0_b32 s95, 16
	s_cselect_b64 s[52:53], -1, 0
	s_bitcmp0_b32 s95, 15
	s_cselect_b64 s[50:51], -1, 0
	s_bitcmp0_b32 s95, 14
	s_cselect_b64 s[48:49], -1, 0
	s_bitcmp0_b32 s95, 13
	s_cselect_b64 s[46:47], -1, 0
	s_bitcmp0_b32 s95, 12
	s_cselect_b64 s[44:45], -1, 0
	s_bitcmp0_b32 s95, 11
	s_cselect_b64 s[42:43], -1, 0
	s_bitcmp0_b32 s95, 10
	s_cselect_b64 s[40:41], -1, 0
	s_bitcmp0_b32 s95, 9
	s_cselect_b64 s[38:39], -1, 0
	s_bitcmp0_b32 s95, 8
	s_cselect_b64 s[36:37], -1, 0
	s_bitcmp0_b32 s95, 7
	s_cselect_b64 s[34:35], -1, 0
	s_bitcmp0_b32 s95, 6
	s_cselect_b64 s[30:31], -1, 0
	s_bitcmp0_b32 s95, 5
	s_cselect_b64 s[24:25], -1, 0
	s_bitcmp0_b32 s95, 4
	s_cselect_b64 s[22:23], -1, 0
	s_bitcmp0_b32 s95, 3
	s_cselect_b64 s[20:21], -1, 0
	s_bitcmp0_b32 s95, 2
	s_cselect_b64 s[18:19], -1, 0
	s_bitcmp0_b32 s95, 1
	s_cselect_b64 s[16:17], -1, 0
	s_cmp_lg_u32 s91, 0
	s_cselect_b64 s[0:1], -1, 0
	s_and_b64 s[0:1], s[0:1], vcc
	v_cndmask_b32_e64 v46, v108, v30, s[0:1]
	v_cmp_gt_f32_e64 s[0:1], v31, v46
	s_and_b64 s[0:1], s[16:17], s[0:1]
	v_sub_f32_e32 v44, v45, v45
	v_cndmask_b32_e64 v46, v46, v31, s[0:1]
	v_cmp_gt_f32_e64 s[16:17], v32, v46
	s_and_b64 s[16:17], s[18:19], s[16:17]
	v_cndmask_b32_e64 v47, 0, 1, s[0:1]
	v_cndmask_b32_e64 v46, v46, v32, s[16:17]
	v_cmp_gt_f32_e64 s[18:19], v33, v46
	s_and_b64 s[18:19], s[20:21], s[18:19]
	v_mul_f32_e32 v44, 0x3fb8aa3b, v44
	v_cndmask_b32_e64 v46, v46, v33, s[18:19]
	v_cmp_gt_f32_e64 s[20:21], v26, v46
	s_and_b64 s[20:21], s[22:23], s[20:21]
	v_exp_f32_e32 v44, v44
	v_cndmask_b32_e64 v46, v46, v26, s[20:21]
	v_cmp_gt_f32_e64 s[22:23], v27, v46
	s_and_b64 s[22:23], s[24:25], s[22:23]
	s_nop 0
	v_cndmask_b32_e64 v46, v46, v27, s[22:23]
	v_cmp_gt_f32_e64 s[24:25], v28, v46
	s_and_b64 s[24:25], s[30:31], s[24:25]
	s_nop 0
	v_cndmask_b32_e64 v46, v46, v28, s[24:25]
	v_cmp_gt_f32_e64 s[30:31], v29, v46
	s_and_b64 s[30:31], s[34:35], s[30:31]
	s_nop 0
	v_cndmask_b32_e64 v46, v46, v29, s[30:31]
	v_cmp_gt_f32_e64 s[34:35], v22, v46
	s_and_b64 s[34:35], s[36:37], s[34:35]
	s_nop 0
	v_cndmask_b32_e64 v46, v46, v22, s[34:35]
	v_cmp_gt_f32_e64 s[36:37], v23, v46
	s_and_b64 s[36:37], s[38:39], s[36:37]
	s_nop 0
	v_cndmask_b32_e64 v46, v46, v23, s[36:37]
	v_cmp_gt_f32_e64 s[38:39], v24, v46
	s_and_b64 s[38:39], s[40:41], s[38:39]
	s_nop 0
	v_cndmask_b32_e64 v46, v46, v24, s[38:39]
	v_cmp_gt_f32_e64 s[40:41], v25, v46
	s_and_b64 s[40:41], s[42:43], s[40:41]
	s_nop 0
	v_cndmask_b32_e64 v46, v46, v25, s[40:41]
	v_cmp_gt_f32_e64 s[42:43], v18, v46
	s_and_b64 s[42:43], s[44:45], s[42:43]
	s_nop 0
	v_cndmask_b32_e64 v46, v46, v18, s[42:43]
	v_cmp_gt_f32_e64 s[44:45], v19, v46
	s_and_b64 s[44:45], s[46:47], s[44:45]
	s_nop 0
	v_cndmask_b32_e64 v46, v46, v19, s[44:45]
	v_cmp_gt_f32_e64 s[46:47], v20, v46
	s_and_b64 s[46:47], s[48:49], s[46:47]
	s_nop 0
	v_cndmask_b32_e64 v46, v46, v20, s[46:47]
	v_cmp_gt_f32_e64 s[48:49], v21, v46
	s_and_b64 s[48:49], s[50:51], s[48:49]
	s_nop 0
	v_cndmask_b32_e64 v46, v46, v21, s[48:49]
	v_cmp_gt_f32_e64 s[50:51], v14, v46
	s_and_b64 s[50:51], s[52:53], s[50:51]
	s_nop 0
	v_cndmask_b32_e64 v46, v46, v14, s[50:51]
	v_cmp_gt_f32_e64 s[52:53], v15, v46
	s_and_b64 s[52:53], s[54:55], s[52:53]
	s_nop 0
	v_cndmask_b32_e64 v46, v46, v15, s[52:53]
	v_cmp_gt_f32_e64 s[54:55], v16, v46
	s_and_b64 s[54:55], s[56:57], s[54:55]
	s_nop 0
	v_cndmask_b32_e64 v46, v46, v16, s[54:55]
	v_cmp_gt_f32_e64 s[56:57], v17, v46
	s_and_b64 s[56:57], s[58:59], s[56:57]
	s_nop 0
	v_cndmask_b32_e64 v46, v46, v17, s[56:57]
	v_cmp_gt_f32_e64 s[58:59], v10, v46
	s_and_b64 s[58:59], s[60:61], s[58:59]
	s_nop 0
	v_cndmask_b32_e64 v46, v46, v10, s[58:59]
	v_cmp_gt_f32_e64 s[60:61], v11, v46
	s_and_b64 s[60:61], s[62:63], s[60:61]
	s_nop 0
	v_cndmask_b32_e64 v46, v46, v11, s[60:61]
	v_cmp_gt_f32_e64 s[62:63], v12, v46
	s_and_b64 s[62:63], s[64:65], s[62:63]
	s_nop 0
	v_cndmask_b32_e64 v46, v46, v12, s[62:63]
	v_cmp_gt_f32_e64 s[64:65], v13, v46
	s_and_b64 s[64:65], s[66:67], s[64:65]
	s_nop 0
	v_cndmask_b32_e64 v46, v46, v13, s[64:65]
	v_cmp_gt_f32_e64 s[66:67], v6, v46
	s_and_b64 s[66:67], s[68:69], s[66:67]
	s_nop 0
	v_cndmask_b32_e64 v46, v46, v6, s[66:67]
	v_cmp_gt_f32_e64 s[68:69], v7, v46
	s_and_b64 s[68:69], s[70:71], s[68:69]
	s_nop 0
	v_cndmask_b32_e64 v46, v46, v7, s[68:69]
	v_cmp_gt_f32_e64 s[70:71], v8, v46
	s_and_b64 s[70:71], s[72:73], s[70:71]
	s_nop 0
	v_cndmask_b32_e64 v46, v46, v8, s[70:71]
	v_cmp_gt_f32_e64 s[72:73], v9, v46
	s_and_b64 s[72:73], s[74:75], s[72:73]
	s_nop 0
	v_cndmask_b32_e64 v46, v46, v9, s[72:73]
	v_cmp_gt_f32_e64 s[74:75], v2, v46
	s_and_b64 s[74:75], s[76:77], s[74:75]
	s_nop 0
	v_cndmask_b32_e64 v46, v46, v2, s[74:75]
	v_cmp_gt_f32_e64 s[76:77], v3, v46
	s_and_b64 s[76:77], s[78:79], s[76:77]
	s_nop 0
	v_cndmask_b32_e64 v46, v46, v3, s[76:77]
	v_cmp_gt_f32_e64 s[78:79], v4, v46
	s_and_b64 s[78:79], s[80:81], s[78:79]
	s_nop 0
	v_cndmask_b32_e64 v46, v46, v4, s[78:79]
	v_cmp_gt_f32_e64 s[80:81], v5, v46
	s_and_b64 s[80:81], s[2:3], s[80:81]
	s_and_b64 s[0:1], s[16:17], exec
	v_readfirstlane_b32 s0, v47
	s_cselect_b32 s2, 2, s0
	s_and_b64 s[0:1], s[18:19], exec
	s_cselect_b32 s2, 3, s2
	s_and_b64 s[0:1], s[20:21], exec
	s_cselect_b32 s2, 4, s2
	s_and_b64 s[0:1], s[22:23], exec
	s_cselect_b32 s2, 5, s2
	s_and_b64 s[0:1], s[24:25], exec
	s_cselect_b32 s2, 6, s2
	s_and_b64 s[0:1], s[30:31], exec
	s_cselect_b32 s2, 7, s2
	s_and_b64 s[0:1], s[34:35], exec
; template <bool FAST>
; __device__ __forceinline__ void p7_route_t(Frame& F, const bool do_route) {
;     ...
;         unsigned taken = 0u; int es[TOPK]; float vs[TOPK];
; #pragma unroll
;         for (int k = 0; k < TOPK; ++k) { float best = -3.0e38f; int bi = 0;
; #pragma unroll
;             for (int e = 0; e < NE; ++e) { const bool ok = !((taken >> e) & 1u) && lg[e] > best; best = ok ? lg[e] : best; bi = ok ? e : bi; }
;             taken |= 1u << bi; es[k] = bi; vs[k] = best; }
;         float ps[TOPK], psum = 0.f;
; #pragma unroll
;         for (int k = 0; k < TOPK; ++k) { ps[k] = __expf(vs[k] - vs[0]); psum += ps[k]; }
	s_cselect_b32 s2, 8, s2
	s_and_b64 s[0:1], s[36:37], exec
	s_cselect_b32 s2, 9, s2
	s_and_b64 s[0:1], s[38:39], exec
	s_cselect_b32 s2, 10, s2
	s_and_b64 s[0:1], s[40:41], exec
	s_cselect_b32 s2, 11, s2
	s_and_b64 s[0:1], s[42:43], exec
	s_cselect_b32 s2, 12, s2
	s_and_b64 s[0:1], s[44:45], exec
	s_cselect_b32 s2, 13, s2
	s_and_b64 s[0:1], s[46:47], exec
	s_cselect_b32 s2, 14, s2
	s_and_b64 s[0:1], s[48:49], exec
	s_cselect_b32 s2, 15, s2
	s_and_b64 s[0:1], s[50:51], exec
	s_cselect_b32 s2, 16, s2
	s_and_b64 s[0:1], s[52:53], exec
	s_cselect_b32 s2, 17, s2
	s_and_b64 s[0:1], s[54:55], exec
	s_cselect_b32 s2, 18, s2
	s_and_b64 s[0:1], s[56:57], exec
	s_cselect_b32 s2, 19, s2
	s_and_b64 s[0:1], s[58:59], exec
	s_cselect_b32 s2, 20, s2
	s_and_b64 s[0:1], s[60:61], exec
	s_cselect_b32 s2, 21, s2
	s_and_b64 s[0:1], s[62:63], exec
	s_cselect_b32 s2, 22, s2
	s_and_b64 s[0:1], s[64:65], exec
	s_cselect_b32 s2, 23, s2
	s_and_b64 s[0:1], s[66:67], exec
	s_cselect_b32 s2, 24, s2
	s_and_b64 s[0:1], s[68:69], exec
	s_cselect_b32 s2, 25, s2
	s_and_b64 s[0:1], s[70:71], exec
	s_cselect_b32 s2, 26, s2
	s_and_b64 s[0:1], s[72:73], exec
	s_cselect_b32 s2, 27, s2
	s_and_b64 s[0:1], s[74:75], exec
	s_cselect_b32 s2, 28, s2
	s_and_b64 s[0:1], s[76:77], exec
	s_cselect_b32 s2, 29, s2
	s_and_b64 s[0:1], s[78:79], exec
	s_cselect_b32 s2, 30, s2
	s_and_b64 s[0:1], s[80:81], exec
	s_cselect_b32 s94, 31, s2
	s_lshl_b32 s0, 1, s94
	s_or_b32 s95, s0, s95
	s_cmp_gt_i32 s95, -1
	s_cselect_b64 s[2:3], -1, 0
	s_bitcmp0_b32 s95, 30
	v_cndmask_b32_e64 v46, v46, v5, s[80:81]
	s_cselect_b64 s[80:81], -1, 0
	s_bitcmp0_b32 s95, 29
	s_cselect_b64 s[78:79], -1, 0
	s_bitcmp0_b32 s95, 28
	s_cselect_b64 s[76:77], -1, 0
	s_bitcmp0_b32 s95, 27
	s_cselect_b64 s[74:75], -1, 0
	s_bitcmp0_b32 s95, 26
	s_cselect_b64 s[72:73], -1, 0
	s_bitcmp0_b32 s95, 25
	s_cselect_b64 s[70:71], -1, 0
	s_bitcmp0_b32 s95, 24
	s_cselect_b64 s[68:69], -1, 0
	s_bitcmp0_b32 s95, 23
	s_cselect_b64 s[66:67], -1, 0
	s_bitcmp0_b32 s95, 22
	s_cselect_b64 s[64:65], -1, 0
	s_bitcmp0_b32 s95, 21
	s_cselect_b64 s[62:63], -1, 0
	s_bitcmp0_b32 s95, 20
	s_cselect_b64 s[60:61], -1, 0
	s_bitcmp0_b32 s95, 19
	s_cselect_b64 s[58:59], -1, 0
	s_bitcmp0_b32 s95, 18
	s_cselect_b64 s[56:57], -1, 0
	s_bitcmp0_b32 s95, 17
	s_cselect_b64 s[54:55], -1, 0
	s_bitcmp0_b32 s95, 16
	s_cselect_b64 s[52:53], -1, 0
	s_bitcmp0_b32 s95, 15
	s_cselect_b64 s[50:51], -1, 0
	s_bitcmp0_b32 s95, 14
	s_cselect_b64 s[48:49], -1, 0
	s_bitcmp0_b32 s95, 13
	s_cselect_b64 s[46:47], -1, 0
	s_bitcmp0_b32 s95, 12
	s_cselect_b64 s[44:45], -1, 0
	s_bitcmp0_b32 s95, 11
	s_cselect_b64 s[42:43], -1, 0
	s_bitcmp0_b32 s95, 10
	s_cselect_b64 s[40:41], -1, 0
	s_bitcmp0_b32 s95, 9
	s_cselect_b64 s[38:39], -1, 0
	s_bitcmp0_b32 s95, 8
	s_cselect_b64 s[36:37], -1, 0
	s_bitcmp0_b32 s95, 7
	s_cselect_b64 s[34:35], -1, 0
	s_bitcmp0_b32 s95, 6
	s_cselect_b64 s[30:31], -1, 0
	s_bitcmp0_b32 s95, 5
	s_cselect_b64 s[24:25], -1, 0
	s_bitcmp0_b32 s95, 4
	s_cselect_b64 s[22:23], -1, 0
	s_bitcmp0_b32 s95, 3
	s_cselect_b64 s[20:21], -1, 0
	s_bitcmp0_b32 s95, 2
	s_cselect_b64 s[18:19], -1, 0
	s_bitcmp0_b32 s95, 1
	s_cselect_b64 s[16:17], -1, 0
	s_bitcmp0_b32 s95, 0
	s_cselect_b64 s[0:1], -1, 0
	s_and_b64 s[0:1], s[0:1], vcc
	v_cndmask_b32_e64 v47, v108, v30, s[0:1]
	v_cmp_gt_f32_e64 s[0:1], v31, v47
	s_and_b64 s[0:1], s[16:17], s[0:1]
	v_sub_f32_e32 v46, v46, v45
	v_cndmask_b32_e64 v47, v47, v31, s[0:1]
	v_cmp_gt_f32_e64 s[16:17], v32, v47
	s_and_b64 s[16:17], s[18:19], s[16:17]
	v_cndmask_b32_e64 v48, 0, 1, s[0:1]
	v_cndmask_b32_e64 v47, v47, v32, s[16:17]
	v_cmp_gt_f32_e64 s[18:19], v33, v47
	s_and_b64 s[18:19], s[20:21], s[18:19]
	v_mul_f32_e32 v46, 0x3fb8aa3b, v46
	v_cndmask_b32_e64 v47, v47, v33, s[18:19]
	v_cmp_gt_f32_e64 s[20:21], v26, v47
	s_and_b64 s[20:21], s[22:23], s[20:21]
	v_exp_f32_e32 v46, v46
	v_cndmask_b32_e64 v47, v47, v26, s[20:21]
	v_cmp_gt_f32_e64 s[22:23], v27, v47
	s_and_b64 s[22:23], s[24:25], s[22:23]
	s_nop 0
	v_cndmask_b32_e64 v47, v47, v27, s[22:23]
	v_cmp_gt_f32_e64 s[24:25], v28, v47
	s_and_b64 s[24:25], s[30:31], s[24:25]
	s_nop 0
	v_cndmask_b32_e64 v47, v47, v28, s[24:25]
	v_cmp_gt_f32_e64 s[30:31], v29, v47
	s_and_b64 s[30:31], s[34:35], s[30:31]
	s_nop 0
	v_cndmask_b32_e64 v47, v47, v29, s[30:31]
	v_cmp_gt_f32_e64 s[34:35], v22, v47
	s_and_b64 s[34:35], s[36:37], s[34:35]
	s_nop 0
	v_cndmask_b32_e64 v47, v47, v22, s[34:35]
	v_cmp_gt_f32_e64 s[36:37], v23, v47
	s_and_b64 s[36:37], s[38:39], s[36:37]
	s_nop 0
	v_cndmask_b32_e64 v47, v47, v23, s[36:37]
	v_cmp_gt_f32_e64 s[38:39], v24, v47
	s_and_b64 s[38:39], s[40:41], s[38:39]
	s_nop 0
	v_cndmask_b32_e64 v47, v47, v24, s[38:39]
	v_cmp_gt_f32_e64 s[40:41], v25, v47
	s_and_b64 s[40:41], s[42:43], s[40:41]
	s_nop 0
	v_cndmask_b32_e64 v47, v47, v25, s[40:41]
	v_cmp_gt_f32_e64 s[42:43], v18, v47
	s_and_b64 s[42:43], s[44:45], s[42:43]
	s_nop 0
	v_cndmask_b32_e64 v47, v47, v18, s[42:43]
	v_cmp_gt_f32_e64 s[44:45], v19, v47
	s_and_b64 s[44:45], s[46:47], s[44:45]
	s_nop 0
	v_cndmask_b32_e64 v47, v47, v19, s[44:45]
	v_cmp_gt_f32_e64 s[46:47], v20, v47
	s_and_b64 s[46:47], s[48:49], s[46:47]
	s_nop 0
	v_cndmask_b32_e64 v47, v47, v20, s[46:47]
	v_cmp_gt_f32_e64 s[48:49], v21, v47
	s_and_b64 s[48:49], s[50:51], s[48:49]
	s_nop 0
	v_cndmask_b32_e64 v47, v47, v21, s[48:49]
	v_cmp_gt_f32_e64 s[50:51], v14, v47
	s_and_b64 s[50:51], s[52:53], s[50:51]
	s_nop 0
	v_cndmask_b32_e64 v47, v47, v14, s[50:51]
	v_cmp_gt_f32_e64 s[52:53], v15, v47
	s_and_b64 s[52:53], s[54:55], s[52:53]
	s_nop 0
	v_cndmask_b32_e64 v47, v47, v15, s[52:53]
	v_cmp_gt_f32_e64 s[54:55], v16, v47
	s_and_b64 s[54:55], s[56:57], s[54:55]
	s_nop 0
; template <bool FAST>
; __device__ __forceinline__ void p7_route_t(Frame& F, const bool do_route) {
;     ...
;         unsigned taken = 0u; int es[TOPK]; float vs[TOPK];
; #pragma unroll
;         for (int k = 0; k < TOPK; ++k) { float best = -3.0e38f; int bi = 0;
; #pragma unroll
;             for (int e = 0; e < NE; ++e) { const bool ok = !((taken >> e) & 1u) && lg[e] > best; best = ok ? lg[e] : best; bi = ok ? e : bi; }
;             taken |= 1u << bi; es[k] = bi; vs[k] = best; }
;         float ps[TOPK], psum = 0.f;
; #pragma unroll
;         for (int k = 0; k < TOPK; ++k) { ps[k] = __expf(vs[k] - vs[0]); psum += ps[k]; }
	v_cndmask_b32_e64 v47, v47, v16, s[54:55]
	v_cmp_gt_f32_e64 s[56:57], v17, v47
	s_and_b64 s[56:57], s[58:59], s[56:57]
	s_nop 0
	v_cndmask_b32_e64 v47, v47, v17, s[56:57]
	v_cmp_gt_f32_e64 s[58:59], v10, v47
	s_and_b64 s[58:59], s[60:61], s[58:59]
	s_nop 0
	v_cndmask_b32_e64 v47, v47, v10, s[58:59]
	v_cmp_gt_f32_e64 s[60:61], v11, v47
	s_and_b64 s[60:61], s[62:63], s[60:61]
	s_nop 0
	v_cndmask_b32_e64 v47, v47, v11, s[60:61]
	v_cmp_gt_f32_e64 s[62:63], v12, v47
	s_and_b64 s[62:63], s[64:65], s[62:63]
	s_nop 0
	v_cndmask_b32_e64 v47, v47, v12, s[62:63]
	v_cmp_gt_f32_e64 s[64:65], v13, v47
	s_and_b64 s[64:65], s[66:67], s[64:65]
	s_nop 0
	v_cndmask_b32_e64 v47, v47, v13, s[64:65]
	v_cmp_gt_f32_e64 s[66:67], v6, v47
	s_and_b64 s[66:67], s[68:69], s[66:67]
	s_nop 0
	v_cndmask_b32_e64 v47, v47, v6, s[66:67]
	v_cmp_gt_f32_e64 s[68:69], v7, v47
	s_and_b64 s[68:69], s[70:71], s[68:69]
	s_nop 0
	v_cndmask_b32_e64 v47, v47, v7, s[68:69]
	v_cmp_gt_f32_e64 s[70:71], v8, v47
	s_and_b64 s[70:71], s[72:73], s[70:71]
	s_nop 0
	v_cndmask_b32_e64 v47, v47, v8, s[70:71]
	v_cmp_gt_f32_e64 s[72:73], v9, v47
	s_and_b64 s[72:73], s[74:75], s[72:73]
	s_nop 0
	v_cndmask_b32_e64 v47, v47, v9, s[72:73]
	v_cmp_gt_f32_e64 s[74:75], v2, v47
	s_and_b64 s[74:75], s[76:77], s[74:75]
	s_nop 0
	v_cndmask_b32_e64 v47, v47, v2, s[74:75]
	v_cmp_gt_f32_e64 s[76:77], v3, v47
	s_and_b64 s[76:77], s[78:79], s[76:77]
	s_nop 0
	v_cndmask_b32_e64 v47, v47, v3, s[76:77]
	v_cmp_gt_f32_e64 s[78:79], v4, v47
	s_and_b64 s[78:79], s[80:81], s[78:79]
	s_nop 0
	v_cndmask_b32_e64 v47, v47, v4, s[78:79]
	v_cmp_gt_f32_e64 s[80:81], v5, v47
	s_and_b64 s[80:81], s[2:3], s[80:81]
	s_and_b64 s[0:1], s[16:17], exec
	v_readfirstlane_b32 s0, v48
	s_cselect_b32 s2, 2, s0
	s_and_b64 s[0:1], s[18:19], exec
	s_cselect_b32 s2, 3, s2
	s_and_b64 s[0:1], s[20:21], exec
	s_cselect_b32 s2, 4, s2
	s_and_b64 s[0:1], s[22:23], exec
	s_cselect_b32 s2, 5, s2
	s_and_b64 s[0:1], s[24:25], exec
	s_cselect_b32 s2, 6, s2
	s_and_b64 s[0:1], s[30:31], exec
	s_cselect_b32 s2, 7, s2
	s_and_b64 s[0:1], s[34:35], exec
	s_cselect_b32 s2, 8, s2
	s_and_b64 s[0:1], s[36:37], exec
	s_cselect_b32 s2, 9, s2
	s_and_b64 s[0:1], s[38:39], exec
	s_cselect_b32 s2, 10, s2
	s_and_b64 s[0:1], s[40:41], exec
	s_cselect_b32 s2, 11, s2
	s_and_b64 s[0:1], s[42:43], exec
	s_cselect_b32 s2, 12, s2
	s_and_b64 s[0:1], s[44:45], exec
	s_cselect_b32 s2, 13, s2
	s_and_b64 s[0:1], s[46:47], exec
	s_cselect_b32 s2, 14, s2
	s_and_b64 s[0:1], s[48:49], exec
	s_cselect_b32 s2, 15, s2
	s_and_b64 s[0:1], s[50:51], exec
	s_cselect_b32 s2, 16, s2
	s_and_b64 s[0:1], s[52:53], exec
	s_cselect_b32 s2, 17, s2
	s_and_b64 s[0:1], s[54:55], exec
	s_cselect_b32 s2, 18, s2
	s_and_b64 s[0:1], s[56:57], exec
	s_cselect_b32 s2, 19, s2
	s_and_b64 s[0:1], s[58:59], exec
	s_cselect_b32 s2, 20, s2
	s_and_b64 s[0:1], s[60:61], exec
	s_cselect_b32 s2, 21, s2
	s_and_b64 s[0:1], s[62:63], exec
	s_cselect_b32 s2, 22, s2
	s_and_b64 s[0:1], s[64:65], exec
	s_cselect_b32 s2, 23, s2
	s_and_b64 s[0:1], s[66:67], exec
	s_cselect_b32 s2, 24, s2
	s_and_b64 s[0:1], s[68:69], exec
	s_cselect_b32 s2, 25, s2
	s_and_b64 s[0:1], s[70:71], exec
	s_cselect_b32 s2, 26, s2
	s_and_b64 s[0:1], s[72:73], exec
	s_cselect_b32 s2, 27, s2
	s_and_b64 s[0:1], s[74:75], exec
	s_cselect_b32 s2, 28, s2
	s_and_b64 s[0:1], s[76:77], exec
	s_cselect_b32 s2, 29, s2
	s_and_b64 s[0:1], s[78:79], exec
	s_cselect_b32 s2, 30, s2
	s_and_b64 s[0:1], s[80:81], exec
	v_cndmask_b32_e64 v47, v47, v5, s[80:81]
	s_cselect_b32 s80, 31, s2
	s_lshl_b32 s0, 1, s80
	s_mov_b32 s81, s26
	s_or_b32 s26, s0, s95
	s_cmp_gt_i32 s26, -1
	s_cselect_b64 s[2:3], -1, 0
	s_bitcmp0_b32 s26, 30
	s_cselect_b64 s[78:79], -1, 0
	s_bitcmp0_b32 s26, 29
	s_cselect_b64 s[76:77], -1, 0
	s_bitcmp0_b32 s26, 28
	s_cselect_b64 s[74:75], -1, 0
	s_bitcmp0_b32 s26, 27
	s_cselect_b64 s[72:73], -1, 0
	s_bitcmp0_b32 s26, 26
	s_cselect_b64 s[70:71], -1, 0
	s_bitcmp0_b32 s26, 25
	s_cselect_b64 s[68:69], -1, 0
	s_bitcmp0_b32 s26, 24
	s_cselect_b64 s[66:67], -1, 0
	s_bitcmp0_b32 s26, 23
	s_cselect_b64 s[64:65], -1, 0
	s_bitcmp0_b32 s26, 22
	s_cselect_b64 s[62:63], -1, 0
	s_bitcmp0_b32 s26, 21
	s_cselect_b64 s[60:61], -1, 0
	s_bitcmp0_b32 s26, 20
	s_cselect_b64 s[58:59], -1, 0
	s_bitcmp0_b32 s26, 19
	s_cselect_b64 s[56:57], -1, 0
	s_bitcmp0_b32 s26, 18
	s_cselect_b64 s[54:55], -1, 0
	s_bitcmp0_b32 s26, 17
	s_cselect_b64 s[52:53], -1, 0
	s_bitcmp0_b32 s26, 16
	s_cselect_b64 s[50:51], -1, 0
	s_bitcmp0_b32 s26, 15
	s_cselect_b64 s[48:49], -1, 0
	s_bitcmp0_b32 s26, 14
	s_cselect_b64 s[46:47], -1, 0
	s_bitcmp0_b32 s26, 13
	s_cselect_b64 s[44:45], -1, 0
	s_bitcmp0_b32 s26, 12
	s_cselect_b64 s[42:43], -1, 0
	s_bitcmp0_b32 s26, 11
	s_cselect_b64 s[40:41], -1, 0
	s_bitcmp0_b32 s26, 10
	s_cselect_b64 s[38:39], -1, 0
	s_bitcmp0_b32 s26, 9
	s_cselect_b64 s[36:37], -1, 0
	s_bitcmp0_b32 s26, 8
	s_cselect_b64 s[34:35], -1, 0
	s_bitcmp0_b32 s26, 7
	s_cselect_b64 s[30:31], -1, 0
	s_bitcmp0_b32 s26, 6
	s_cselect_b64 s[24:25], -1, 0
	s_bitcmp0_b32 s26, 5
	s_cselect_b64 s[22:23], -1, 0
	s_bitcmp0_b32 s26, 4
	s_cselect_b64 s[20:21], -1, 0
	s_bitcmp0_b32 s26, 3
	s_cselect_b64 s[18:19], -1, 0
	s_bitcmp0_b32 s26, 2
	s_cselect_b64 s[16:17], -1, 0
	s_bitcmp0_b32 s26, 1
	s_cselect_b64 s[0:1], -1, 0
	s_bitcmp0_b32 s26, 0
	s_cselect_b64 s[26:27], -1, 0
	s_and_b64 vcc, s[26:27], vcc
	v_cndmask_b32_e32 v30, v108, v30, vcc
	v_cmp_gt_f32_e32 vcc, v31, v30
	s_and_b64 vcc, s[0:1], vcc
	v_sub_f32_e32 v47, v47, v45
	v_cndmask_b32_e32 v30, v30, v31, vcc
	v_cmp_gt_f32_e64 s[0:1], v32, v30
	s_and_b64 s[0:1], s[16:17], s[0:1]
	v_mul_f32_e32 v47, 0x3fb8aa3b, v47
	v_cndmask_b32_e64 v30, v30, v32, s[0:1]
; template <bool FAST>
; __device__ __forceinline__ void p7_route_t(Frame& F, const bool do_route) {
;     ...
;         unsigned taken = 0u; int es[TOPK]; float vs[TOPK];
; #pragma unroll
;         for (int k = 0; k < TOPK; ++k) { float best = -3.0e38f; int bi = 0;
; #pragma unroll
;             for (int e = 0; e < NE; ++e) { const bool ok = !((taken >> e) & 1u) && lg[e] > best; best = ok ? lg[e] : best; bi = ok ? e : bi; }
;             taken |= 1u << bi; es[k] = bi; vs[k] = best; }
;         float ps[TOPK], psum = 0.f;
; #pragma unroll
;         for (int k = 0; k < TOPK; ++k) { ps[k] = __expf(vs[k] - vs[0]); psum += ps[k]; }
;         if (do_route && valid && F.lane < TOPK) {
;             const int k = F.lane; const int e = k == 0 ? es[0] : k == 1 ? es[1] : k == 2 ? es[2] : es[3]; const float p = k == 0 ? ps[0] : k == 1 ? ps[1] : k == 2 ? ps[2] : ps[3];
;             const int lr = (int)__hip_atomic_fetch_add(lcnt + e, 1u, __ATOMIC_RELAXED, __HIP_MEMORY_SCOPE_WORKGROUP);
;             tok_e[row * TOPK + k] = e; tok_rank[row * TOPK + k] = lr; tok_gate[row * TOPK + k] = p / psum;
;         }
	v_cmp_gt_f32_e64 s[16:17], v33, v30
	s_and_b64 s[16:17], s[18:19], s[16:17]
	v_exp_f32_e32 v47, v47
	v_cndmask_b32_e64 v30, v30, v33, s[16:17]
	v_cmp_gt_f32_e64 s[18:19], v26, v30
	s_and_b64 s[18:19], s[20:21], s[18:19]
	s_mov_b32 s26, s81
	v_cndmask_b32_e64 v26, v30, v26, s[18:19]
	v_cmp_gt_f32_e64 s[20:21], v27, v26
	s_and_b64 s[20:21], s[22:23], s[20:21]
	s_nop 0
	v_cndmask_b32_e64 v26, v26, v27, s[20:21]
	v_cmp_gt_f32_e64 s[22:23], v28, v26
	s_and_b64 s[22:23], s[24:25], s[22:23]
	s_nop 0
	v_cndmask_b32_e64 v26, v26, v28, s[22:23]
	v_cmp_gt_f32_e64 s[24:25], v29, v26
	s_and_b64 s[24:25], s[30:31], s[24:25]
	s_nop 0
	v_cndmask_b32_e64 v26, v26, v29, s[24:25]
	v_cmp_gt_f32_e64 s[30:31], v22, v26
	s_and_b64 s[30:31], s[34:35], s[30:31]
	s_nop 0
	v_cndmask_b32_e64 v22, v26, v22, s[30:31]
	v_cmp_gt_f32_e64 s[34:35], v23, v22
	s_and_b64 s[34:35], s[36:37], s[34:35]
	s_nop 0
	v_cndmask_b32_e64 v22, v22, v23, s[34:35]
	v_cmp_gt_f32_e64 s[36:37], v24, v22
	s_and_b64 s[36:37], s[38:39], s[36:37]
	s_nop 0
	v_cndmask_b32_e64 v22, v22, v24, s[36:37]
	v_cmp_gt_f32_e64 s[38:39], v25, v22
	s_and_b64 s[38:39], s[40:41], s[38:39]
	s_nop 0
	v_cndmask_b32_e64 v22, v22, v25, s[38:39]
	v_cmp_gt_f32_e64 s[40:41], v18, v22
	s_and_b64 s[40:41], s[42:43], s[40:41]
	s_nop 0
	v_cndmask_b32_e64 v18, v22, v18, s[40:41]
	v_cmp_gt_f32_e64 s[42:43], v19, v18
	s_and_b64 s[42:43], s[44:45], s[42:43]
	s_nop 0
	v_cndmask_b32_e64 v18, v18, v19, s[42:43]
	v_cmp_gt_f32_e64 s[44:45], v20, v18
	s_and_b64 s[44:45], s[46:47], s[44:45]
	s_nop 0
	v_cndmask_b32_e64 v18, v18, v20, s[44:45]
	v_cmp_gt_f32_e64 s[46:47], v21, v18
	s_and_b64 s[46:47], s[48:49], s[46:47]
	s_nop 0
	v_cndmask_b32_e64 v18, v18, v21, s[46:47]
	v_cmp_gt_f32_e64 s[48:49], v14, v18
	s_and_b64 s[48:49], s[50:51], s[48:49]
	s_nop 0
	v_cndmask_b32_e64 v14, v18, v14, s[48:49]
	v_cmp_gt_f32_e64 s[50:51], v15, v14
	s_and_b64 s[50:51], s[52:53], s[50:51]
	s_nop 0
	v_cndmask_b32_e64 v14, v14, v15, s[50:51]
	v_cmp_gt_f32_e64 s[52:53], v16, v14
	s_and_b64 s[52:53], s[54:55], s[52:53]
	s_nop 0
	v_cndmask_b32_e64 v14, v14, v16, s[52:53]
	v_cmp_gt_f32_e64 s[54:55], v17, v14
	s_and_b64 s[54:55], s[56:57], s[54:55]
	s_nop 0
	v_cndmask_b32_e64 v14, v14, v17, s[54:55]
	v_cmp_gt_f32_e64 s[56:57], v10, v14
	s_and_b64 s[56:57], s[58:59], s[56:57]
	s_nop 0
	v_cndmask_b32_e64 v10, v14, v10, s[56:57]
	v_cmp_gt_f32_e64 s[58:59], v11, v10
	s_and_b64 s[58:59], s[60:61], s[58:59]
	s_nop 0
	v_cndmask_b32_e64 v10, v10, v11, s[58:59]
	v_cmp_gt_f32_e64 s[60:61], v12, v10
	s_and_b64 s[60:61], s[62:63], s[60:61]
	s_nop 0
	v_cndmask_b32_e64 v10, v10, v12, s[60:61]
	v_cmp_gt_f32_e64 s[62:63], v13, v10
	s_and_b64 s[62:63], s[64:65], s[62:63]
	s_nop 0
	v_cndmask_b32_e64 v10, v10, v13, s[62:63]
	v_cmp_gt_f32_e64 s[64:65], v6, v10
	s_and_b64 s[64:65], s[66:67], s[64:65]
	s_nop 0
	v_cndmask_b32_e64 v6, v10, v6, s[64:65]
	v_cmp_gt_f32_e64 s[66:67], v7, v6
	s_and_b64 s[66:67], s[68:69], s[66:67]
	s_nop 0
	v_cndmask_b32_e64 v6, v6, v7, s[66:67]
	v_cmp_gt_f32_e64 s[68:69], v8, v6
	s_and_b64 s[68:69], s[70:71], s[68:69]
	s_nop 0
	v_cndmask_b32_e64 v6, v6, v8, s[68:69]
	v_cmp_gt_f32_e64 s[70:71], v9, v6
	s_and_b64 s[70:71], s[72:73], s[70:71]
	s_nop 0
	v_cndmask_b32_e64 v6, v6, v9, s[70:71]
	v_cmp_gt_f32_e64 s[72:73], v2, v6
	s_and_b64 s[72:73], s[74:75], s[72:73]
	s_nop 0
	v_cndmask_b32_e64 v2, v6, v2, s[72:73]
	v_cmp_gt_f32_e64 s[74:75], v3, v2
	s_and_b64 s[74:75], s[76:77], s[74:75]
	s_nop 0
	v_cndmask_b32_e64 v2, v2, v3, s[74:75]
	v_cmp_gt_f32_e64 s[76:77], v4, v2
	s_and_b64 s[76:77], s[78:79], s[76:77]
	v_add_f32_e32 v3, 0, v44
	v_cndmask_b32_e64 v2, v2, v4, s[76:77]
	v_cmp_gt_f32_e64 s[78:79], v5, v2
	s_and_b64 s[78:79], s[2:3], s[78:79]
	v_add_f32_e32 v3, v3, v46
	v_cndmask_b32_e64 v2, v2, v5, s[78:79]
	v_sub_f32_e32 v2, v2, v45
	v_mul_f32_e32 v2, 0x3fb8aa3b, v2
	v_exp_f32_e32 v2, v2
	v_add_f32_e32 v3, v3, v47
	s_and_b64 s[0:1], s[0:1], exec
	v_mov_b32_e32 v4, s80
	v_add_f32_e32 v6, v3, v2
	v_cndmask_b32_e64 v3, 0, 1, vcc
	v_cndmask_b32_e64 v2, v2, v47, s[14:15]
	v_readfirstlane_b32 s0, v3
	s_cselect_b32 s2, 2, s0
	s_and_b64 s[0:1], s[16:17], exec
	s_cselect_b32 s2, 3, s2
	s_and_b64 s[0:1], s[18:19], exec
	s_cselect_b32 s2, 4, s2
	s_and_b64 s[0:1], s[20:21], exec
	s_cselect_b32 s2, 5, s2
	s_and_b64 s[0:1], s[22:23], exec
	s_cselect_b32 s2, 6, s2
	s_and_b64 s[0:1], s[24:25], exec
	s_cselect_b32 s2, 7, s2
	s_and_b64 s[0:1], s[30:31], exec
	s_cselect_b32 s2, 8, s2
	s_and_b64 s[0:1], s[34:35], exec
	s_cselect_b32 s2, 9, s2
	s_and_b64 s[0:1], s[36:37], exec
	s_cselect_b32 s2, 10, s2
	s_and_b64 s[0:1], s[38:39], exec
	s_cselect_b32 s2, 11, s2
	s_and_b64 s[0:1], s[40:41], exec
	s_cselect_b32 s2, 12, s2
	s_and_b64 s[0:1], s[42:43], exec
	s_cselect_b32 s2, 13, s2
	s_and_b64 s[0:1], s[44:45], exec
	s_cselect_b32 s2, 14, s2
	s_and_b64 s[0:1], s[46:47], exec
	s_cselect_b32 s2, 15, s2
	s_and_b64 s[0:1], s[48:49], exec
	s_cselect_b32 s2, 16, s2
	s_and_b64 s[0:1], s[50:51], exec
	s_cselect_b32 s2, 17, s2
	s_and_b64 s[0:1], s[52:53], exec
	s_cselect_b32 s2, 18, s2
	s_and_b64 s[0:1], s[54:55], exec
	s_cselect_b32 s2, 19, s2
	s_and_b64 s[0:1], s[56:57], exec
	s_cselect_b32 s2, 20, s2
	s_and_b64 s[0:1], s[58:59], exec
	s_cselect_b32 s2, 21, s2
	s_and_b64 s[0:1], s[60:61], exec
	s_cselect_b32 s2, 22, s2
	s_and_b64 s[0:1], s[62:63], exec
	s_cselect_b32 s2, 23, s2
	s_and_b64 s[0:1], s[64:65], exec
	s_cselect_b32 s2, 24, s2
	s_and_b64 s[0:1], s[66:67], exec
	s_cselect_b32 s2, 25, s2
	s_and_b64 s[0:1], s[68:69], exec
	s_cselect_b32 s2, 26, s2
	s_and_b64 s[0:1], s[70:71], exec
	s_cselect_b32 s2, 27, s2
	s_and_b64 s[0:1], s[72:73], exec
	s_cselect_b32 s2, 28, s2
	s_and_b64 s[0:1], s[74:75], exec
	s_cselect_b32 s2, 29, s2
	s_and_b64 s[0:1], s[76:77], exec
	s_cselect_b32 s2, 30, s2
	s_and_b64 s[0:1], s[78:79], exec
	s_cselect_b32 s0, 31, s2
	v_mov_b32_e32 v3, s0
	v_cndmask_b32_e64 v3, v3, v4, s[14:15]
	v_mov_b32_e32 v4, s94
	v_cndmask_b32_e64 v3, v3, v4, s[12:13]
	v_mov_b32_e32 v4, s91
	v_cndmask_b32_e64 v7, v3, v4, s[10:11]
	v_cndmask_b32_e64 v2, v2, v46, s[12:13]
	v_cndmask_b32_e64 v8, v2, v44, s[10:11]
	v_lshl_add_u32 v2, v7, 2, 0
	ds_add_rtn_u32 v9, v2, v109
	v_lshl_or_b32 v2, s90, 2, v1
	v_div_scale_f32 v10, s[0:1], v6, v6, v8
	v_ashrrev_i32_e32 v3, 31, v2
	v_rcp_f32_e32 v11, v10
	v_lshlrev_b64 v[2:3], 2, v[2:3]
	v_lshl_add_u64 v[4:5], s[82:83], 0, v[2:3]
	global_store_dword v[4:5], v7, off sc1
	v_lshl_add_u64 v[4:5], s[86:87], 0, v[2:3]
	s_waitcnt lgkmcnt(0)
	global_store_dword v[4:5], v9, off sc1
	v_fma_f32 v4, -v10, v11, 1.0
	v_fmac_f32_e32 v11, v4, v11
	v_div_scale_f32 v4, vcc, v8, v6, v8
	v_mul_f32_e32 v5, v4, v11
	v_fma_f32 v7, -v10, v5, v4
	v_fmac_f32_e32 v5, v7, v11
	v_fma_f32 v4, -v10, v5, v4
	v_readlane_b32 s0, v254, 33
	v_readlane_b32 s66, v254, 36
	v_div_fmas_f32 v4, v4, v11, v5
	v_readlane_b32 s1, v254, 34
	v_readlane_b32 s67, v254, 37
	v_readlane_b32 s79, v254, 38
	v_div_fixup_f32 v4, v4, v6, v8
	v_lshl_add_u64 v[2:3], s[0:1], 0, v[2:3]
	global_store_dword v[2:3], v4, off sc1
	s_branch .LBB0_789

; template <bool FAST>
; __device__ __forceinline__ void p7_route_t(Frame& F, const bool do_route) {
;     ...
;     for (int it = 0; it < NIT; ++it) { const int row = FAST ? (F.bx * NIT + it) * 8 + F.wave : gw + it * NGW;
;         if (row < M_LAT && F.lane < TOPK) { const int e = tok_e[row * TOPK + F.lane]; const int idx = (int)lcnt[32 + e] + tok_rank[row * TOPK + F.lane];
;             tok_rank[row * TOPK + F.lane] = idx; elist[((size_t)e * RR + rep) * RCAP + idx] = row; } }
.LBB0_843:
	s_sub_i32 s9, s7, 24
	s_cmpk_lt_i32 s9, 0x4000
	s_cselect_b64 s[2:3], -1, 0
	s_and_b64 s[10:11], s[2:3], s[4:5]
	s_and_saveexec_b64 s[2:3], s[10:11]
	s_cbranch_execz .LBB0_845
	v_add_u32_e32 v4, 0xffffffa0, v2
	v_ashrrev_i32_e32 v5, 31, v4
	v_lshlrev_b64 v[4:5], 2, v[4:5]
	v_lshl_add_u64 v[6:7], s[82:83], 0, v[4:5]
	global_load_dword v6, v[6:7], off
	v_lshl_add_u64 v[4:5], s[86:87], 0, v[4:5]
	global_load_dword v3, v[4:5], off
	s_waitcnt vmcnt(1)
	v_lshl_add_u32 v7, v6, 2, 0
	ds_read_b32 v8, v7 offset:128
	v_ashrrev_i32_e32 v7, 31, v6
	v_lshlrev_b64 v[6:7], 17, v[6:7]
	v_lshl_add_u64 v[6:7], s[0:1], 0, v[6:7]
	s_waitcnt vmcnt(0) lgkmcnt(0)
	v_add_u32_e32 v8, v3, v8
	v_ashrrev_i32_e32 v9, 31, v8
	global_store_dword v[4:5], v8, off sc1
	v_lshl_add_u64 v[4:5], v[8:9], 2, v[6:7]
	v_mov_b32_e32 v3, s9
	global_store_dword v[4:5], v3, off sc1
.LBB0_845:
	s_or_b64 exec, exec, s[2:3]
	s_add_i32 s9, s7, -16
	s_cmpk_lt_i32 s9, 0x4000
	s_cselect_b64 s[2:3], -1, 0
	s_and_b64 s[10:11], s[2:3], s[4:5]
	s_and_saveexec_b64 s[2:3], s[10:11]
	s_cbranch_execz .LBB0_847
	v_subrev_u32_e32 v4, 64, v2
	v_ashrrev_i32_e32 v5, 31, v4
	v_lshlrev_b64 v[4:5], 2, v[4:5]
	v_lshl_add_u64 v[6:7], s[82:83], 0, v[4:5]
	global_load_dword v6, v[6:7], off
	v_lshl_add_u64 v[4:5], s[86:87], 0, v[4:5]
	global_load_dword v3, v[4:5], off
	s_waitcnt vmcnt(1)
	v_lshl_add_u32 v7, v6, 2, 0
	ds_read_b32 v8, v7 offset:128
	v_ashrrev_i32_e32 v7, 31, v6
	v_lshlrev_b64 v[6:7], 17, v[6:7]
	v_lshl_add_u64 v[6:7], s[0:1], 0, v[6:7]
	s_waitcnt vmcnt(0) lgkmcnt(0)
	v_add_u32_e32 v8, v3, v8
	v_ashrrev_i32_e32 v9, 31, v8
	global_store_dword v[4:5], v8, off sc1
	v_lshl_add_u64 v[4:5], v[8:9], 2, v[6:7]
	v_mov_b32_e32 v3, s9
	global_store_dword v[4:5], v3, off sc1
.LBB0_847:
	s_or_b64 exec, exec, s[2:3]
	s_add_i32 s9, s7, -8
	s_cmpk_lt_i32 s9, 0x4000
	s_cselect_b64 s[2:3], -1, 0
	s_and_b64 s[10:11], s[2:3], s[4:5]
	s_and_saveexec_b64 s[2:3], s[10:11]
	s_cbranch_execz .LBB0_849
	v_subrev_u32_e32 v4, 32, v2
	v_ashrrev_i32_e32 v5, 31, v4
	v_lshlrev_b64 v[4:5], 2, v[4:5]
	v_lshl_add_u64 v[6:7], s[82:83], 0, v[4:5]
	global_load_dword v6, v[6:7], off
	v_lshl_add_u64 v[4:5], s[86:87], 0, v[4:5]
	global_load_dword v3, v[4:5], off
	s_waitcnt vmcnt(1)
	v_lshl_add_u32 v7, v6, 2, 0
	ds_read_b32 v8, v7 offset:128
	v_ashrrev_i32_e32 v7, 31, v6
	v_lshlrev_b64 v[6:7], 17, v[6:7]
	v_lshl_add_u64 v[6:7], s[0:1], 0, v[6:7]
	s_waitcnt vmcnt(0) lgkmcnt(0)
	v_add_u32_e32 v8, v3, v8
	v_ashrrev_i32_e32 v9, 31, v8
	global_store_dword v[4:5], v8, off sc1
	v_lshl_add_u64 v[4:5], v[8:9], 2, v[6:7]
	v_mov_b32_e32 v3, s9
	global_store_dword v[4:5], v3, off sc1
.LBB0_849:
	s_or_b64 exec, exec, s[2:3]
	s_cmpk_lt_i32 s7, 0x4000
	s_cselect_b64 s[2:3], -1, 0
	s_and_b64 s[10:11], s[2:3], s[4:5]
	s_and_saveexec_b64 s[2:3], s[10:11]
	s_cbranch_execz .LBB0_842
	v_ashrrev_i32_e32 v3, 31, v2
	v_lshlrev_b64 v[4:5], 2, v[2:3]
	v_lshl_add_u64 v[6:7], s[82:83], 0, v[4:5]
	global_load_dword v6, v[6:7], off
	v_lshl_add_u64 v[4:5], s[86:87], 0, v[4:5]
	global_load_dword v3, v[4:5], off
	s_waitcnt vmcnt(1)
	v_lshl_add_u32 v7, v6, 2, 0
	ds_read_b32 v8, v7 offset:128
	v_ashrrev_i32_e32 v7, 31, v6
	v_lshlrev_b64 v[6:7], 17, v[6:7]
	v_lshl_add_u64 v[6:7], s[0:1], 0, v[6:7]
	s_waitcnt vmcnt(0) lgkmcnt(0)
	v_add_u32_e32 v8, v3, v8
	v_ashrrev_i32_e32 v9, 31, v8
	global_store_dword v[4:5], v8, off sc1
	v_lshl_add_u64 v[4:5], v[8:9], 2, v[6:7]
	v_mov_b32_e32 v3, s7
	global_store_dword v[4:5], v3, off sc1
	s_branch .LBB0_842

; template <bool FAST>
; __device__ __forceinline__ void p7_route_t(Frame& F, const bool do_route) {
;     ...
;     for (int it = 0; it < NIT; ++it) { const int row = FAST ? (F.bx * NIT + it) * 8 + F.wave : gw + it * NGW;
;         if (row < M_LAT && F.lane < TOPK) { const int e = tok_e[row * TOPK + F.lane]; const int idx = (int)lcnt[32 + e] + tok_rank[row * TOPK + F.lane];
;             tok_rank[row * TOPK + F.lane] = idx; elist[((size_t)e * RR + rep) * RCAP + idx] = row; } }
.LBB0_854:
	s_cmpk_lt_i32 s6, 0x4000
	s_cselect_b64 s[4:5], -1, 0
	s_and_b64 s[8:9], s[4:5], s[2:3]
	s_and_saveexec_b64 s[4:5], s[8:9]
	s_cbranch_execz .LBB0_853
	v_ashrrev_i32_e32 v3, 31, v2
	v_lshlrev_b64 v[4:5], 2, v[2:3]
	v_lshl_add_u64 v[6:7], s[82:83], 0, v[4:5]
	global_load_dword v6, v[6:7], off
	v_lshl_add_u64 v[4:5], s[86:87], 0, v[4:5]
	global_load_dword v3, v[4:5], off
	s_waitcnt vmcnt(1)
	v_lshl_add_u32 v7, v6, 2, 0
	ds_read_b32 v8, v7 offset:128
	v_ashrrev_i32_e32 v7, 31, v6
	v_lshlrev_b64 v[6:7], 17, v[6:7]
	v_lshl_add_u64 v[6:7], s[0:1], 0, v[6:7]
	s_waitcnt vmcnt(0) lgkmcnt(0)
	v_add_u32_e32 v8, v3, v8
	v_ashrrev_i32_e32 v9, 31, v8
	global_store_dword v[4:5], v8, off sc1
	v_lshl_add_u64 v[4:5], v[8:9], 2, v[6:7]
	v_mov_b32_e32 v3, s6
	global_store_dword v[4:5], v3, off sc1
	s_branch .LBB0_853

; #define LAS __attribute__((address_space(3)))
; __device__ __forceinline__ unsigned pk4_fp8(float a, float b, float c, float d) { int w = 0; w = __builtin_amdgcn_cvt_pk_fp8_f32(a, b, w, false); w = __builtin_amdgcn_cvt_pk_fp8_f32(c, d, w, true); return (unsigned)w; }
;     __device__ __forceinline__ void operator()(const f32x4 (&acc)[2][2][4][2], const Unit& u, int wr, int wc, int fr, int fq) const {
;         const int e = u.pn / npn, pnl = u.pn - e * npn; const int tid = threadIdx.x;
;         const int col0 = pnl * BM + wc * 32 + 8 * fq;
;         f32x4 bv[2][2];
; #pragma unroll
;         for (int bj = 0; bj < 2; ++bj)
; #pragma unroll
;             for (int n = 0; n < 2; ++n) bv[bj][n] = *(const f32x4*)(bias + (size_t)e * bias_ld + col0 + bj * HALF + 4 * n);
;         LAS unsigned char* wp = stg + (16 * wr + fr) * STG8_PITCH + 16 * wc + 4 * fq;
;         const int rr = (tid >> 3) & 31, cc = tid & 7, ms = tid >> 8;
;         const LAS unsigned char* rp = stg + rr * STG8_PITCH + cc * 16;
;         unsigned char* gp = O + (size_t)(u.pm * BM + 64 * (rr >> 4) + (rr & 15)) * ldc + pnl * (BM / 2) + cc * 16;
; #pragma unroll
;         for (int ai = 0; ai < 2; ++ai) {
; #pragma unroll
;             for (int m = 0; m < 4; ++m)
; #pragma unroll
;                 for (int bj = 0; bj < 2; ++bj) { const f32x4 v0 = acc[ai][bj][m][0] * scale + bv[bj][0], v1 = acc[ai][bj][m][1] * scale + bv[bj][1];
;                     *(LAS unsigned*)(wp + m * (32 * STG8_PITCH) + 64 * bj) = pk4_fp8(swiglu1(v0[0], v0[1]), swiglu1(v0[2], v0[3]), swiglu1(v1[0], v1[1]), swiglu1(v1[2], v1[3])); }
.LBB0_1010:
	s_ashr_i32 s2, s23, 31
	s_lshr_b32 s2, s2, 28
	s_add_i32 s3, s23, s2
	s_ashr_i32 s2, s3, 4
	s_and_b32 s3, s3, -16
	s_sub_i32 s23, s23, s3
	s_ashr_i32 s3, s2, 31
	s_lshl_b64 s[2:3], s[2:3], 14
	v_readlane_b32 s52, v254, 0
	v_lshl_or_b32 v2, s23, 8, v200
	v_readlane_b32 s53, v254, 1
	s_add_u32 s2, s52, s2
	s_addc_u32 s3, s53, s3
	v_ashrrev_i32_e32 v3, 31, v2
	s_nop 15
	s_nop 15
	v_lshl_add_u64 v[2:3], v[2:3], 2, s[2:3]
	global_load_dwordx4 v[14:17], v[2:3], off
	global_load_dwordx4 v[10:13], v[2:3], off offset:16
	global_load_dwordx4 v[6:9], v[2:3], off offset:512
	s_nop 0
	global_load_dwordx4 v[2:5], v[2:3], off offset:528
	v_mov_b32_e32 v176, 0
	v_lshl_or_b32 v18, s22, 8, v201
	v_ashrrev_i32_e32 v19, 31, v18
	v_lshlrev_b64 v[18:19], 11, v[18:19]
	s_lshl_b32 s22, s23, 7
	v_lshl_add_u64 v[18:19], s[8:9], 0, v[18:19]
	s_ashr_i32 s23, s22, 31
	v_lshl_add_u64 v[18:19], v[18:19], 0, s[22:23]
	v_lshl_add_u64 v[18:19], v[18:19], 0, v[170:171]
	s_cmp_eq_u32 s42, s46
	s_mov_b64 s[2:3], -1
	v_readlane_b32 s54, v254, 2
	v_readlane_b32 s55, v254, 3
	v_readlane_b32 s56, v254, 4
	v_readlane_b32 s57, v254, 5
	v_readlane_b32 s58, v254, 6
	v_readlane_b32 s59, v254, 7
	s_waitcnt vmcnt(0)
	v_pk_fma_f32 v[20:21], v[160:161], s[16:17], v[16:17] op_sel_hi:[1,0,1]
	v_pk_fma_f32 v[22:23], v[158:159], s[16:17], v[14:15] op_sel_hi:[1,0,1]
	v_min_f32_e32 v20, 0x40e00000, v20
	v_min_f32_e32 v22, 0x40e00000, v22
	v_pk_fma_f32 v[32:33], v[148:149], s[16:17], v[4:5] op_sel_hi:[1,0,1]
	v_mul_f32_e32 v148, 0xc01d265f, v22
	v_mul_f32_e32 v149, 0xc01d265f, v20
	v_pk_fma_f32 v[24:25], v[156:157], s[16:17], v[12:13] op_sel_hi:[1,0,1]
	v_pk_fma_f32 v[26:27], v[154:155], s[16:17], v[10:11] op_sel_hi:[1,0,1]
	v_exp_f32_e32 v148, v148
	v_exp_f32_e32 v149, v149
	v_min_f32_e32 v26, 0x40e00000, v26
	v_min_f32_e32 v24, 0x40e00000, v24
	v_pk_fma_f32 v[28:29], v[152:153], s[16:17], v[8:9] op_sel_hi:[1,0,1]
	v_pk_fma_f32 v[30:31], v[150:151], s[16:17], v[6:7] op_sel_hi:[1,0,1]
	v_mul_f32_e32 v150, 0xc01d265f, v26
	v_mul_f32_e32 v151, 0xc01d265f, v24
	v_min_f32_e32 v30, 0x40e00000, v30
	v_min_f32_e32 v28, 0x40e00000, v28
	v_mul_f32_e32 v152, 0xc01d265f, v30
	v_mul_f32_e32 v153, 0xc01d265f, v28
	v_exp_f32_e32 v150, v150
	v_exp_f32_e32 v151, v151
	v_add_f32_e32 v148, 1.0, v148
	v_add_f32_e32 v149, 1.0, v149
	v_rcp_f32_e32 v148, v148
	v_rcp_f32_e32 v149, v149
	v_pk_fma_f32 v[146:147], v[146:147], s[16:17], v[2:3] op_sel_hi:[1,0,1]
	v_exp_f32_e32 v152, v152
	v_exp_f32_e32 v153, v153
	v_min_f32_e32 v146, 0x40e00000, v146
	v_min_f32_e32 v32, 0x40e00000, v32
	v_med3_f32 v23, v23, s47, v204
	v_med3_f32 v21, v21, s47, v204
	v_mul_f32_e32 v154, 0xc01d265f, v146
	v_mul_f32_e32 v155, 0xc01d265f, v32
	v_add_f32_e32 v150, 1.0, v150
	v_add_f32_e32 v151, 1.0, v151
	v_add_f32_e32 v23, 1.0, v23
	v_add_f32_e32 v21, 1.0, v21
	v_rcp_f32_e32 v150, v150
	v_rcp_f32_e32 v151, v151
	v_mul_f32_e32 v22, v22, v148
	v_mul_f32_e32 v20, v20, v149
	v_exp_f32_e32 v154, v154
	v_exp_f32_e32 v155, v155
	v_add_f32_e32 v152, 1.0, v152
	v_add_f32_e32 v153, 1.0, v153
	v_mul_f32_e32 v22, v23, v22
	v_mul_f32_e32 v20, v21, v20
	v_rcp_f32_e32 v152, v152
	v_rcp_f32_e32 v153, v153
	v_cvt_pk_fp8_f32 v176, v22, v20
	v_med3_f32 v27, v27, s47, v204
	v_med3_f32 v25, v25, s47, v204
	v_add_f32_e32 v27, 1.0, v27
	v_add_f32_e32 v25, 1.0, v25
	v_mul_f32_e32 v26, v26, v150
	v_mul_f32_e32 v24, v24, v151
	v_med3_f32 v31, v31, s47, v204
	v_med3_f32 v29, v29, s47, v204
	v_add_f32_e32 v154, 1.0, v154
	v_add_f32_e32 v155, 1.0, v155
	v_mul_f32_e32 v21, v27, v26
	v_mul_f32_e32 v23, v25, v24
	v_add_f32_e32 v31, 1.0, v31
	v_add_f32_e32 v29, 1.0, v29
	v_rcp_f32_e32 v154, v154
	v_mul_f32_e32 v30, v30, v152
	v_mul_f32_e32 v28, v28, v153
	v_cvt_pk_fp8_f32 v176, v21, v23 op_sel:[0,0,1]
	v_rcp_f32_e32 v21, v155
	v_mul_f32_e32 v20, v31, v30
	v_mul_f32_e32 v22, v29, v28
	v_mov_b32_e32 v28, 0
	v_cvt_pk_fp8_f32 v28, v20, v22
	v_med3_f32 v147, v147, s47, v204
	v_med3_f32 v23, v33, s47, v204
	v_add_f32_e32 v147, 1.0, v147
	v_mul_f32_e32 v146, v146, v154
	v_mul_f32_e32 v20, v32, v21
	v_add_f32_e32 v21, 1.0, v23
	v_pk_fma_f32 v[22:23], v[142:143], s[16:17], v[14:15] op_sel_hi:[1,0,1]
	v_mul_f32_e32 v24, v147, v146
	v_mul_f32_e32 v20, v21, v20
	v_min_f32_e32 v22, 0x40e00000, v22
	v_cvt_pk_fp8_f32 v28, v24, v20 op_sel:[0,0,1]
	v_mul_f32_e32 v24, 0xc01d265f, v22
	v_exp_f32_e32 v29, v24
	v_pk_fma_f32 v[20:21], v[144:145], s[16:17], v[16:17] op_sel_hi:[1,0,1]
	v_pk_fma_f32 v[26:27], v[138:139], s[16:17], v[10:11] op_sel_hi:[1,0,1]
	v_min_f32_e32 v20, 0x40e00000, v20
	v_add_f32_e32 v29, 1.0, v29
	v_mul_f32_e32 v30, 0xc01d265f, v20
	v_rcp_f32_e32 v29, v29
	v_exp_f32_e32 v30, v30
	v_med3_f32 v23, v23, s47, v204
	v_min_f32_e32 v26, 0x40e00000, v26
	v_mul_f32_e32 v22, v22, v29
	v_add_f32_e32 v23, 1.0, v23
	v_mul_f32_e32 v29, 0xc01d265f, v26
	v_mul_f32_e32 v22, v23, v22
	v_add_f32_e32 v23, 1.0, v30
	v_rcp_f32_e32 v23, v23
	v_exp_f32_e32 v29, v29
	v_pk_fma_f32 v[24:25], v[140:141], s[16:17], v[12:13] op_sel_hi:[1,0,1]
	v_med3_f32 v21, v21, s47, v204
	v_min_f32_e32 v24, 0x40e00000, v24
	v_mul_f32_e32 v20, v20, v23
	v_add_f32_e32 v23, 1.0, v29
	v_mul_f32_e32 v29, 0xc01d265f, v24
	v_rcp_f32_e32 v23, v23
	v_exp_f32_e32 v29, v29
	v_add_f32_e32 v21, 1.0, v21
	v_mul_f32_e32 v20, v21, v20
	v_mul_f32_e32 v23, v26, v23
	v_add_f32_e32 v26, 1.0, v29
	v_rcp_f32_e32 v26, v26
	v_med3_f32 v21, v27, s47, v204
	v_add_f32_e32 v21, 1.0, v21
	v_mul_f32_e32 v23, v21, v23
	v_med3_f32 v21, v25, s47, v204
	v_mul_f32_e32 v24, v24, v26
	v_add_f32_e32 v21, 1.0, v21
	v_mov_b32_e32 v29, 0
	v_mul_f32_e32 v24, v21, v24
	v_cvt_pk_fp8_f32 v29, v22, v20
	v_pk_fma_f32 v[20:21], v[134:135], s[16:17], v[6:7] op_sel_hi:[1,0,1]
; #define LAS __attribute__((address_space(3)))
; __device__ __forceinline__ unsigned pk4_fp8(float a, float b, float c, float d) { int w = 0; w = __builtin_amdgcn_cvt_pk_fp8_f32(a, b, w, false); w = __builtin_amdgcn_cvt_pk_fp8_f32(c, d, w, true); return (unsigned)w; }
;     __device__ __forceinline__ void operator()(const f32x4 (&acc)[2][2][4][2], const Unit& u, int wr, int wc, int fr, int fq) const {
;     ...
; #pragma unroll
;             for (int m = 0; m < 4; ++m)
; #pragma unroll
;                 for (int bj = 0; bj < 2; ++bj) { const f32x4 v0 = acc[ai][bj][m][0] * scale + bv[bj][0], v1 = acc[ai][bj][m][1] * scale + bv[bj][1];
;                     *(LAS unsigned*)(wp + m * (32 * STG8_PITCH) + 64 * bj) = pk4_fp8(swiglu1(v0[0], v0[1]), swiglu1(v0[2], v0[3]), swiglu1(v1[0], v1[1]), swiglu1(v1[2], v1[3])); }
	ds_write2_b32 v202, v176, v28 offset1:16
	v_min_f32_e32 v20, 0x40e00000, v20
	v_mul_f32_e32 v22, 0xc01d265f, v20
	v_exp_f32_e32 v26, v22
	v_cvt_pk_fp8_f32 v29, v23, v24 op_sel:[0,0,1]
	v_pk_fma_f32 v[22:23], v[136:137], s[16:17], v[8:9] op_sel_hi:[1,0,1]
	v_med3_f32 v21, v21, s47, v204
	v_add_f32_e32 v26, 1.0, v26
	v_min_f32_e32 v22, 0x40e00000, v22
	v_rcp_f32_e32 v30, v26
	v_mul_f32_e32 v26, 0xc01d265f, v22
	v_exp_f32_e32 v31, v26
	v_pk_fma_f32 v[26:27], v[130:131], s[16:17], v[2:3] op_sel_hi:[1,0,1]
	v_mul_f32_e32 v20, v20, v30
	v_add_f32_e32 v21, 1.0, v21
	v_mul_f32_e32 v20, v21, v20
	v_med3_f32 v21, v23, s47, v204
	v_min_f32_e32 v23, 0x40e00000, v26
	v_add_f32_e32 v30, 1.0, v31
	v_mul_f32_e32 v26, 0xc01d265f, v23
	v_rcp_f32_e32 v30, v30
	v_exp_f32_e32 v26, v26
	v_pk_fma_f32 v[24:25], v[132:133], s[16:17], v[4:5] op_sel_hi:[1,0,1]
	v_mul_f32_e32 v22, v22, v30
	v_add_f32_e32 v21, 1.0, v21
	v_min_f32_e32 v24, 0x40e00000, v24
	v_mul_f32_e32 v21, v21, v22
	v_med3_f32 v22, v27, s47, v204
	v_add_f32_e32 v26, 1.0, v26
	v_mul_f32_e32 v27, 0xc01d265f, v24
	v_rcp_f32_e32 v26, v26
	v_exp_f32_e32 v27, v27
	v_add_f32_e32 v22, 1.0, v22
	v_mul_f32_e32 v23, v23, v26
	v_mul_f32_e32 v22, v22, v23
	v_add_f32_e32 v23, 1.0, v27
	v_rcp_f32_e32 v23, v23
	v_med3_f32 v25, v25, s47, v204
	v_mov_b32_e32 v26, 0
	v_cvt_pk_fp8_f32 v26, v20, v21
	v_mul_f32_e32 v20, v24, v23
	v_add_f32_e32 v21, 1.0, v25
	v_pk_fma_f32 v[24:25], v[126:127], s[16:17], v[14:15] op_sel_hi:[1,0,1]
	v_mul_f32_e32 v20, v21, v20
	v_min_f32_e32 v23, 0x40e00000, v24
	v_mul_f32_e32 v24, 0xc01d265f, v23
	v_exp_f32_e32 v24, v24
	v_cvt_pk_fp8_f32 v26, v22, v20 op_sel:[0,0,1]
	v_pk_fma_f32 v[20:21], v[128:129], s[16:17], v[16:17] op_sel_hi:[1,0,1]
	v_add_u32_e32 v22, 0x1000, v202
	v_add_f32_e32 v24, 1.0, v24
	v_min_f32_e32 v20, 0x40e00000, v20
	v_rcp_f32_e32 v24, v24
	v_mul_f32_e32 v30, 0xc01d265f, v20
	v_exp_f32_e32 v30, v30
	ds_write2_b32 v22, v29, v26 offset0:128 offset1:144
	v_pk_fma_f32 v[28:29], v[122:123], s[16:17], v[10:11] op_sel_hi:[1,0,1]
	v_med3_f32 v25, v25, s47, v204
	v_mul_f32_e32 v23, v23, v24
	v_add_f32_e32 v24, 1.0, v25
	v_min_f32_e32 v25, 0x40e00000, v28
	v_mul_f32_e32 v28, 0xc01d265f, v25
	v_mul_f32_e32 v23, v24, v23
	v_add_f32_e32 v24, 1.0, v30
	v_rcp_f32_e32 v24, v24
	v_exp_f32_e32 v28, v28
	v_pk_fma_f32 v[26:27], v[124:125], s[16:17], v[12:13] op_sel_hi:[1,0,1]
	v_med3_f32 v21, v21, s47, v204
	v_min_f32_e32 v26, 0x40e00000, v26
	v_mul_f32_e32 v20, v20, v24
	v_add_f32_e32 v24, 1.0, v28
	v_mul_f32_e32 v28, 0xc01d265f, v26
	v_rcp_f32_e32 v24, v24
	v_exp_f32_e32 v28, v28
	v_add_f32_e32 v21, 1.0, v21
	v_mul_f32_e32 v20, v21, v20
	v_mul_f32_e32 v24, v25, v24
	v_add_f32_e32 v25, 1.0, v28
	v_rcp_f32_e32 v25, v25
	v_med3_f32 v21, v29, s47, v204
	v_add_f32_e32 v21, 1.0, v21
	v_mul_f32_e32 v24, v21, v24
	v_med3_f32 v21, v27, s47, v204
	v_mul_f32_e32 v25, v26, v25
	v_add_f32_e32 v21, 1.0, v21
	v_mov_b32_e32 v30, 0
	v_mul_f32_e32 v25, v21, v25
	v_cvt_pk_fp8_f32 v30, v23, v20
	v_pk_fma_f32 v[20:21], v[118:119], s[16:17], v[6:7] op_sel_hi:[1,0,1]
	v_pk_fma_f32 v[26:27], v[116:117], s[16:17], v[4:5] op_sel_hi:[1,0,1]
	v_min_f32_e32 v20, 0x40e00000, v20
	v_mul_f32_e32 v23, 0xc01d265f, v20
	v_exp_f32_e32 v23, v23
	v_cvt_pk_fp8_f32 v30, v24, v25 op_sel:[0,0,1]
	v_pk_fma_f32 v[24:25], v[120:121], s[16:17], v[8:9] op_sel_hi:[1,0,1]
	v_med3_f32 v21, v21, s47, v204
	v_min_f32_e32 v24, 0x40e00000, v24
	v_mul_f32_e32 v28, 0xc01d265f, v24
	v_add_f32_e32 v23, 1.0, v23
	v_rcp_f32_e32 v23, v23
	v_exp_f32_e32 v31, v28
	v_pk_fma_f32 v[28:29], v[114:115], s[16:17], v[2:3] op_sel_hi:[1,0,1]
	v_add_f32_e32 v21, 1.0, v21
	v_mul_f32_e32 v20, v20, v23
	v_add_f32_e32 v23, 1.0, v31
	v_rcp_f32_e32 v23, v23
	v_mul_f32_e32 v20, v21, v20
	v_med3_f32 v21, v25, s47, v204
	v_min_f32_e32 v26, 0x40e00000, v26
	v_mul_f32_e32 v23, v24, v23
	v_min_f32_e32 v24, 0x40e00000, v28
	v_mul_f32_e32 v25, 0xc01d265f, v24
	v_exp_f32_e32 v25, v25
	v_mul_f32_e32 v28, 0xc01d265f, v26
	v_exp_f32_e32 v28, v28
	v_add_f32_e32 v25, 1.0, v25
	v_rcp_f32_e32 v25, v25
	v_add_f32_e32 v21, 1.0, v21
	v_mul_f32_e32 v21, v21, v23
	v_med3_f32 v23, v29, s47, v204
	v_mul_f32_e32 v24, v24, v25
	v_add_f32_e32 v23, 1.0, v23
	v_mul_f32_e32 v23, v23, v24
	v_add_f32_e32 v24, 1.0, v28
	v_rcp_f32_e32 v24, v24
	v_mov_b32_e32 v31, 0
	v_cvt_pk_fp8_f32 v31, v20, v21
	v_med3_f32 v25, v27, s47, v204
	v_mul_f32_e32 v20, v26, v24
	v_add_f32_e32 v21, 1.0, v25
	v_mul_f32_e32 v20, v21, v20
	v_pk_fma_f32 v[24:25], v[110:111], s[16:17], v[14:15] op_sel_hi:[1,0,1]
	v_cvt_pk_fp8_f32 v31, v23, v20 op_sel:[0,0,1]
	v_min_f32_e32 v23, 0x40e00000, v24
	v_mul_f32_e32 v24, 0xc01d265f, v23
	v_exp_f32_e32 v24, v24
	v_pk_fma_f32 v[20:21], v[112:113], s[16:17], v[16:17] op_sel_hi:[1,0,1]
	v_pk_fma_f32 v[28:29], v[106:107], s[16:17], v[10:11] op_sel_hi:[1,0,1]
	v_min_f32_e32 v20, 0x40e00000, v20
	v_add_f32_e32 v24, 1.0, v24
	v_rcp_f32_e32 v24, v24
	v_mul_f32_e32 v32, 0xc01d265f, v20
	v_exp_f32_e32 v32, v32
	v_med3_f32 v25, v25, s47, v204
	v_mul_f32_e32 v23, v23, v24
	v_add_f32_e32 v24, 1.0, v25
	v_min_f32_e32 v25, 0x40e00000, v28
	v_mul_f32_e32 v28, 0xc01d265f, v25
	v_mul_f32_e32 v23, v24, v23
	v_add_f32_e32 v24, 1.0, v32
	v_rcp_f32_e32 v24, v24
	v_exp_f32_e32 v28, v28
	v_pk_fma_f32 v[26:27], v[108:109], s[16:17], v[12:13] op_sel_hi:[1,0,1]
	v_med3_f32 v21, v21, s47, v204
	v_min_f32_e32 v26, 0x40e00000, v26
	v_mul_f32_e32 v20, v20, v24
	v_add_f32_e32 v24, 1.0, v28
	v_mul_f32_e32 v28, 0xc01d265f, v26
	v_rcp_f32_e32 v24, v24
	v_exp_f32_e32 v28, v28
	v_add_f32_e32 v21, 1.0, v21
	v_mul_f32_e32 v20, v21, v20
	v_mul_f32_e32 v24, v25, v24
	v_add_f32_e32 v25, 1.0, v28
	v_rcp_f32_e32 v25, v25
; #define LAS __attribute__((address_space(3)))
; __device__ __forceinline__ unsigned pk4_fp8(float a, float b, float c, float d) { int w = 0; w = __builtin_amdgcn_cvt_pk_fp8_f32(a, b, w, false); w = __builtin_amdgcn_cvt_pk_fp8_f32(c, d, w, true); return (unsigned)w; }
; __device__ __forceinline__ float swiglu1(float g, float l) {
;     g = fminf(g, 7.0f); l = fminf(fmaxf(l, -7.0f), 7.0f);
;     const float s = __builtin_amdgcn_rcpf(1.0f + __expf(-1.702f * g));
;     return g * s * (l + 1.0f);
; }
;     __device__ __forceinline__ void operator()(const f32x4 (&acc)[2][2][4][2], const Unit& u, int wr, int wc, int fr, int fq) const {
;     ...
;         for (int ai = 0; ai < 2; ++ai) {
; #pragma unroll
;             for (int m = 0; m < 4; ++m)
; #pragma unroll
;                 for (int bj = 0; bj < 2; ++bj) { const f32x4 v0 = acc[ai][bj][m][0] * scale + bv[bj][0], v1 = acc[ai][bj][m][1] * scale + bv[bj][1];
;                     *(LAS unsigned*)(wp + m * (32 * STG8_PITCH) + 64 * bj) = pk4_fp8(swiglu1(v0[0], v0[1]), swiglu1(v0[2], v0[3]), swiglu1(v1[0], v1[1]), swiglu1(v1[2], v1[3])); }
;             asm volatile("s_waitcnt lgkmcnt(0)" ::: "memory"); __builtin_amdgcn_s_barrier(); asm volatile("" ::: "memory");
; #pragma unroll
;             for (int k2 = 0; k2 < 2; ++k2) { const int m = ms + 2 * k2;
;                 *(u32x4*)(gp + (size_t)(ai * HALF + m * 16) * ldc) = *(const LAS u32x4*)(rp + m * (32 * STG8_PITCH)); }
;             asm volatile("s_waitcnt lgkmcnt(0)" ::: "memory"); __builtin_amdgcn_s_barrier(); asm volatile("" ::: "memory");
	v_med3_f32 v21, v29, s47, v204
	v_add_f32_e32 v21, 1.0, v21
	v_mul_f32_e32 v24, v21, v24
	v_med3_f32 v21, v27, s47, v204
	v_mul_f32_e32 v25, v26, v25
	v_add_f32_e32 v21, 1.0, v21
	v_mov_b32_e32 v32, 0
	v_mul_f32_e32 v25, v21, v25
	v_cvt_pk_fp8_f32 v32, v23, v20
	v_pk_fma_f32 v[20:21], v[102:103], s[16:17], v[6:7] op_sel_hi:[1,0,1]
	v_pk_fma_f32 v[26:27], v[100:101], s[16:17], v[4:5] op_sel_hi:[1,0,1]
	v_min_f32_e32 v20, 0x40e00000, v20
	v_mul_f32_e32 v23, 0xc01d265f, v20
	v_exp_f32_e32 v23, v23
	v_cvt_pk_fp8_f32 v32, v24, v25 op_sel:[0,0,1]
	v_pk_fma_f32 v[24:25], v[104:105], s[16:17], v[8:9] op_sel_hi:[1,0,1]
	v_med3_f32 v21, v21, s47, v204
	v_min_f32_e32 v24, 0x40e00000, v24
	v_mul_f32_e32 v28, 0xc01d265f, v24
	v_add_f32_e32 v23, 1.0, v23
	v_rcp_f32_e32 v23, v23
	v_exp_f32_e32 v33, v28
	v_pk_fma_f32 v[28:29], v[98:99], s[16:17], v[2:3] op_sel_hi:[1,0,1]
	v_add_f32_e32 v21, 1.0, v21
	v_mul_f32_e32 v20, v20, v23
	v_add_f32_e32 v23, 1.0, v33
	v_rcp_f32_e32 v23, v23
	v_mul_f32_e32 v20, v21, v20
	v_med3_f32 v21, v25, s47, v204
	v_min_f32_e32 v26, 0x40e00000, v26
	v_mul_f32_e32 v23, v24, v23
	v_min_f32_e32 v24, 0x40e00000, v28
	v_mul_f32_e32 v25, 0xc01d265f, v24
	v_exp_f32_e32 v25, v25
	v_mul_f32_e32 v28, 0xc01d265f, v26
	v_exp_f32_e32 v28, v28
	v_add_f32_e32 v25, 1.0, v25
	v_rcp_f32_e32 v25, v25
	v_add_f32_e32 v21, 1.0, v21
	v_mul_f32_e32 v21, v21, v23
	v_med3_f32 v23, v29, s47, v204
	v_mul_f32_e32 v24, v24, v25
	v_add_f32_e32 v23, 1.0, v23
	v_mul_f32_e32 v23, v23, v24
	v_add_f32_e32 v24, 1.0, v28
	v_rcp_f32_e32 v24, v24
	v_med3_f32 v25, v27, s47, v204
	v_mov_b32_e32 v27, 0
	v_cvt_pk_fp8_f32 v27, v20, v21
	v_mul_f32_e32 v20, v26, v24
	v_add_f32_e32 v21, 1.0, v25
	v_mul_f32_e32 v20, v21, v20
	v_cvt_pk_fp8_f32 v27, v23, v20 op_sel:[0,0,1]
	v_add_u32_e32 v23, 0x2400, v202
	v_add_u32_e32 v24, 0x3400, v202
	ds_write2_b32 v23, v30, v31 offset1:16
	ds_write2_b32 v24, v32, v27 offset0:128 offset1:144
	s_waitcnt lgkmcnt(0)
	s_barrier
	ds_read_b128 v[26:29], v203
	ds_read_b128 v[30:33], v203 offset:9216
	v_lshl_add_u64 v[20:21], v[18:19], 0, v[172:173]
	v_lshl_add_u64 v[18:19], v[18:19], 0, v[174:175]
	s_waitcnt lgkmcnt(1)
	global_store_dwordx4 v[20:21], v[26:29], off sc1
	s_waitcnt lgkmcnt(0)
	global_store_dwordx4 v[18:19], v[30:33], off sc1
	v_pk_fma_f32 v[28:29], v[94:95], s[16:17], v[14:15] op_sel_hi:[1,0,1]
	v_pk_fma_f32 v[26:27], v[96:97], s[16:17], v[16:17] op_sel_hi:[1,0,1]
	v_min_f32_e32 v25, 0x40e00000, v28
	v_mul_f32_e32 v28, 0xc01d265f, v25
	v_exp_f32_e32 v28, v28
	v_min_f32_e32 v26, 0x40e00000, v26
	v_pk_fma_f32 v[32:33], v[90:91], s[16:17], v[10:11] op_sel_hi:[1,0,1]
	v_mul_f32_e32 v90, 0xc01d265f, v26
	v_add_f32_e32 v28, 1.0, v28
	v_rcp_f32_e32 v28, v28
	v_exp_f32_e32 v90, v90
	v_med3_f32 v29, v29, s47, v204
	v_mul_f32_e32 v25, v25, v28
	v_add_f32_e32 v28, 1.0, v29
	v_min_f32_e32 v29, 0x40e00000, v32
	v_mul_f32_e32 v32, 0xc01d265f, v29
	v_mul_f32_e32 v25, v28, v25
	v_add_f32_e32 v28, 1.0, v90
	v_rcp_f32_e32 v28, v28
	v_exp_f32_e32 v32, v32
	v_pk_fma_f32 v[30:31], v[92:93], s[16:17], v[12:13] op_sel_hi:[1,0,1]
	v_med3_f32 v27, v27, s47, v204
	v_min_f32_e32 v30, 0x40e00000, v30
	v_mul_f32_e32 v26, v26, v28
	v_add_f32_e32 v28, 1.0, v32
	v_mul_f32_e32 v32, 0xc01d265f, v30
	v_rcp_f32_e32 v28, v28
	v_exp_f32_e32 v32, v32
	v_add_f32_e32 v27, 1.0, v27
	v_mul_f32_e32 v26, v27, v26
	v_mul_f32_e32 v28, v29, v28
	v_add_f32_e32 v29, 1.0, v32
	v_rcp_f32_e32 v29, v29
	v_med3_f32 v27, v33, s47, v204
	v_add_f32_e32 v27, 1.0, v27
	v_mul_f32_e32 v28, v27, v28
	v_med3_f32 v27, v31, s47, v204
	v_mul_f32_e32 v29, v30, v29
	v_add_f32_e32 v27, 1.0, v27
	v_mov_b32_e32 v90, 0
	v_mul_f32_e32 v29, v27, v29
	v_cvt_pk_fp8_f32 v90, v25, v26
	v_pk_fma_f32 v[26:27], v[86:87], s[16:17], v[6:7] op_sel_hi:[1,0,1]
	v_pk_fma_f32 v[30:31], v[84:85], s[16:17], v[4:5] op_sel_hi:[1,0,1]
	v_min_f32_e32 v25, 0x40e00000, v26
	v_mul_f32_e32 v26, 0xc01d265f, v25
	v_exp_f32_e32 v26, v26
	v_cvt_pk_fp8_f32 v90, v28, v29 op_sel:[0,0,1]
	v_pk_fma_f32 v[28:29], v[88:89], s[16:17], v[8:9] op_sel_hi:[1,0,1]
	v_med3_f32 v27, v27, s47, v204
	v_min_f32_e32 v28, 0x40e00000, v28
	v_mul_f32_e32 v32, 0xc01d265f, v28
	v_add_f32_e32 v26, 1.0, v26
	v_rcp_f32_e32 v26, v26
	v_exp_f32_e32 v84, v32
	v_pk_fma_f32 v[32:33], v[82:83], s[16:17], v[2:3] op_sel_hi:[1,0,1]
	v_add_f32_e32 v27, 1.0, v27
	v_mul_f32_e32 v25, v25, v26
	v_add_f32_e32 v26, 1.0, v84
	v_rcp_f32_e32 v26, v26
	v_mul_f32_e32 v25, v27, v25
	v_med3_f32 v27, v29, s47, v204
	v_min_f32_e32 v30, 0x40e00000, v30
	v_mul_f32_e32 v26, v28, v26
	v_min_f32_e32 v28, 0x40e00000, v32
	v_mul_f32_e32 v29, 0xc01d265f, v28
	v_exp_f32_e32 v29, v29
	v_mul_f32_e32 v32, 0xc01d265f, v30
	v_exp_f32_e32 v32, v32
	v_add_f32_e32 v29, 1.0, v29
	v_rcp_f32_e32 v29, v29
	v_add_f32_e32 v27, 1.0, v27
	v_mul_f32_e32 v26, v27, v26
	v_med3_f32 v27, v33, s47, v204
	v_mul_f32_e32 v28, v28, v29
	v_add_f32_e32 v27, 1.0, v27
	v_mul_f32_e32 v27, v27, v28
	v_add_f32_e32 v28, 1.0, v32
	v_rcp_f32_e32 v28, v28
	v_mov_b32_e32 v82, 0
	v_cvt_pk_fp8_f32 v82, v25, v26
	v_med3_f32 v29, v31, s47, v204
	v_mul_f32_e32 v25, v30, v28
	v_add_f32_e32 v26, 1.0, v29
	v_mul_f32_e32 v25, v26, v25
	v_pk_fma_f32 v[28:29], v[78:79], s[16:17], v[14:15] op_sel_hi:[1,0,1]
	v_cvt_pk_fp8_f32 v82, v27, v25 op_sel:[0,0,1]
	v_min_f32_e32 v25, 0x40e00000, v28
	v_mul_f32_e32 v28, 0xc01d265f, v25
	v_exp_f32_e32 v28, v28
	v_pk_fma_f32 v[26:27], v[80:81], s[16:17], v[16:17] op_sel_hi:[1,0,1]
	v_pk_fma_f32 v[32:33], v[74:75], s[16:17], v[10:11] op_sel_hi:[1,0,1]
	v_min_f32_e32 v26, 0x40e00000, v26
	v_add_f32_e32 v28, 1.0, v28
	v_rcp_f32_e32 v28, v28
	v_mul_f32_e32 v74, 0xc01d265f, v26
	v_exp_f32_e32 v74, v74
; #define LAS __attribute__((address_space(3)))
; __device__ __forceinline__ unsigned pk4_fp8(float a, float b, float c, float d) { int w = 0; w = __builtin_amdgcn_cvt_pk_fp8_f32(a, b, w, false); w = __builtin_amdgcn_cvt_pk_fp8_f32(c, d, w, true); return (unsigned)w; }
; __device__ __forceinline__ float swiglu1(float g, float l) {
;     g = fminf(g, 7.0f); l = fminf(fmaxf(l, -7.0f), 7.0f);
;     const float s = __builtin_amdgcn_rcpf(1.0f + __expf(-1.702f * g));
;     return g * s * (l + 1.0f);
; }
;     __device__ __forceinline__ void operator()(const f32x4 (&acc)[2][2][4][2], const Unit& u, int wr, int wc, int fr, int fq) const {
;     ...
;                 for (int bj = 0; bj < 2; ++bj) { const f32x4 v0 = acc[ai][bj][m][0] * scale + bv[bj][0], v1 = acc[ai][bj][m][1] * scale + bv[bj][1];
;                     *(LAS unsigned*)(wp + m * (32 * STG8_PITCH) + 64 * bj) = pk4_fp8(swiglu1(v0[0], v0[1]), swiglu1(v0[2], v0[3]), swiglu1(v1[0], v1[1]), swiglu1(v1[2], v1[3])); }
	v_med3_f32 v29, v29, s47, v204
	v_mul_f32_e32 v25, v25, v28
	v_add_f32_e32 v28, 1.0, v29
	v_min_f32_e32 v29, 0x40e00000, v32
	v_mul_f32_e32 v32, 0xc01d265f, v29
	v_mul_f32_e32 v25, v28, v25
	v_add_f32_e32 v28, 1.0, v74
	v_rcp_f32_e32 v28, v28
	v_exp_f32_e32 v32, v32
	v_pk_fma_f32 v[30:31], v[76:77], s[16:17], v[12:13] op_sel_hi:[1,0,1]
	v_med3_f32 v27, v27, s47, v204
	v_min_f32_e32 v30, 0x40e00000, v30
	v_mul_f32_e32 v26, v26, v28
	v_add_f32_e32 v28, 1.0, v32
	v_mul_f32_e32 v32, 0xc01d265f, v30
	v_rcp_f32_e32 v28, v28
	v_exp_f32_e32 v32, v32
	v_add_f32_e32 v27, 1.0, v27
	v_mul_f32_e32 v26, v27, v26
	v_mul_f32_e32 v28, v29, v28
	v_add_f32_e32 v29, 1.0, v32
	v_rcp_f32_e32 v29, v29
	v_med3_f32 v27, v33, s47, v204
	v_add_f32_e32 v27, 1.0, v27
	v_mul_f32_e32 v28, v27, v28
	v_med3_f32 v27, v31, s47, v204
	v_mul_f32_e32 v29, v30, v29
	v_add_f32_e32 v27, 1.0, v27
	v_mov_b32_e32 v74, 0
	v_mul_f32_e32 v29, v27, v29
	v_cvt_pk_fp8_f32 v74, v25, v26
	v_pk_fma_f32 v[26:27], v[70:71], s[16:17], v[6:7] op_sel_hi:[1,0,1]
	v_pk_fma_f32 v[30:31], v[68:69], s[16:17], v[4:5] op_sel_hi:[1,0,1]
	v_min_f32_e32 v25, 0x40e00000, v26
	v_mul_f32_e32 v26, 0xc01d265f, v25
	v_exp_f32_e32 v26, v26
	v_cvt_pk_fp8_f32 v74, v28, v29 op_sel:[0,0,1]
	v_pk_fma_f32 v[28:29], v[72:73], s[16:17], v[8:9] op_sel_hi:[1,0,1]
	v_med3_f32 v27, v27, s47, v204
	v_min_f32_e32 v28, 0x40e00000, v28
	v_mul_f32_e32 v32, 0xc01d265f, v28
	v_add_f32_e32 v26, 1.0, v26
	v_rcp_f32_e32 v26, v26
	v_exp_f32_e32 v68, v32
	v_pk_fma_f32 v[32:33], v[66:67], s[16:17], v[2:3] op_sel_hi:[1,0,1]
	v_add_f32_e32 v27, 1.0, v27
	v_mul_f32_e32 v25, v25, v26
	v_add_f32_e32 v26, 1.0, v68
	v_rcp_f32_e32 v26, v26
	v_mul_f32_e32 v25, v27, v25
	v_med3_f32 v27, v29, s47, v204
	v_min_f32_e32 v30, 0x40e00000, v30
	v_mul_f32_e32 v26, v28, v26
	v_min_f32_e32 v28, 0x40e00000, v32
	v_mul_f32_e32 v29, 0xc01d265f, v28
	v_exp_f32_e32 v29, v29
	v_mul_f32_e32 v32, 0xc01d265f, v30
	v_exp_f32_e32 v32, v32
	v_add_f32_e32 v29, 1.0, v29
	v_rcp_f32_e32 v29, v29
	v_add_f32_e32 v27, 1.0, v27
	v_mul_f32_e32 v26, v27, v26
	v_med3_f32 v27, v33, s47, v204
	v_mul_f32_e32 v28, v28, v29
	v_add_f32_e32 v27, 1.0, v27
	v_mul_f32_e32 v27, v27, v28
	v_add_f32_e32 v28, 1.0, v32
	v_rcp_f32_e32 v28, v28
	v_mov_b32_e32 v66, 0
	v_cvt_pk_fp8_f32 v66, v25, v26
	v_med3_f32 v29, v31, s47, v204
	v_mul_f32_e32 v25, v30, v28
	v_add_f32_e32 v26, 1.0, v29
	v_mul_f32_e32 v25, v26, v25
	v_pk_fma_f32 v[28:29], v[58:59], s[16:17], v[14:15] op_sel_hi:[1,0,1]
	v_cvt_pk_fp8_f32 v66, v27, v25 op_sel:[0,0,1]
	v_min_f32_e32 v25, 0x40e00000, v28
	v_mul_f32_e32 v28, 0xc01d265f, v25
	v_exp_f32_e32 v28, v28
	v_pk_fma_f32 v[26:27], v[60:61], s[16:17], v[16:17] op_sel_hi:[1,0,1]
	v_pk_fma_f32 v[32:33], v[50:51], s[16:17], v[10:11] op_sel_hi:[1,0,1]
	v_min_f32_e32 v26, 0x40e00000, v26
	v_add_f32_e32 v28, 1.0, v28
	v_rcp_f32_e32 v28, v28
	v_mul_f32_e32 v50, 0xc01d265f, v26
	v_exp_f32_e32 v50, v50
	v_med3_f32 v29, v29, s47, v204
	v_mul_f32_e32 v25, v25, v28
	v_add_f32_e32 v28, 1.0, v29
	v_min_f32_e32 v29, 0x40e00000, v32
	v_mul_f32_e32 v32, 0xc01d265f, v29
	v_mul_f32_e32 v25, v28, v25
	v_add_f32_e32 v28, 1.0, v50
	v_rcp_f32_e32 v28, v28
	v_exp_f32_e32 v32, v32
	v_pk_fma_f32 v[30:31], v[52:53], s[16:17], v[12:13] op_sel_hi:[1,0,1]
	v_med3_f32 v27, v27, s47, v204
	v_min_f32_e32 v30, 0x40e00000, v30
	v_mul_f32_e32 v26, v26, v28
	v_add_f32_e32 v28, 1.0, v32
	v_mul_f32_e32 v32, 0xc01d265f, v30
	v_rcp_f32_e32 v28, v28
	v_exp_f32_e32 v32, v32
	v_add_f32_e32 v27, 1.0, v27
	v_mul_f32_e32 v26, v27, v26
	v_mul_f32_e32 v28, v29, v28
	v_add_f32_e32 v29, 1.0, v32
	v_rcp_f32_e32 v29, v29
	v_med3_f32 v27, v33, s47, v204
	v_add_f32_e32 v27, 1.0, v27
	v_mul_f32_e32 v28, v27, v28
	v_med3_f32 v27, v31, s47, v204
	v_mul_f32_e32 v29, v30, v29
	v_add_f32_e32 v27, 1.0, v27
	v_mov_b32_e32 v50, 0
	v_mul_f32_e32 v29, v27, v29
	v_cvt_pk_fp8_f32 v50, v25, v26
	v_pk_fma_f32 v[26:27], v[62:63], s[16:17], v[6:7] op_sel_hi:[1,0,1]
	v_pk_fma_f32 v[30:31], v[56:57], s[16:17], v[4:5] op_sel_hi:[1,0,1]
	v_min_f32_e32 v25, 0x40e00000, v26
	v_mul_f32_e32 v26, 0xc01d265f, v25
	v_exp_f32_e32 v26, v26
	v_cvt_pk_fp8_f32 v50, v28, v29 op_sel:[0,0,1]
	v_pk_fma_f32 v[28:29], v[64:65], s[16:17], v[8:9] op_sel_hi:[1,0,1]
	v_med3_f32 v27, v27, s47, v204
	v_min_f32_e32 v28, 0x40e00000, v28
	v_mul_f32_e32 v32, 0xc01d265f, v28
	v_add_f32_e32 v26, 1.0, v26
	v_rcp_f32_e32 v26, v26
	v_exp_f32_e32 v51, v32
	v_pk_fma_f32 v[32:33], v[54:55], s[16:17], v[2:3] op_sel_hi:[1,0,1]
	v_add_f32_e32 v27, 1.0, v27
; #define LAS __attribute__((address_space(3)))
; __device__ __forceinline__ unsigned pk4_fp8(float a, float b, float c, float d) { int w = 0; w = __builtin_amdgcn_cvt_pk_fp8_f32(a, b, w, false); w = __builtin_amdgcn_cvt_pk_fp8_f32(c, d, w, true); return (unsigned)w; }
;     __device__ __forceinline__ void operator()(const f32x4 (&acc)[2][2][4][2], const Unit& u, int wr, int wc, int fr, int fq) const {
;     ...
;                 for (int bj = 0; bj < 2; ++bj) { const f32x4 v0 = acc[ai][bj][m][0] * scale + bv[bj][0], v1 = acc[ai][bj][m][1] * scale + bv[bj][1];
;                     *(LAS unsigned*)(wp + m * (32 * STG8_PITCH) + 64 * bj) = pk4_fp8(swiglu1(v0[0], v0[1]), swiglu1(v0[2], v0[3]), swiglu1(v1[0], v1[1]), swiglu1(v1[2], v1[3])); }
;             asm volatile("s_waitcnt lgkmcnt(0)" ::: "memory"); __builtin_amdgcn_s_barrier(); asm volatile("" ::: "memory");
; #pragma unroll
;             for (int k2 = 0; k2 < 2; ++k2) { const int m = ms + 2 * k2;
;                 *(u32x4*)(gp + (size_t)(ai * HALF + m * 16) * ldc) = *(const LAS u32x4*)(rp + m * (32 * STG8_PITCH)); }
;             asm volatile("s_waitcnt lgkmcnt(0)" ::: "memory"); __builtin_amdgcn_s_barrier(); asm volatile("" ::: "memory");
;         }
	v_mul_f32_e32 v25, v25, v26
	v_add_f32_e32 v26, 1.0, v51
	v_rcp_f32_e32 v26, v26
	v_mul_f32_e32 v25, v27, v25
	v_med3_f32 v27, v29, s47, v204
	v_min_f32_e32 v30, 0x40e00000, v30
	v_mul_f32_e32 v26, v28, v26
	v_min_f32_e32 v28, 0x40e00000, v32
	v_mul_f32_e32 v29, 0xc01d265f, v28
	v_exp_f32_e32 v29, v29
	v_mul_f32_e32 v32, 0xc01d265f, v30
	v_exp_f32_e32 v32, v32
	v_add_f32_e32 v29, 1.0, v29
	v_rcp_f32_e32 v29, v29
	v_add_f32_e32 v27, 1.0, v27
	v_mul_f32_e32 v26, v27, v26
	v_med3_f32 v27, v33, s47, v204
	v_mul_f32_e32 v28, v28, v29
	v_add_f32_e32 v27, 1.0, v27
	v_mul_f32_e32 v27, v27, v28
	v_add_f32_e32 v28, 1.0, v32
	v_rcp_f32_e32 v28, v28
	v_med3_f32 v29, v31, s47, v204
	v_mov_b32_e32 v31, 0
	v_cvt_pk_fp8_f32 v31, v25, v26
	v_mul_f32_e32 v25, v30, v28
	v_add_f32_e32 v26, 1.0, v29
	v_pk_fma_f32 v[14:15], v[38:39], s[16:17], v[14:15] op_sel_hi:[1,0,1]
	v_mul_f32_e32 v25, v26, v25
	v_min_f32_e32 v14, 0x40e00000, v14
	v_cvt_pk_fp8_f32 v31, v27, v25 op_sel:[0,0,1]
	v_mul_f32_e32 v25, 0xc01d265f, v14
	v_exp_f32_e32 v25, v25
	v_pk_fma_f32 v[16:17], v[40:41], s[16:17], v[16:17] op_sel_hi:[1,0,1]
	v_pk_fma_f32 v[10:11], v[34:35], s[16:17], v[10:11] op_sel_hi:[1,0,1]
	v_min_f32_e32 v16, 0x40e00000, v16
	v_add_f32_e32 v25, 1.0, v25
	v_mul_f32_e32 v26, 0xc01d265f, v16
	v_rcp_f32_e32 v25, v25
	v_exp_f32_e32 v26, v26
	v_med3_f32 v15, v15, s47, v204
	v_min_f32_e32 v10, 0x40e00000, v10
	v_mul_f32_e32 v14, v14, v25
	v_add_f32_e32 v15, 1.0, v15
	v_mul_f32_e32 v25, 0xc01d265f, v10
	v_mul_f32_e32 v14, v15, v14
	v_add_f32_e32 v15, 1.0, v26
	v_rcp_f32_e32 v15, v15
	v_exp_f32_e32 v25, v25
	v_pk_fma_f32 v[12:13], v[36:37], s[16:17], v[12:13] op_sel_hi:[1,0,1]
	v_med3_f32 v17, v17, s47, v204
	v_min_f32_e32 v12, 0x40e00000, v12
	v_mul_f32_e32 v15, v16, v15
	v_add_f32_e32 v16, 1.0, v17
	v_add_f32_e32 v17, 1.0, v25
	v_mul_f32_e32 v25, 0xc01d265f, v12
	v_exp_f32_e32 v25, v25
	v_rcp_f32_e32 v17, v17
	v_mul_f32_e32 v15, v16, v15
	v_med3_f32 v11, v11, s47, v204
	v_add_f32_e32 v16, 1.0, v25
	v_rcp_f32_e32 v16, v16
	v_mul_f32_e32 v10, v10, v17
	v_add_f32_e32 v11, 1.0, v11
	v_pk_fma_f32 v[6:7], v[46:47], s[16:17], v[6:7] op_sel_hi:[1,0,1]
	v_mul_f32_e32 v10, v11, v10
	v_med3_f32 v11, v13, s47, v204
	v_min_f32_e32 v6, 0x40e00000, v6
	v_mul_f32_e32 v12, v12, v16
	v_add_f32_e32 v11, 1.0, v11
	v_mul_f32_e32 v13, 0xc01d265f, v6
	v_mul_f32_e32 v11, v11, v12
	v_mov_b32_e32 v12, 0
	v_cvt_pk_fp8_f32 v12, v14, v15
	v_exp_f32_e32 v13, v13
	v_pk_fma_f32 v[8:9], v[48:49], s[16:17], v[8:9] op_sel_hi:[1,0,1]
	v_pk_fma_f32 v[2:3], v[42:43], s[16:17], v[2:3] op_sel_hi:[1,0,1]
	v_min_f32_e32 v8, 0x40e00000, v8
	v_cvt_pk_fp8_f32 v12, v10, v11 op_sel:[0,0,1]
	v_add_f32_e32 v10, 1.0, v13
	v_mul_f32_e32 v11, 0xc01d265f, v8
	v_rcp_f32_e32 v10, v10
	v_exp_f32_e32 v11, v11
	v_med3_f32 v7, v7, s47, v204
	v_mul_f32_e32 v6, v6, v10
	v_add_f32_e32 v7, 1.0, v7
	v_min_f32_e32 v2, 0x40e00000, v2
	v_add_f32_e32 v10, 1.0, v11
	v_mul_f32_e32 v6, v7, v6
	v_med3_f32 v7, v9, s47, v204
	v_mul_f32_e32 v9, 0xc01d265f, v2
	v_rcp_f32_e32 v10, v10
	v_exp_f32_e32 v9, v9
	v_pk_fma_f32 v[4:5], v[44:45], s[16:17], v[4:5] op_sel_hi:[1,0,1]
	v_mul_f32_e32 v8, v8, v10
	v_add_f32_e32 v7, 1.0, v7
	v_min_f32_e32 v4, 0x40e00000, v4
	v_mul_f32_e32 v7, v7, v8
	v_add_f32_e32 v8, 1.0, v9
	v_mul_f32_e32 v9, 0xc01d265f, v4
	v_rcp_f32_e32 v8, v8
	v_exp_f32_e32 v9, v9
	v_med3_f32 v3, v3, s47, v204
	v_mul_f32_e32 v2, v2, v8
	v_add_f32_e32 v3, 1.0, v3
	v_mul_f32_e32 v2, v3, v2
	v_add_f32_e32 v3, 1.0, v9
	v_rcp_f32_e32 v3, v3
	v_mov_b32_e32 v8, 0
	v_cvt_pk_fp8_f32 v8, v6, v7
	v_med3_f32 v5, v5, s47, v204
	v_mul_f32_e32 v3, v4, v3
	v_add_f32_e32 v4, 1.0, v5
	v_mul_f32_e32 v3, v4, v3
	v_cvt_pk_fp8_f32 v8, v2, v3 op_sel:[0,0,1]
	s_waitcnt lgkmcnt(0)
	s_barrier
	ds_write2_b32 v202, v90, v82 offset1:16
	ds_write2_b32 v22, v74, v66 offset0:128 offset1:144
	ds_write2_b32 v23, v50, v31 offset1:16
	ds_write2_b32 v24, v12, v8 offset0:128 offset1:144
	s_waitcnt lgkmcnt(0)
	s_barrier
	ds_read_b128 v[2:5], v203
	ds_read_b128 v[6:9], v203 offset:9216
	v_add_co_u32_e32 v10, vcc, s48, v20
	s_nop 1
	v_addc_co_u32_e32 v11, vcc, 0, v21, vcc
	s_waitcnt lgkmcnt(1)
	global_store_dwordx4 v[10:11], v[2:5], off sc1
	s_nop 1
	v_add_co_u32_e32 v2, vcc, 0x40000, v18
	s_nop 1
	v_addc_co_u32_e32 v3, vcc, 0, v19, vcc
	s_waitcnt lgkmcnt(0)
	global_store_dwordx4 v[2:3], v[6:9], off sc1
	s_waitcnt lgkmcnt(0)
	s_barrier
	s_cbranch_scc1 .LBB0_993
	s_andn2_b64 vcc, exec, s[6:7]
	s_cbranch_vccnz .LBB0_992
	s_barrier
	s_branch .LBB0_992

; #define LAS __attribute__((address_space(3)))
; __device__ __forceinline__ unsigned pk4_fp8(float a, float b, float c, float d) { int w = 0; w = __builtin_amdgcn_cvt_pk_fp8_f32(a, b, w, false); w = __builtin_amdgcn_cvt_pk_fp8_f32(c, d, w, true); return (unsigned)w; }
;     __device__ __forceinline__ void operator()(const f32x4 (&acc)[2][2][4][2], const Unit& u, int wr, int wc, int fr, int fq) const {
;         const int e = u.pn / npn, pnl = u.pn - e * npn; const int tid = threadIdx.x;
;         const int col0 = pnl * BM + wc * 32 + 8 * fq;
;         f32x4 bv[2][2];
; #pragma unroll
;         for (int bj = 0; bj < 2; ++bj)
; #pragma unroll
;             for (int n = 0; n < 2; ++n) bv[bj][n] = *(const f32x4*)(bias + (size_t)e * bias_ld + col0 + bj * HALF + 4 * n);
;         constexpr int PITCH = 272, SLAB = 32 * PITCH;
;         LAS unsigned char* wp = stg + (16 * wr + fr) * PITCH + 32 * wc + 8 * fq;
;         const int rr = tid >> 4, cc = tid & 15; const LAS unsigned char* rp = stg + rr * PITCH + cc * 16;
;         unsigned char* gp = O + (size_t)(u.pm * BM + 64 * (rr >> 4) + (rr & 15)) * ldc + pnl * BM + cc * 16;
; #pragma unroll
;         for (int ai = 0; ai < 2; ++ai)
; #pragma unroll
;             for (int mp = 0; mp < 2; ++mp) {
; #pragma unroll
;                 for (int ms = 0; ms < 2; ++ms)
; #pragma unroll
;                     for (int bj = 0; bj < 2; ++bj) { const int m = 2 * mp + ms; const f32x4 v0 = acc[ai][bj][m][0] * scale + bv[bj][0], v1 = acc[ai][bj][m][1] * scale + bv[bj][1];
;                         u32x2 w; w.x = pk4_fp8(v0[0], v0[1], v0[2], v0[3]); w.y = pk4_fp8(v1[0], v1[1], v1[2], v1[3]);
;                         *(LAS u32x2*)(wp + ms * SLAB + 128 * bj) = w; }
;                 asm volatile("s_waitcnt lgkmcnt(0)" ::: "memory"); __builtin_amdgcn_s_barrier(); asm volatile("" ::: "memory");
; #pragma unroll
;                 for (int ms = 0; ms < 2; ++ms) *(u32x4*)(gp + (size_t)(ai * HALF + (2 * mp + ms) * 16) * ldc) = *(const LAS u32x4*)(rp + ms * SLAB);
.LBB0_1150:
	s_ashr_i32 s2, s21, 31
	s_lshr_b32 s2, s2, 29
	s_add_i32 s2, s21, s2
	s_ashr_i32 s2, s2, 3
	s_lshl_b32 s3, s2, 11
	s_lshl_b32 s21, s21, 8
	v_readlane_b32 s56, v254, 0
	s_sub_i32 s22, s21, s3
	s_ashr_i32 s3, s2, 31
	v_readlane_b32 s60, v254, 4
	v_readlane_b32 s61, v254, 5
	s_lshl_b64 s[2:3], s[2:3], 13
	v_readlane_b32 s62, v254, 6
	v_readlane_b32 s63, v254, 7
	s_mov_b64 s[24:25], s[60:61]
	v_or_b32_e32 v2, s22, v186
	s_add_u32 s2, s24, s2
	s_addc_u32 s3, s25, s3
	v_ashrrev_i32_e32 v3, 31, v2
	s_nop 15
	s_nop 15
	v_lshl_add_u64 v[2:3], v[2:3], 2, s[2:3]
	global_load_dwordx4 v[14:17], v[2:3], off
	global_load_dwordx4 v[10:13], v[2:3], off offset:16
	global_load_dwordx4 v[6:9], v[2:3], off offset:512
	s_nop 0
	global_load_dwordx4 v[2:5], v[2:3], off offset:528
	v_mov_b32_e32 v20, 0
	v_mov_b32_e32 v21, 0
	v_mov_b32_e32 v22, 0
	v_mov_b32_e32 v23, 0
	v_mov_b32_e32 v24, 0
	v_mov_b32_e32 v25, 0
	v_mov_b32_e32 v26, 0
	v_mov_b32_e32 v27, 0
	v_lshl_or_b32 v18, s20, 8, v187
	v_add_u32_e32 v178, 0x2000, v188
	v_ashrrev_i32_e32 v19, 31, v18
	v_lshlrev_b64 v[18:19], 11, v[18:19]
	v_mov_b32_e32 v32, 0
	v_mov_b32_e32 v33, 0
	v_lshl_add_u64 v[18:19], s[4:5], 0, v[18:19]
	s_ashr_i32 s23, s22, 31
	v_lshl_add_u64 v[18:19], v[18:19], 0, s[22:23]
	v_lshl_add_u64 v[18:19], v[18:19], 0, v[170:171]
	v_add_co_u32_e32 v176, vcc, s50, v18
	v_mov_b32_e32 v28, 0
	v_mov_b32_e32 v29, 0
	v_mov_b32_e32 v30, 0
	v_mov_b32_e32 v31, 0
	v_addc_co_u32_e32 v177, vcc, 0, v19, vcc
	s_cmp_eq_u32 s49, s48
	s_mov_b64 s[2:3], -1
	v_readlane_b32 s57, v254, 1
	v_readlane_b32 s58, v254, 2
	v_readlane_b32 s59, v254, 3
	s_mov_b64 s[26:27], s[62:63]
	s_waitcnt vmcnt(0)
	v_pk_fma_f32 v[158:159], v[158:159], s[12:13], v[14:15] op_sel_hi:[1,0,1]
	v_pk_fma_f32 v[154:155], v[154:155], s[12:13], v[10:11] op_sel_hi:[1,0,1]
	v_pk_fma_f32 v[138:139], v[138:139], s[12:13], v[6:7] op_sel_hi:[1,0,1]
	v_pk_fma_f32 v[130:131], v[130:131], s[12:13], v[2:3] op_sel_hi:[1,0,1]
	v_pk_fma_f32 v[150:151], v[150:151], s[12:13], v[14:15] op_sel_hi:[1,0,1]
	v_pk_fma_f32 v[146:147], v[146:147], s[12:13], v[10:11] op_sel_hi:[1,0,1]
	v_pk_fma_f32 v[126:127], v[126:127], s[12:13], v[6:7] op_sel_hi:[1,0,1]
	v_pk_fma_f32 v[122:123], v[122:123], s[12:13], v[2:3] op_sel_hi:[1,0,1]
	v_cvt_pk_fp8_f32 v20, v158, v159
	v_cvt_pk_fp8_f32 v21, v154, v155
	v_cvt_pk_fp8_f32 v22, v138, v139
	v_cvt_pk_fp8_f32 v23, v130, v131
	v_cvt_pk_fp8_f32 v24, v150, v151
	v_cvt_pk_fp8_f32 v25, v146, v147
	v_cvt_pk_fp8_f32 v26, v126, v127
	v_cvt_pk_fp8_f32 v27, v122, v123
	v_pk_fma_f32 v[160:161], v[160:161], s[12:13], v[16:17] op_sel_hi:[1,0,1]
	v_pk_fma_f32 v[156:157], v[156:157], s[12:13], v[12:13] op_sel_hi:[1,0,1]
	v_pk_fma_f32 v[140:141], v[140:141], s[12:13], v[8:9] op_sel_hi:[1,0,1]
	v_pk_fma_f32 v[132:133], v[132:133], s[12:13], v[4:5] op_sel_hi:[1,0,1]
	v_pk_fma_f32 v[152:153], v[152:153], s[12:13], v[16:17] op_sel_hi:[1,0,1]
	v_pk_fma_f32 v[148:149], v[148:149], s[12:13], v[12:13] op_sel_hi:[1,0,1]
	v_pk_fma_f32 v[128:129], v[128:129], s[12:13], v[8:9] op_sel_hi:[1,0,1]
	v_pk_fma_f32 v[124:125], v[124:125], s[12:13], v[4:5] op_sel_hi:[1,0,1]
	v_cvt_pk_fp8_f32 v20, v160, v161 op_sel:[0,0,1]
	v_cvt_pk_fp8_f32 v21, v156, v157 op_sel:[0,0,1]
	v_cvt_pk_fp8_f32 v22, v140, v141 op_sel:[0,0,1]
	v_cvt_pk_fp8_f32 v23, v132, v133 op_sel:[0,0,1]
	v_cvt_pk_fp8_f32 v24, v152, v153 op_sel:[0,0,1]
	v_cvt_pk_fp8_f32 v25, v148, v149 op_sel:[0,0,1]
	v_cvt_pk_fp8_f32 v26, v128, v129 op_sel:[0,0,1]
	v_cvt_pk_fp8_f32 v27, v124, v125 op_sel:[0,0,1]
	ds_write2_b64 v188, v[20:21], v[22:23] offset1:16
	ds_write2_b64 v178, v[24:25], v[26:27] offset0:64 offset1:80
	s_waitcnt lgkmcnt(0)
	s_barrier
	ds_read_b128 v[20:23], v189
	ds_read_b128 v[24:27], v189 offset:8704
	v_pk_fma_f32 v[110:111], v[110:111], s[12:13], v[14:15] op_sel_hi:[1,0,1]
	v_pk_fma_f32 v[106:107], v[106:107], s[12:13], v[10:11] op_sel_hi:[1,0,1]
	v_cvt_pk_fp8_f32 v32, v110, v111
	v_cvt_pk_fp8_f32 v33, v106, v107
	v_pk_fma_f32 v[142:143], v[142:143], s[12:13], v[14:15] op_sel_hi:[1,0,1]
	v_pk_fma_f32 v[134:135], v[134:135], s[12:13], v[10:11] op_sel_hi:[1,0,1]
	v_pk_fma_f32 v[118:119], v[118:119], s[12:13], v[6:7] op_sel_hi:[1,0,1]
	v_pk_fma_f32 v[114:115], v[114:115], s[12:13], v[2:3] op_sel_hi:[1,0,1]
	s_waitcnt lgkmcnt(1)
	global_store_dwordx4 v[18:19], v[20:23], off sc1
	s_waitcnt lgkmcnt(0)
	global_store_dwordx4 v[176:177], v[24:27], off sc1
	v_cvt_pk_fp8_f32 v28, v142, v143
	v_pk_fma_f32 v[20:21], v[112:113], s[12:13], v[16:17] op_sel_hi:[1,0,1]
	v_pk_fma_f32 v[22:23], v[108:109], s[12:13], v[12:13] op_sel_hi:[1,0,1]
	v_cvt_pk_fp8_f32 v29, v134, v135
	v_cvt_pk_fp8_f32 v30, v118, v119
	v_cvt_pk_fp8_f32 v31, v114, v115
	v_cvt_pk_fp8_f32 v32, v20, v21 op_sel:[0,0,1]
	v_cvt_pk_fp8_f32 v33, v22, v23 op_sel:[0,0,1]
	v_pk_fma_f32 v[20:21], v[102:103], s[12:13], v[6:7] op_sel_hi:[1,0,1]
	v_pk_fma_f32 v[22:23], v[98:99], s[12:13], v[2:3] op_sel_hi:[1,0,1]
	v_mov_b32_e32 v24, 0
	v_mov_b32_e32 v25, 0
	v_cvt_pk_fp8_f32 v24, v20, v21
	v_cvt_pk_fp8_f32 v25, v22, v23
	v_pk_fma_f32 v[144:145], v[144:145], s[12:13], v[16:17] op_sel_hi:[1,0,1]
	v_pk_fma_f32 v[136:137], v[136:137], s[12:13], v[12:13] op_sel_hi:[1,0,1]
	v_pk_fma_f32 v[120:121], v[120:121], s[12:13], v[8:9] op_sel_hi:[1,0,1]
	v_pk_fma_f32 v[116:117], v[116:117], s[12:13], v[4:5] op_sel_hi:[1,0,1]
	v_cvt_pk_fp8_f32 v28, v144, v145 op_sel:[0,0,1]
	v_cvt_pk_fp8_f32 v29, v136, v137 op_sel:[0,0,1]
	v_cvt_pk_fp8_f32 v30, v120, v121 op_sel:[0,0,1]
	v_cvt_pk_fp8_f32 v31, v116, v117 op_sel:[0,0,1]
	v_pk_fma_f32 v[20:21], v[104:105], s[12:13], v[8:9] op_sel_hi:[1,0,1]
	v_pk_fma_f32 v[22:23], v[100:101], s[12:13], v[4:5] op_sel_hi:[1,0,1]
	v_cvt_pk_fp8_f32 v24, v20, v21 op_sel:[0,0,1]
	v_cvt_pk_fp8_f32 v25, v22, v23 op_sel:[0,0,1]
	s_waitcnt lgkmcnt(0)
	s_barrier
; #define LAS __attribute__((address_space(3)))
; __device__ __forceinline__ unsigned pk4_fp8(float a, float b, float c, float d) { int w = 0; w = __builtin_amdgcn_cvt_pk_fp8_f32(a, b, w, false); w = __builtin_amdgcn_cvt_pk_fp8_f32(c, d, w, true); return (unsigned)w; }
;     __device__ __forceinline__ void operator()(const f32x4 (&acc)[2][2][4][2], const Unit& u, int wr, int wc, int fr, int fq) const {
;     ...
;                     for (int bj = 0; bj < 2; ++bj) { const int m = 2 * mp + ms; const f32x4 v0 = acc[ai][bj][m][0] * scale + bv[bj][0], v1 = acc[ai][bj][m][1] * scale + bv[bj][1];
;                         u32x2 w; w.x = pk4_fp8(v0[0], v0[1], v0[2], v0[3]); w.y = pk4_fp8(v1[0], v1[1], v1[2], v1[3]);
;                         *(LAS u32x2*)(wp + ms * SLAB + 128 * bj) = w; }
;                 asm volatile("s_waitcnt lgkmcnt(0)" ::: "memory"); __builtin_amdgcn_s_barrier(); asm volatile("" ::: "memory");
; #pragma unroll
;                 for (int ms = 0; ms < 2; ++ms) *(u32x4*)(gp + (size_t)(ai * HALF + (2 * mp + ms) * 16) * ldc) = *(const LAS u32x4*)(rp + ms * SLAB);
;                 asm volatile("s_waitcnt lgkmcnt(0)" ::: "memory"); __builtin_amdgcn_s_barrier(); asm volatile("" ::: "memory");
;             }
	ds_write2_b64 v188, v[28:29], v[30:31] offset1:16
	ds_write2_b64 v178, v[32:33], v[24:25] offset0:64 offset1:80
	s_waitcnt lgkmcnt(0)
	s_barrier
	ds_read_b128 v[20:23], v189
	ds_read_b128 v[24:27], v189 offset:8704
	v_add_co_u32_e32 v28, vcc, s51, v18
	v_mov_b32_e32 v30, 0
	s_nop 0
	v_addc_co_u32_e32 v29, vcc, 0, v19, vcc
	s_waitcnt lgkmcnt(1)
	global_store_dwordx4 v[28:29], v[20:23], off sc1
	v_mov_b32_e32 v28, 0
	v_mov_b32_e32 v29, 0
	v_add_co_u32_e32 v20, vcc, s47, v18
	v_pk_fma_f32 v[22:23], v[90:91], s[12:13], v[10:11] op_sel_hi:[1,0,1]
	s_nop 0
	v_addc_co_u32_e32 v21, vcc, 0, v19, vcc
	s_waitcnt lgkmcnt(0)
	global_store_dwordx4 v[20:21], v[24:27], off sc1
	v_pk_fma_f32 v[20:21], v[94:95], s[12:13], v[14:15] op_sel_hi:[1,0,1]
	v_mov_b32_e32 v31, 0
	v_mov_b32_e32 v24, 0
	v_mov_b32_e32 v25, 0
	v_cvt_pk_fp8_f32 v24, v20, v21
	v_cvt_pk_fp8_f32 v25, v22, v23
	v_pk_fma_f32 v[20:21], v[96:97], s[12:13], v[16:17] op_sel_hi:[1,0,1]
	v_pk_fma_f32 v[22:23], v[92:93], s[12:13], v[12:13] op_sel_hi:[1,0,1]
	v_cvt_pk_fp8_f32 v24, v20, v21 op_sel:[0,0,1]
	v_cvt_pk_fp8_f32 v25, v22, v23 op_sel:[0,0,1]
	v_pk_fma_f32 v[20:21], v[82:83], s[12:13], v[6:7] op_sel_hi:[1,0,1]
	v_pk_fma_f32 v[22:23], v[74:75], s[12:13], v[2:3] op_sel_hi:[1,0,1]
	v_mov_b32_e32 v26, 0
	v_mov_b32_e32 v27, 0
	v_cvt_pk_fp8_f32 v26, v20, v21
	v_cvt_pk_fp8_f32 v27, v22, v23
	v_pk_fma_f32 v[20:21], v[84:85], s[12:13], v[8:9] op_sel_hi:[1,0,1]
	v_pk_fma_f32 v[22:23], v[76:77], s[12:13], v[4:5] op_sel_hi:[1,0,1]
	v_cvt_pk_fp8_f32 v26, v20, v21 op_sel:[0,0,1]
	v_cvt_pk_fp8_f32 v27, v22, v23 op_sel:[0,0,1]
	v_pk_fma_f32 v[20:21], v[86:87], s[12:13], v[14:15] op_sel_hi:[1,0,1]
	v_pk_fma_f32 v[22:23], v[78:79], s[12:13], v[10:11] op_sel_hi:[1,0,1]
	v_cvt_pk_fp8_f32 v28, v20, v21
	v_cvt_pk_fp8_f32 v29, v22, v23
	v_pk_fma_f32 v[20:21], v[88:89], s[12:13], v[16:17] op_sel_hi:[1,0,1]
	v_pk_fma_f32 v[22:23], v[80:81], s[12:13], v[12:13] op_sel_hi:[1,0,1]
	v_cvt_pk_fp8_f32 v28, v20, v21 op_sel:[0,0,1]
	v_cvt_pk_fp8_f32 v29, v22, v23 op_sel:[0,0,1]
	v_pk_fma_f32 v[20:21], v[70:71], s[12:13], v[6:7] op_sel_hi:[1,0,1]
	v_pk_fma_f32 v[22:23], v[66:67], s[12:13], v[2:3] op_sel_hi:[1,0,1]
	v_cvt_pk_fp8_f32 v30, v20, v21
	v_cvt_pk_fp8_f32 v31, v22, v23
	v_pk_fma_f32 v[20:21], v[72:73], s[12:13], v[8:9] op_sel_hi:[1,0,1]
	v_pk_fma_f32 v[22:23], v[68:69], s[12:13], v[4:5] op_sel_hi:[1,0,1]
	v_cvt_pk_fp8_f32 v30, v20, v21 op_sel:[0,0,1]
	v_cvt_pk_fp8_f32 v31, v22, v23 op_sel:[0,0,1]
	s_waitcnt lgkmcnt(0)
	s_barrier
	ds_write2_b64 v188, v[24:25], v[26:27] offset1:16
	ds_write2_b64 v178, v[28:29], v[30:31] offset0:64 offset1:80
	s_waitcnt lgkmcnt(0)
	s_barrier
	ds_read_b128 v[20:23], v189
	ds_read_b128 v[24:27], v189 offset:8704
	v_add_co_u32_e32 v28, vcc, s52, v18
	s_nop 1
	v_addc_co_u32_e32 v29, vcc, 0, v19, vcc
	s_waitcnt lgkmcnt(1)
	global_store_dwordx4 v[28:29], v[20:23], off sc1
	s_nop 1
	v_add_co_u32_e32 v20, vcc, s53, v18
	v_pk_fma_f32 v[22:23], v[58:59], s[12:13], v[10:11] op_sel_hi:[1,0,1]
	s_nop 0
	v_addc_co_u32_e32 v21, vcc, 0, v19, vcc
	s_waitcnt lgkmcnt(0)
	global_store_dwordx4 v[20:21], v[24:27], off sc1
	v_pk_fma_f32 v[20:21], v[62:63], s[12:13], v[14:15] op_sel_hi:[1,0,1]
	v_pk_fma_f32 v[14:15], v[54:55], s[12:13], v[14:15] op_sel_hi:[1,0,1]
	v_mov_b32_e32 v24, 0
	v_cvt_pk_fp8_f32 v24, v20, v21
	v_pk_fma_f32 v[20:21], v[64:65], s[12:13], v[16:17] op_sel_hi:[1,0,1]
	v_mov_b32_e32 v26, 0
	v_mov_b32_e32 v25, 0
	v_cvt_pk_fp8_f32 v24, v20, v21 op_sel:[0,0,1]
	v_pk_fma_f32 v[20:21], v[50:51], s[12:13], v[6:7] op_sel_hi:[1,0,1]
	v_cvt_pk_fp8_f32 v25, v22, v23
	v_cvt_pk_fp8_f32 v26, v20, v21
	v_pk_fma_f32 v[20:21], v[52:53], s[12:13], v[8:9] op_sel_hi:[1,0,1]
	v_pk_fma_f32 v[22:23], v[60:61], s[12:13], v[12:13] op_sel_hi:[1,0,1]
	v_pk_fma_f32 v[10:11], v[46:47], s[12:13], v[10:11] op_sel_hi:[1,0,1]
	v_cvt_pk_fp8_f32 v26, v20, v21 op_sel:[0,0,1]
	v_mov_b32_e32 v20, 0
	v_cvt_pk_fp8_f32 v20, v14, v15
	v_mov_b32_e32 v21, 0
	v_cvt_pk_fp8_f32 v25, v22, v23 op_sel:[0,0,1]
	v_pk_fma_f32 v[22:23], v[42:43], s[12:13], v[2:3] op_sel_hi:[1,0,1]
	v_mov_b32_e32 v27, 0
	v_cvt_pk_fp8_f32 v21, v10, v11
	v_pk_fma_f32 v[10:11], v[56:57], s[12:13], v[16:17] op_sel_hi:[1,0,1]
	v_cvt_pk_fp8_f32 v27, v22, v23
	v_cvt_pk_fp8_f32 v20, v10, v11 op_sel:[0,0,1]
	v_pk_fma_f32 v[6:7], v[38:39], s[12:13], v[6:7] op_sel_hi:[1,0,1]
	v_pk_fma_f32 v[2:3], v[34:35], s[12:13], v[2:3] op_sel_hi:[1,0,1]
	v_mov_b32_e32 v10, 0
	v_mov_b32_e32 v11, 0
	v_cvt_pk_fp8_f32 v10, v6, v7
	v_cvt_pk_fp8_f32 v11, v2, v3
	v_pk_fma_f32 v[22:23], v[44:45], s[12:13], v[4:5] op_sel_hi:[1,0,1]
	v_pk_fma_f32 v[12:13], v[48:49], s[12:13], v[12:13] op_sel_hi:[1,0,1]
	v_cvt_pk_fp8_f32 v27, v22, v23 op_sel:[0,0,1]
	v_pk_fma_f32 v[2:3], v[40:41], s[12:13], v[8:9] op_sel_hi:[1,0,1]
	v_pk_fma_f32 v[4:5], v[36:37], s[12:13], v[4:5] op_sel_hi:[1,0,1]
	v_cvt_pk_fp8_f32 v21, v12, v13 op_sel:[0,0,1]
	v_cvt_pk_fp8_f32 v10, v2, v3 op_sel:[0,0,1]
	v_cvt_pk_fp8_f32 v11, v4, v5 op_sel:[0,0,1]
	s_waitcnt lgkmcnt(0)
	s_barrier
	ds_write2_b64 v188, v[24:25], v[26:27] offset1:16
	ds_write2_b64 v178, v[20:21], v[10:11] offset0:64 offset1:80
	s_waitcnt lgkmcnt(0)
	s_barrier
	ds_read_b128 v[2:5], v189
	ds_read_b128 v[6:9], v189 offset:8704
	v_add_co_u32_e32 v10, vcc, 0x50000, v18
	s_nop 1
	v_addc_co_u32_e32 v11, vcc, 0, v19, vcc
	s_waitcnt lgkmcnt(1)
	global_store_dwordx4 v[10:11], v[2:5], off sc1
	s_nop 1
	v_add_co_u32_e32 v2, vcc, 0x58000, v18
	s_nop 1
	v_addc_co_u32_e32 v3, vcc, 0, v19, vcc
	s_waitcnt lgkmcnt(0)
	global_store_dwordx4 v[2:3], v[6:9], off sc1
	s_waitcnt lgkmcnt(0)
	s_barrier
	s_cbranch_scc1 .LBB0_1143
	s_andn2_b64 vcc, exec, s[0:1]
	s_cbranch_vccnz .LBB0_1142
	s_barrier
	s_branch .LBB0_1142
